# speedup vs baseline: 1.0004x; 1.0004x over previous
.LBB6_32:
	s_or_b64 exec, exec, s[2:3]
	s_add_i32 s0, 0, 0x18000
	v_add_u32_e32 v48, s0, v39
	s_mov_b64 s[0:1], 0x80
	v_readfirstlane_b32 s22, v48
	v_add_u32_e32 v49, 0x2000, v48
	v_lshl_add_u64 v[2:3], v[30:31], 0, s[0:1]
	s_mov_b32 m0, s22
	v_readfirstlane_b32 s21, v49
	v_add_u32_e32 v46, 0x8000, v35
	s_waitcnt vmcnt(4)
	s_barrier
	global_load_lds_dwordx4 v[2:3], off
	v_lshl_add_u64 v[2:3], v[32:33], 0, s[0:1]
	s_mov_b32 m0, s21
	v_readfirstlane_b32 s19, v46
	v_add_u32_e32 v47, 0xa000, v35
	s_add_i32 s2, 0, 0x1c000
	global_load_lds_dwordx4 v[2:3], off
	v_lshl_add_u64 v[2:3], v[26:27], 0, s[0:1]
	s_mov_b32 m0, s19
	v_readfirstlane_b32 s17, v47
	v_add_u32_e32 v38, s2, v39
	global_load_lds_dwordx4 v[2:3], off
	v_lshl_add_u64 v[2:3], v[28:29], 0, s[0:1]
	s_mov_b32 m0, s17
	v_readfirstlane_b32 s4, v38
	v_add_u32_e32 v40, 0x2000, v38
	global_load_lds_dwordx4 v[2:3], off
	v_lshl_add_u64 v[2:3], v[22:23], 0, s[0:1]
	s_mov_b32 m0, s4
	v_readfirstlane_b32 s3, v40
	global_load_lds_dwordx4 v[2:3], off
	v_lshl_add_u64 v[2:3], v[24:25], 0, s[0:1]
	s_mov_b32 m0, s3
	v_and_b32_e32 v4, 48, v0
	global_load_lds_dwordx4 v[2:3], off
	v_lshlrev_b32_e32 v2, 6, v0
	v_and_b32_e32 v3, 0x3c0, v2
	v_and_b32_e32 v5, 32, v103
	v_bitop3_b32 v6, v3, v5, v4 bitop3:0x36
	v_and_b32_e32 v2, 0x3000, v2
	v_add3_u32 v234, 0, v2, v6
	v_add_u32_e32 v2, 0x10000, v234
	v_add_u32_e32 v4, 0x10800, v234
	s_waitcnt vmcnt(6)
	s_barrier
	v_add_u32_e32 v3, 0x10400, v234
	ds_read_b128 v[10:13], v2
	ds_read_b128 v[14:17], v3
	v_add_u32_e32 v5, 0x10c00, v234
	ds_read_b128 v[50:53], v4
	ds_read_b128 v[54:57], v5
	v_and_b32_e32 v1, 0x2000, v1
	v_add3_u32 v1, 0, v1, v6
	v_add_u32_e32 v37, 0xc000, v35
	v_add_u32_e32 v39, 0xe000, v35
	v_readfirstlane_b32 s7, v37
	v_lshl_add_u64 v[6:7], v[18:19], 0, s[0:1]
	s_mov_b32 m0, s7
	v_readfirstlane_b32 s2, v39
	global_load_lds_dwordx4 v[6:7], off
	v_lshl_add_u64 v[6:7], v[20:21], 0, s[0:1]
	s_mov_b32 m0, s2
	s_nop 0
	global_load_lds_dwordx4 v[6:7], off
	ds_read_b128 v[42:45], v1
	ds_read_b128 v[58:61], v1 offset:1024
	ds_read_b128 v[62:65], v1 offset:2048
	ds_read_b128 v[66:69], v1 offset:3072
	ds_read_b128 v[70:73], v1 offset:4096
	ds_read_b128 v[74:77], v1 offset:5120
	ds_read_b128 v[78:81], v1 offset:6144
	ds_read_b128 v[82:85], v1 offset:7168
	s_waitcnt lgkmcnt(8)
	s_barrier
	s_waitcnt lgkmcnt(0)
	s_setprio 1
	s_waitcnt lgkmcnt(0)
	v_mfma_f32_16x16x32_f16 v[6:9], v[10:13], v[42:45], 0
	v_mfma_f32_16x16x32_f16 v[86:89], v[14:17], v[58:61], v[6:9]
	v_mfma_f32_16x16x32_f16 v[6:9], v[50:53], v[42:45], 0
	v_mfma_f32_16x16x32_f16 v[90:93], v[54:57], v[58:61], v[6:9]
	v_mfma_f32_16x16x32_f16 v[6:9], v[10:13], v[62:65], 0
	v_mfma_f32_16x16x32_f16 v[94:97], v[14:17], v[66:69], v[6:9]
	v_mfma_f32_16x16x32_f16 v[6:9], v[50:53], v[62:65], 0
	v_mfma_f32_16x16x32_f16 v[98:101], v[54:57], v[66:69], v[6:9]
	v_mfma_f32_16x16x32_f16 v[6:9], v[10:13], v[70:73], 0
	v_mfma_f32_16x16x32_f16 v[102:105], v[14:17], v[74:77], v[6:9]
	v_mfma_f32_16x16x32_f16 v[6:9], v[50:53], v[70:73], 0
	v_mfma_f32_16x16x32_f16 v[106:109], v[54:57], v[74:77], v[6:9]
	v_mfma_f32_16x16x32_f16 v[6:9], v[10:13], v[78:81], 0
	v_mfma_f32_16x16x32_f16 v[110:113], v[14:17], v[82:85], v[6:9]
	v_mfma_f32_16x16x32_f16 v[6:9], v[50:53], v[78:81], 0
	v_mfma_f32_16x16x32_f16 v[114:117], v[54:57], v[82:85], v[6:9]
	s_setprio 0
	s_barrier
	s_mov_b64 s[0:1], 0x100
	v_readfirstlane_b32 s15, v36
	v_add_u32_e32 v41, 0x2000, v36
	s_nop 1
	v_add_u32_e32 v6, 0x14000, v234
	v_add_u32_e32 v8, 0x14800, v234
	v_lshl_add_u64 v[134:135], v[30:31], 0, s[0:1]
	s_mov_b32 m0, s15
	v_readfirstlane_b32 s5, v41
	v_add_u32_e32 v7, 0x14400, v234
	ds_read_b128 v[118:121], v6
	ds_read_b128 v[122:125], v7
	v_add_u32_e32 v9, 0x14c00, v234
	ds_read_b128 v[126:129], v8
	ds_read_b128 v[130:133], v9
	global_load_lds_dwordx4 v[134:135], off
	v_lshl_add_u64 v[134:135], v[32:33], 0, s[0:1]
	s_mov_b32 m0, s5
	s_nop 0
	global_load_lds_dwordx4 v[134:135], off
	s_barrier
	s_waitcnt lgkmcnt(0)
	s_setprio 1
	s_waitcnt lgkmcnt(0)
	v_mfma_f32_16x16x32_f16 v[134:137], v[118:121], v[42:45], 0
	v_mfma_f32_16x16x32_f16 v[42:45], v[126:129], v[42:45], 0
	v_mfma_f32_16x16x32_f16 v[134:137], v[122:125], v[58:61], v[134:137]
	v_mfma_f32_16x16x32_f16 v[58:61], v[130:133], v[58:61], v[42:45]
	v_mfma_f32_16x16x32_f16 v[42:45], v[118:121], v[62:65], 0
	v_mfma_f32_16x16x32_f16 v[138:141], v[122:125], v[66:69], v[42:45]
	v_mfma_f32_16x16x32_f16 v[42:45], v[126:129], v[62:65], 0
	v_mfma_f32_16x16x32_f16 v[62:65], v[130:133], v[66:69], v[42:45]
	v_mfma_f32_16x16x32_f16 v[42:45], v[118:121], v[70:73], 0
	v_mfma_f32_16x16x32_f16 v[66:69], v[122:125], v[74:77], v[42:45]
	v_mfma_f32_16x16x32_f16 v[42:45], v[126:129], v[70:73], 0
	v_mfma_f32_16x16x32_f16 v[70:73], v[130:133], v[74:77], v[42:45]
	v_mfma_f32_16x16x32_f16 v[42:45], v[118:121], v[78:81], 0
	v_mfma_f32_16x16x32_f16 v[74:77], v[122:125], v[82:85], v[42:45]
	v_mfma_f32_16x16x32_f16 v[42:45], v[126:129], v[78:81], 0
	v_mfma_f32_16x16x32_f16 v[78:81], v[130:133], v[82:85], v[42:45]
	s_setprio 0
	v_readfirstlane_b32 s16, v35
	s_nop 4
	v_lshl_add_u64 v[42:43], v[26:27], 0, s[0:1]
	s_mov_b32 m0, s16
	s_barrier
	ds_read_b128 v[82:85], v1 offset:16384
	ds_read_b128 v[142:145], v1 offset:17408
	ds_read_b128 v[146:149], v1 offset:18432
	ds_read_b128 v[150:153], v1 offset:19456
	ds_read_b128 v[154:157], v1 offset:20480
	ds_read_b128 v[158:161], v1 offset:21504
	ds_read_b128 v[162:165], v1 offset:22528
	ds_read_b128 v[166:169], v1 offset:23552
	global_load_lds_dwordx4 v[42:43], off
	v_add_u32_e32 v42, 0x2000, v35
	v_lshl_add_u64 v[44:45], v[28:29], 0, s[0:1]
	v_readfirstlane_b32 s10, v42
	s_mov_b32 m0, s10
	s_nop 0
	global_load_lds_dwordx4 v[44:45], off
	s_barrier
	s_waitcnt lgkmcnt(0)
	s_setprio 1
	s_waitcnt lgkmcnt(0)
	v_mfma_f32_16x16x32_f16 v[170:173], v[10:13], v[82:85], 0
	v_mfma_f32_16x16x32_f16 v[178:181], v[10:13], v[146:149], 0
	v_mfma_f32_16x16x32_f16 v[186:189], v[10:13], v[154:157], 0
	v_mfma_f32_16x16x32_f16 v[10:13], v[10:13], v[162:165], 0
	v_mfma_f32_16x16x32_f16 v[174:177], v[50:53], v[82:85], 0
	v_mfma_f32_16x16x32_f16 v[182:185], v[50:53], v[146:149], 0
	v_mfma_f32_16x16x32_f16 v[190:193], v[50:53], v[154:157], 0
	v_mfma_f32_16x16x32_f16 v[194:197], v[14:17], v[166:169], v[10:13]
	v_mfma_f32_16x16x32_f16 v[10:13], v[50:53], v[162:165], 0
	v_mfma_f32_16x16x32_f16 v[170:173], v[14:17], v[142:145], v[170:173]
	v_mfma_f32_16x16x32_f16 v[174:177], v[54:57], v[142:145], v[174:177]
	v_mfma_f32_16x16x32_f16 v[178:181], v[14:17], v[150:153], v[178:181]
	v_mfma_f32_16x16x32_f16 v[182:185], v[54:57], v[150:153], v[182:185]
	v_mfma_f32_16x16x32_f16 v[186:189], v[14:17], v[158:161], v[186:189]
	v_mfma_f32_16x16x32_f16 v[190:193], v[54:57], v[158:161], v[190:193]
	v_mfma_f32_16x16x32_f16 v[50:53], v[54:57], v[166:169], v[10:13]
	s_setprio 0
	s_barrier
	v_readfirstlane_b32 s14, v34
	v_add_u32_e32 v43, 0x2000, v34
	v_lshl_add_u64 v[10:11], v[22:23], 0, s[0:1]
	s_mov_b32 m0, s14
	v_readfirstlane_b32 s11, v43
	global_load_lds_dwordx4 v[10:11], off
	v_lshl_add_u64 v[10:11], v[24:25], 0, s[0:1]
	s_mov_b32 m0, s11
	s_nop 0
	global_load_lds_dwordx4 v[10:11], off
	s_waitcnt vmcnt(6)
	s_barrier
	s_setprio 1
	v_mfma_f32_16x16x32_f16 v[10:13], v[118:121], v[82:85], 0
	v_mfma_f32_16x16x32_f16 v[54:57], v[122:125], v[142:145], v[10:13]
	v_mfma_f32_16x16x32_f16 v[10:13], v[126:129], v[82:85], 0
	v_mfma_f32_16x16x32_f16 v[82:85], v[130:133], v[142:145], v[10:13]
	v_mfma_f32_16x16x32_f16 v[10:13], v[118:121], v[146:149], 0
	v_mfma_f32_16x16x32_f16 v[142:145], v[122:125], v[150:153], v[10:13]
	v_mfma_f32_16x16x32_f16 v[10:13], v[126:129], v[146:149], 0
	v_mfma_f32_16x16x32_f16 v[146:149], v[130:133], v[150:153], v[10:13]
	v_mfma_f32_16x16x32_f16 v[10:13], v[118:121], v[154:157], 0
	v_mfma_f32_16x16x32_f16 v[150:153], v[122:125], v[158:161], v[10:13]
	v_mfma_f32_16x16x32_f16 v[10:13], v[126:129], v[154:157], 0
	v_mfma_f32_16x16x32_f16 v[154:157], v[130:133], v[158:161], v[10:13]
	v_mfma_f32_16x16x32_f16 v[10:13], v[118:121], v[162:165], 0
	v_mfma_f32_16x16x32_f16 v[118:121], v[122:125], v[166:169], v[10:13]
	v_mfma_f32_16x16x32_f16 v[10:13], v[126:129], v[162:165], 0
	v_mfma_f32_16x16x32_f16 v[122:125], v[130:133], v[166:169], v[10:13]
	s_setprio 0
	s_nop 5
	v_add_u32_e32 v10, 0x18000, v234
	v_add_u32_e32 v12, 0x18800, v234
	s_barrier
	v_add_u32_e32 v11, 0x18400, v234
	ds_read_b128 v[126:129], v10
	ds_read_b128 v[130:133], v11
	v_add_u32_e32 v13, 0x18c00, v234
	ds_read_b128 v[158:161], v12
	ds_read_b128 v[162:165], v13
	v_add_u32_e32 v44, 0x4000, v35
	v_add_u32_e32 v45, 0x6000, v35
	v_readfirstlane_b32 s20, v44
	v_lshl_add_u64 v[14:15], v[18:19], 0, s[0:1]
	s_mov_b32 m0, s20
	v_readfirstlane_b32 s18, v45
	ds_read_b128 v[166:169], v1 offset:32768
	ds_read_b128 v[198:201], v1 offset:33792
	ds_read_b128 v[202:205], v1 offset:34816
	ds_read_b128 v[206:209], v1 offset:35840
	ds_read_b128 v[210:213], v1 offset:36864
	ds_read_b128 v[214:217], v1 offset:37888
	ds_read_b128 v[218:221], v1 offset:38912
	ds_read_b128 v[222:225], v1 offset:39936
	global_load_lds_dwordx4 v[14:15], off
	v_lshl_add_u64 v[14:15], v[20:21], 0, s[0:1]
	s_mov_b32 m0, s18
	s_nop 0
	global_load_lds_dwordx4 v[14:15], off
	s_waitcnt lgkmcnt(8)
	s_barrier
	s_waitcnt lgkmcnt(0)
	s_setprio 1
	s_waitcnt lgkmcnt(0)
	v_mfma_f32_16x16x32_f16 v[14:17], v[126:129], v[166:169], v[86:89]
	v_mfma_f32_16x16x32_f16 v[86:89], v[130:133], v[198:201], v[14:17]
	v_mfma_f32_16x16x32_f16 v[14:17], v[158:161], v[166:169], v[90:93]
	v_mfma_f32_16x16x32_f16 v[90:93], v[162:165], v[198:201], v[14:17]
	v_mfma_f32_16x16x32_f16 v[14:17], v[126:129], v[202:205], v[94:97]
	v_mfma_f32_16x16x32_f16 v[94:97], v[130:133], v[206:209], v[14:17]
	v_mfma_f32_16x16x32_f16 v[14:17], v[158:161], v[202:205], v[98:101]
	v_mfma_f32_16x16x32_f16 v[98:101], v[162:165], v[206:209], v[14:17]
	v_mfma_f32_16x16x32_f16 v[14:17], v[126:129], v[210:213], v[102:105]
	v_mfma_f32_16x16x32_f16 v[102:105], v[130:133], v[214:217], v[14:17]
	v_mfma_f32_16x16x32_f16 v[14:17], v[158:161], v[210:213], v[106:109]
	v_mfma_f32_16x16x32_f16 v[106:109], v[162:165], v[214:217], v[14:17]
	v_mfma_f32_16x16x32_f16 v[14:17], v[126:129], v[218:221], v[110:113]
	v_mfma_f32_16x16x32_f16 v[110:113], v[130:133], v[222:225], v[14:17]
	v_mfma_f32_16x16x32_f16 v[14:17], v[158:161], v[218:221], v[114:117]
	v_mfma_f32_16x16x32_f16 v[114:117], v[162:165], v[222:225], v[14:17]
	s_setprio 0
	s_barrier
	s_mov_b64 s[0:1], 0x180
	s_mov_b32 m0, s22
	s_nop 2
	v_add_u32_e32 v14, 0x1c000, v234
	v_add_u32_e32 v16, 0x1c800, v234
	v_lshl_add_u64 v[242:243], v[30:31], 0, s[0:1]
	v_add_u32_e32 v15, 0x1c400, v234
	ds_read_b128 v[226:229], v14
	ds_read_b128 v[230:233], v15
	v_add_u32_e32 v17, 0x1cc00, v234
	ds_read_b128 v[234:237], v16
	ds_read_b128 v[238:241], v17
	global_load_lds_dwordx4 v[242:243], off
	v_lshl_add_u64 v[242:243], v[32:33], 0, s[0:1]
	s_mov_b32 m0, s21
	s_nop 0
	global_load_lds_dwordx4 v[242:243], off
	s_barrier
	s_waitcnt lgkmcnt(0)
	s_setprio 1
	s_waitcnt lgkmcnt(0)
	v_mfma_f32_16x16x32_f16 v[134:137], v[226:229], v[166:169], v[134:137]
	v_mfma_f32_16x16x32_f16 v[138:141], v[226:229], v[202:205], v[138:141]
	v_mfma_f32_16x16x32_f16 v[66:69], v[226:229], v[210:213], v[66:69]
	v_mfma_f32_16x16x32_f16 v[70:73], v[234:237], v[210:213], v[70:73]
	v_mfma_f32_16x16x32_f16 v[74:77], v[226:229], v[218:221], v[74:77]
	v_mfma_f32_16x16x32_f16 v[78:81], v[234:237], v[218:221], v[78:81]
	v_mfma_f32_16x16x32_f16 v[134:137], v[230:233], v[198:201], v[134:137]
	v_mfma_f32_16x16x32_f16 v[58:61], v[234:237], v[166:169], v[58:61]
	v_mfma_f32_16x16x32_f16 v[138:141], v[230:233], v[206:209], v[138:141]
	v_mfma_f32_16x16x32_f16 v[62:65], v[234:237], v[202:205], v[62:65]
	v_mfma_f32_16x16x32_f16 v[66:69], v[230:233], v[214:217], v[66:69]
	v_mfma_f32_16x16x32_f16 v[70:73], v[238:241], v[214:217], v[70:73]
	v_mfma_f32_16x16x32_f16 v[74:77], v[230:233], v[222:225], v[74:77]
	v_mfma_f32_16x16x32_f16 v[78:81], v[238:241], v[222:225], v[78:81]
	v_mfma_f32_16x16x32_f16 v[58:61], v[238:241], v[198:201], v[58:61]
	v_mfma_f32_16x16x32_f16 v[62:65], v[238:241], v[206:209], v[62:65]
	s_setprio 0
	s_mov_b32 m0, s19
	v_lshl_add_u64 v[242:243], v[26:27], 0, s[0:1]
	s_barrier
	ds_read_b128 v[166:169], v1 offset:49152
	ds_read_b128 v[198:201], v1 offset:50176
	ds_read_b128 v[202:205], v1 offset:51200
	ds_read_b128 v[206:209], v1 offset:52224
	ds_read_b128 v[210:213], v1 offset:53248
	ds_read_b128 v[214:217], v1 offset:54272
	ds_read_b128 v[218:221], v1 offset:55296
	ds_read_b128 v[222:225], v1 offset:56320
	global_load_lds_dwordx4 v[242:243], off
	v_lshl_add_u64 v[242:243], v[28:29], 0, s[0:1]
	s_mov_b32 m0, s17
	s_nop 0
	global_load_lds_dwordx4 v[242:243], off
	s_barrier
	s_waitcnt lgkmcnt(0)
	s_setprio 1
	s_waitcnt lgkmcnt(0)
	v_mfma_f32_16x16x32_f16 v[170:173], v[126:129], v[166:169], v[170:173]
	v_mfma_f32_16x16x32_f16 v[178:181], v[126:129], v[202:205], v[178:181]
	v_mfma_f32_16x16x32_f16 v[186:189], v[126:129], v[210:213], v[186:189]
	v_mfma_f32_16x16x32_f16 v[126:129], v[126:129], v[218:221], v[194:197]
	v_mfma_f32_16x16x32_f16 v[174:177], v[158:161], v[166:169], v[174:177]
	v_mfma_f32_16x16x32_f16 v[182:185], v[158:161], v[202:205], v[182:185]
	v_mfma_f32_16x16x32_f16 v[190:193], v[158:161], v[210:213], v[190:193]
	v_mfma_f32_16x16x32_f16 v[126:129], v[130:133], v[222:225], v[126:129]
	v_mfma_f32_16x16x32_f16 v[50:53], v[158:161], v[218:221], v[50:53]
	v_mfma_f32_16x16x32_f16 v[170:173], v[130:133], v[198:201], v[170:173]
	v_mfma_f32_16x16x32_f16 v[174:177], v[162:165], v[198:201], v[174:177]
	v_mfma_f32_16x16x32_f16 v[178:181], v[130:133], v[206:209], v[178:181]
	v_mfma_f32_16x16x32_f16 v[182:185], v[162:165], v[206:209], v[182:185]
	v_mfma_f32_16x16x32_f16 v[186:189], v[130:133], v[214:217], v[186:189]
	v_mfma_f32_16x16x32_f16 v[190:193], v[162:165], v[214:217], v[190:193]
	v_mfma_f32_16x16x32_f16 v[50:53], v[162:165], v[222:225], v[50:53]
	s_setprio 0
	s_barrier
	s_mov_b32 m0, s4
	v_lshl_add_u64 v[130:131], v[22:23], 0, s[0:1]
	global_load_lds_dwordx4 v[130:131], off
	v_lshl_add_u64 v[130:131], v[24:25], 0, s[0:1]
	s_mov_b32 m0, s3
	s_nop 0
	global_load_lds_dwordx4 v[130:131], off
	s_waitcnt vmcnt(6)
	s_barrier
	s_setprio 1
	v_mfma_f32_16x16x32_f16 v[82:85], v[234:237], v[166:169], v[82:85]
	v_mfma_f32_16x16x32_f16 v[130:133], v[226:229], v[202:205], v[142:145]
	v_mfma_f32_16x16x32_f16 v[142:145], v[234:237], v[202:205], v[146:149]
	v_mfma_f32_16x16x32_f16 v[146:149], v[226:229], v[210:213], v[150:153]
	v_mfma_f32_16x16x32_f16 v[150:153], v[234:237], v[210:213], v[154:157]
	v_mfma_f32_16x16x32_f16 v[118:121], v[226:229], v[218:221], v[118:121]
	v_mfma_f32_16x16x32_f16 v[122:125], v[234:237], v[218:221], v[122:125]
	v_mfma_f32_16x16x32_f16 v[54:57], v[226:229], v[166:169], v[54:57]
	v_mfma_f32_16x16x32_f16 v[82:85], v[238:241], v[198:201], v[82:85]
	v_mfma_f32_16x16x32_f16 v[130:133], v[230:233], v[206:209], v[130:133]
	v_mfma_f32_16x16x32_f16 v[142:145], v[238:241], v[206:209], v[142:145]
	v_mfma_f32_16x16x32_f16 v[150:153], v[238:241], v[214:217], v[150:153]
	v_mfma_f32_16x16x32_f16 v[118:121], v[230:233], v[222:225], v[118:121]
	v_mfma_f32_16x16x32_f16 v[122:125], v[238:241], v[222:225], v[122:125]
	v_mfma_f32_16x16x32_f16 v[54:57], v[230:233], v[198:201], v[54:57]
	v_mfma_f32_16x16x32_f16 v[146:149], v[230:233], v[214:217], v[146:149]
	s_setprio 0
	s_barrier
	ds_read_b128 v[154:157], v2
	ds_read_b128 v[158:161], v3
	ds_read_b128 v[162:165], v4
	ds_read_b128 v[166:169], v5
	s_mov_b32 m0, s7
	v_lshl_add_u64 v[194:195], v[18:19], 0, s[0:1]
	global_load_lds_dwordx4 v[194:195], off
	v_lshl_add_u64 v[194:195], v[20:21], 0, s[0:1]
	s_mov_b32 m0, s2
	s_nop 0
	global_load_lds_dwordx4 v[194:195], off
	ds_read_b128 v[194:197], v1
	ds_read_b128 v[198:201], v1 offset:1024
	ds_read_b128 v[202:205], v1 offset:2048
	ds_read_b128 v[206:209], v1 offset:3072
	ds_read_b128 v[210:213], v1 offset:4096
	ds_read_b128 v[214:217], v1 offset:5120
	ds_read_b128 v[218:221], v1 offset:6144
	ds_read_b128 v[222:225], v1 offset:7168
	s_waitcnt lgkmcnt(8)
	s_barrier
	s_waitcnt lgkmcnt(0)
	s_setprio 1
	s_waitcnt lgkmcnt(0)
	v_mfma_f32_16x16x32_f16 v[86:89], v[154:157], v[194:197], v[86:89]
	v_mfma_f32_16x16x32_f16 v[90:93], v[162:165], v[194:197], v[90:93]
	v_mfma_f32_16x16x32_f16 v[94:97], v[154:157], v[202:205], v[94:97]
	v_mfma_f32_16x16x32_f16 v[98:101], v[162:165], v[202:205], v[98:101]
	v_mfma_f32_16x16x32_f16 v[102:105], v[154:157], v[210:213], v[102:105]
	v_mfma_f32_16x16x32_f16 v[106:109], v[162:165], v[210:213], v[106:109]
	v_mfma_f32_16x16x32_f16 v[110:113], v[154:157], v[218:221], v[110:113]
	v_mfma_f32_16x16x32_f16 v[114:117], v[162:165], v[218:221], v[114:117]
	v_mfma_f32_16x16x32_f16 v[86:89], v[158:161], v[198:201], v[86:89]
	v_mfma_f32_16x16x32_f16 v[90:93], v[166:169], v[198:201], v[90:93]
	v_mfma_f32_16x16x32_f16 v[94:97], v[158:161], v[206:209], v[94:97]
	v_mfma_f32_16x16x32_f16 v[98:101], v[166:169], v[206:209], v[98:101]
	v_mfma_f32_16x16x32_f16 v[102:105], v[158:161], v[214:217], v[102:105]
	v_mfma_f32_16x16x32_f16 v[106:109], v[166:169], v[214:217], v[106:109]
	v_mfma_f32_16x16x32_f16 v[110:113], v[158:161], v[222:225], v[110:113]
	v_mfma_f32_16x16x32_f16 v[114:117], v[166:169], v[222:225], v[114:117]
	s_setprio 0
	s_barrier
	s_mov_b64 s[0:1], 0x200
	s_mov_b32 m0, s15
	v_lshl_add_u64 v[242:243], v[30:31], 0, s[0:1]
	ds_read_b128 v[226:229], v6
	ds_read_b128 v[230:233], v7
	ds_read_b128 v[234:237], v8
	ds_read_b128 v[238:241], v9
	global_load_lds_dwordx4 v[242:243], off
	v_lshl_add_u64 v[242:243], v[32:33], 0, s[0:1]
	s_mov_b32 m0, s5
	s_nop 0
	global_load_lds_dwordx4 v[242:243], off
	s_barrier
	s_waitcnt lgkmcnt(0)
	s_setprio 1
	s_waitcnt lgkmcnt(0)
	v_mfma_f32_16x16x32_f16 v[134:137], v[226:229], v[194:197], v[134:137]
	v_mfma_f32_16x16x32_f16 v[138:141], v[226:229], v[202:205], v[138:141]
	v_mfma_f32_16x16x32_f16 v[66:69], v[226:229], v[210:213], v[66:69]
	v_mfma_f32_16x16x32_f16 v[70:73], v[234:237], v[210:213], v[70:73]
	v_mfma_f32_16x16x32_f16 v[74:77], v[226:229], v[218:221], v[74:77]
	v_mfma_f32_16x16x32_f16 v[78:81], v[234:237], v[218:221], v[78:81]
	v_mfma_f32_16x16x32_f16 v[134:137], v[230:233], v[198:201], v[134:137]
	v_mfma_f32_16x16x32_f16 v[58:61], v[234:237], v[194:197], v[58:61]
	v_mfma_f32_16x16x32_f16 v[138:141], v[230:233], v[206:209], v[138:141]
	v_mfma_f32_16x16x32_f16 v[62:65], v[234:237], v[202:205], v[62:65]
	v_mfma_f32_16x16x32_f16 v[66:69], v[230:233], v[214:217], v[66:69]
	v_mfma_f32_16x16x32_f16 v[70:73], v[238:241], v[214:217], v[70:73]
	v_mfma_f32_16x16x32_f16 v[74:77], v[230:233], v[222:225], v[74:77]
	v_mfma_f32_16x16x32_f16 v[78:81], v[238:241], v[222:225], v[78:81]
	v_mfma_f32_16x16x32_f16 v[58:61], v[238:241], v[198:201], v[58:61]
	v_mfma_f32_16x16x32_f16 v[62:65], v[238:241], v[206:209], v[62:65]
	s_setprio 0
	s_mov_b32 m0, s16
	v_lshl_add_u64 v[242:243], v[26:27], 0, s[0:1]
	s_barrier
	ds_read_b128 v[194:197], v1 offset:16384
	ds_read_b128 v[198:201], v1 offset:17408
	ds_read_b128 v[202:205], v1 offset:18432
	ds_read_b128 v[206:209], v1 offset:19456
	ds_read_b128 v[210:213], v1 offset:20480
	ds_read_b128 v[214:217], v1 offset:21504
	ds_read_b128 v[218:221], v1 offset:22528
	ds_read_b128 v[222:225], v1 offset:23552
	global_load_lds_dwordx4 v[242:243], off
	v_lshl_add_u64 v[242:243], v[28:29], 0, s[0:1]
	s_mov_b32 m0, s10
	s_nop 0
	global_load_lds_dwordx4 v[242:243], off
	s_barrier
	s_waitcnt lgkmcnt(0)
	s_setprio 1
	s_waitcnt lgkmcnt(0)
	v_mfma_f32_16x16x32_f16 v[126:129], v[154:157], v[218:221], v[126:129]
	v_mfma_f32_16x16x32_f16 v[170:173], v[154:157], v[194:197], v[170:173]
	v_mfma_f32_16x16x32_f16 v[174:177], v[162:165], v[194:197], v[174:177]
	v_mfma_f32_16x16x32_f16 v[178:181], v[154:157], v[202:205], v[178:181]
	v_mfma_f32_16x16x32_f16 v[182:185], v[162:165], v[202:205], v[182:185]
	v_mfma_f32_16x16x32_f16 v[186:189], v[154:157], v[210:213], v[186:189]
	v_mfma_f32_16x16x32_f16 v[190:193], v[162:165], v[210:213], v[190:193]
	v_mfma_f32_16x16x32_f16 v[126:129], v[158:161], v[222:225], v[126:129]
	v_mfma_f32_16x16x32_f16 v[50:53], v[162:165], v[218:221], v[50:53]
	v_mfma_f32_16x16x32_f16 v[170:173], v[158:161], v[198:201], v[170:173]
	v_mfma_f32_16x16x32_f16 v[174:177], v[166:169], v[198:201], v[174:177]
	v_mfma_f32_16x16x32_f16 v[178:181], v[158:161], v[206:209], v[178:181]
	v_mfma_f32_16x16x32_f16 v[182:185], v[166:169], v[206:209], v[182:185]
	v_mfma_f32_16x16x32_f16 v[186:189], v[158:161], v[214:217], v[186:189]
	v_mfma_f32_16x16x32_f16 v[190:193], v[166:169], v[214:217], v[190:193]
	v_mfma_f32_16x16x32_f16 v[50:53], v[166:169], v[222:225], v[50:53]
	s_setprio 0
	s_barrier
	s_mov_b32 m0, s14
	v_lshl_add_u64 v[154:155], v[22:23], 0, s[0:1]
	global_load_lds_dwordx4 v[154:155], off
	v_lshl_add_u64 v[154:155], v[24:25], 0, s[0:1]
	s_mov_b32 m0, s11
	s_nop 0
	global_load_lds_dwordx4 v[154:155], off
	s_waitcnt vmcnt(6)
	s_barrier
	s_setprio 1
	v_mfma_f32_16x16x32_f16 v[82:85], v[234:237], v[194:197], v[82:85]
	v_mfma_f32_16x16x32_f16 v[130:133], v[226:229], v[202:205], v[130:133]
	v_mfma_f32_16x16x32_f16 v[142:145], v[234:237], v[202:205], v[142:145]
	v_mfma_f32_16x16x32_f16 v[150:153], v[234:237], v[210:213], v[150:153]
	v_mfma_f32_16x16x32_f16 v[118:121], v[226:229], v[218:221], v[118:121]
	v_mfma_f32_16x16x32_f16 v[122:125], v[234:237], v[218:221], v[122:125]
	v_mfma_f32_16x16x32_f16 v[54:57], v[226:229], v[194:197], v[54:57]
	v_mfma_f32_16x16x32_f16 v[82:85], v[238:241], v[198:201], v[82:85]
	v_mfma_f32_16x16x32_f16 v[130:133], v[230:233], v[206:209], v[130:133]
	v_mfma_f32_16x16x32_f16 v[142:145], v[238:241], v[206:209], v[142:145]
	v_mfma_f32_16x16x32_f16 v[146:149], v[226:229], v[210:213], v[146:149]
	v_mfma_f32_16x16x32_f16 v[150:153], v[238:241], v[214:217], v[150:153]
	v_mfma_f32_16x16x32_f16 v[118:121], v[230:233], v[222:225], v[118:121]
	v_mfma_f32_16x16x32_f16 v[122:125], v[238:241], v[222:225], v[122:125]
	v_mfma_f32_16x16x32_f16 v[54:57], v[230:233], v[198:201], v[54:57]
	v_mfma_f32_16x16x32_f16 v[146:149], v[230:233], v[214:217], v[146:149]
	s_setprio 0
	s_barrier
	ds_read_b128 v[154:157], v10
	ds_read_b128 v[158:161], v11
	ds_read_b128 v[162:165], v12
	ds_read_b128 v[166:169], v13
	s_mov_b32 m0, s20
	v_lshl_add_u64 v[226:227], v[18:19], 0, s[0:1]
	ds_read_b128 v[194:197], v1 offset:32768
	ds_read_b128 v[198:201], v1 offset:33792
	ds_read_b128 v[202:205], v1 offset:34816
	ds_read_b128 v[206:209], v1 offset:35840
	ds_read_b128 v[210:213], v1 offset:36864
	ds_read_b128 v[214:217], v1 offset:37888
	ds_read_b128 v[218:221], v1 offset:38912
	ds_read_b128 v[222:225], v1 offset:39936
	global_load_lds_dwordx4 v[226:227], off
	v_lshl_add_u64 v[226:227], v[20:21], 0, s[0:1]
	s_mov_b32 m0, s18
	s_nop 0
	global_load_lds_dwordx4 v[226:227], off
	s_waitcnt lgkmcnt(8)
	s_barrier
	s_waitcnt lgkmcnt(0)
	s_setprio 1
	s_waitcnt lgkmcnt(0)
	v_mfma_f32_16x16x32_f16 v[86:89], v[154:157], v[194:197], v[86:89]
	v_mfma_f32_16x16x32_f16 v[90:93], v[162:165], v[194:197], v[90:93]
	v_mfma_f32_16x16x32_f16 v[94:97], v[154:157], v[202:205], v[94:97]
	v_mfma_f32_16x16x32_f16 v[98:101], v[162:165], v[202:205], v[98:101]
	v_mfma_f32_16x16x32_f16 v[102:105], v[154:157], v[210:213], v[102:105]
	v_mfma_f32_16x16x32_f16 v[106:109], v[162:165], v[210:213], v[106:109]
	v_mfma_f32_16x16x32_f16 v[110:113], v[154:157], v[218:221], v[110:113]
	v_mfma_f32_16x16x32_f16 v[114:117], v[162:165], v[218:221], v[114:117]
	v_mfma_f32_16x16x32_f16 v[86:89], v[158:161], v[198:201], v[86:89]
	v_mfma_f32_16x16x32_f16 v[90:93], v[166:169], v[198:201], v[90:93]
	v_mfma_f32_16x16x32_f16 v[94:97], v[158:161], v[206:209], v[94:97]
	v_mfma_f32_16x16x32_f16 v[98:101], v[166:169], v[206:209], v[98:101]
	v_mfma_f32_16x16x32_f16 v[102:105], v[158:161], v[214:217], v[102:105]
	v_mfma_f32_16x16x32_f16 v[106:109], v[166:169], v[214:217], v[106:109]
	v_mfma_f32_16x16x32_f16 v[110:113], v[158:161], v[222:225], v[110:113]
	v_mfma_f32_16x16x32_f16 v[114:117], v[166:169], v[222:225], v[114:117]
	s_setprio 0
	s_barrier
	s_mov_b64 s[0:1], 0x280
	v_readfirstlane_b32 s10, v48
	v_lshl_add_u64 v[242:243], v[30:31], 0, s[0:1]
	s_mov_b32 m0, s10
	v_readfirstlane_b32 s2, v49
	ds_read_b128 v[226:229], v14
	ds_read_b128 v[230:233], v15
	ds_read_b128 v[234:237], v16
	ds_read_b128 v[238:241], v17
	global_load_lds_dwordx4 v[242:243], off
	v_lshl_add_u64 v[242:243], v[32:33], 0, s[0:1]
	s_mov_b32 m0, s2
	s_nop 0
	global_load_lds_dwordx4 v[242:243], off
	s_barrier
	s_waitcnt lgkmcnt(0)
	s_setprio 1
	s_waitcnt lgkmcnt(0)
	v_mfma_f32_16x16x32_f16 v[134:137], v[226:229], v[194:197], v[134:137]
	v_mfma_f32_16x16x32_f16 v[138:141], v[226:229], v[202:205], v[138:141]
	v_mfma_f32_16x16x32_f16 v[66:69], v[226:229], v[210:213], v[66:69]
	v_mfma_f32_16x16x32_f16 v[70:73], v[234:237], v[210:213], v[70:73]
	v_mfma_f32_16x16x32_f16 v[74:77], v[226:229], v[218:221], v[74:77]
	v_mfma_f32_16x16x32_f16 v[78:81], v[234:237], v[218:221], v[78:81]
	v_mfma_f32_16x16x32_f16 v[134:137], v[230:233], v[198:201], v[134:137]
	v_mfma_f32_16x16x32_f16 v[58:61], v[234:237], v[194:197], v[58:61]
	v_mfma_f32_16x16x32_f16 v[138:141], v[230:233], v[206:209], v[138:141]
	v_mfma_f32_16x16x32_f16 v[62:65], v[234:237], v[202:205], v[62:65]
	v_mfma_f32_16x16x32_f16 v[66:69], v[230:233], v[214:217], v[66:69]
	v_mfma_f32_16x16x32_f16 v[70:73], v[238:241], v[214:217], v[70:73]
	v_mfma_f32_16x16x32_f16 v[74:77], v[230:233], v[222:225], v[74:77]
	v_mfma_f32_16x16x32_f16 v[78:81], v[238:241], v[222:225], v[78:81]
	v_mfma_f32_16x16x32_f16 v[58:61], v[238:241], v[198:201], v[58:61]
	v_mfma_f32_16x16x32_f16 v[62:65], v[238:241], v[206:209], v[62:65]
	s_setprio 0
	v_readfirstlane_b32 s11, v46
	v_lshl_add_u64 v[48:49], v[26:27], 0, s[0:1]
	s_mov_b32 m0, s11
	v_readfirstlane_b32 s3, v47
	s_barrier
	ds_read_b128 v[194:197], v1 offset:49152
	ds_read_b128 v[198:201], v1 offset:50176
	ds_read_b128 v[202:205], v1 offset:51200
	ds_read_b128 v[206:209], v1 offset:52224
	ds_read_b128 v[210:213], v1 offset:53248
	ds_read_b128 v[214:217], v1 offset:54272
	ds_read_b128 v[218:221], v1 offset:55296
	ds_read_b128 v[222:225], v1 offset:56320
	global_load_lds_dwordx4 v[48:49], off
	v_lshl_add_u64 v[48:49], v[28:29], 0, s[0:1]
	s_mov_b32 m0, s3
	s_nop 0
	global_load_lds_dwordx4 v[48:49], off
	s_barrier
	s_waitcnt lgkmcnt(0)
	s_setprio 1
	s_waitcnt lgkmcnt(0)
	v_mfma_f32_16x16x32_f16 v[126:129], v[154:157], v[218:221], v[126:129]
	v_mfma_f32_16x16x32_f16 v[46:49], v[154:157], v[194:197], v[170:173]
	v_mfma_f32_16x16x32_f16 v[170:173], v[162:165], v[194:197], v[174:177]
	v_mfma_f32_16x16x32_f16 v[174:177], v[154:157], v[202:205], v[178:181]
	v_mfma_f32_16x16x32_f16 v[178:181], v[162:165], v[202:205], v[182:185]
	v_mfma_f32_16x16x32_f16 v[182:185], v[154:157], v[210:213], v[186:189]
	v_mfma_f32_16x16x32_f16 v[186:189], v[162:165], v[210:213], v[190:193]
	v_mfma_f32_16x16x32_f16 v[126:129], v[158:161], v[222:225], v[126:129]
	v_mfma_f32_16x16x32_f16 v[50:53], v[162:165], v[218:221], v[50:53]
	v_mfma_f32_16x16x32_f16 v[46:49], v[158:161], v[198:201], v[46:49]
	v_mfma_f32_16x16x32_f16 v[170:173], v[166:169], v[198:201], v[170:173]
	v_mfma_f32_16x16x32_f16 v[174:177], v[158:161], v[206:209], v[174:177]
	v_mfma_f32_16x16x32_f16 v[178:181], v[166:169], v[206:209], v[178:181]
	v_mfma_f32_16x16x32_f16 v[182:185], v[158:161], v[214:217], v[182:185]
	v_mfma_f32_16x16x32_f16 v[186:189], v[166:169], v[214:217], v[186:189]
	v_mfma_f32_16x16x32_f16 v[50:53], v[166:169], v[222:225], v[50:53]
	s_setprio 0
	s_barrier
	v_readfirstlane_b32 s5, v38
	v_lshl_add_u64 v[154:155], v[22:23], 0, s[0:1]
	s_mov_b32 m0, s5
	v_readfirstlane_b32 s4, v40
	global_load_lds_dwordx4 v[154:155], off
	v_lshl_add_u64 v[154:155], v[24:25], 0, s[0:1]
	s_mov_b32 m0, s4
	s_nop 0
	global_load_lds_dwordx4 v[154:155], off
	s_waitcnt vmcnt(6)
	s_barrier
	s_setprio 1
	v_mfma_f32_16x16x32_f16 v[82:85], v[234:237], v[194:197], v[82:85]
	v_mfma_f32_16x16x32_f16 v[130:133], v[226:229], v[202:205], v[130:133]
	v_mfma_f32_16x16x32_f16 v[142:145], v[234:237], v[202:205], v[142:145]
	v_mfma_f32_16x16x32_f16 v[150:153], v[234:237], v[210:213], v[150:153]
	v_mfma_f32_16x16x32_f16 v[118:121], v[226:229], v[218:221], v[118:121]
	v_mfma_f32_16x16x32_f16 v[122:125], v[234:237], v[218:221], v[122:125]
	v_mfma_f32_16x16x32_f16 v[54:57], v[226:229], v[194:197], v[54:57]
	v_mfma_f32_16x16x32_f16 v[82:85], v[238:241], v[198:201], v[82:85]
	v_mfma_f32_16x16x32_f16 v[130:133], v[230:233], v[206:209], v[130:133]
	v_mfma_f32_16x16x32_f16 v[142:145], v[238:241], v[206:209], v[142:145]
	v_mfma_f32_16x16x32_f16 v[146:149], v[226:229], v[210:213], v[146:149]
	v_mfma_f32_16x16x32_f16 v[150:153], v[238:241], v[214:217], v[150:153]
	v_mfma_f32_16x16x32_f16 v[118:121], v[230:233], v[222:225], v[118:121]
	v_mfma_f32_16x16x32_f16 v[122:125], v[238:241], v[222:225], v[122:125]
	v_mfma_f32_16x16x32_f16 v[54:57], v[230:233], v[198:201], v[54:57]
	v_mfma_f32_16x16x32_f16 v[146:149], v[230:233], v[214:217], v[146:149]
	s_setprio 0
	s_barrier
	ds_read_b128 v[154:157], v2
	ds_read_b128 v[158:161], v3
	ds_read_b128 v[162:165], v4
	ds_read_b128 v[166:169], v5
	v_readfirstlane_b32 s14, v37
	v_lshl_add_u64 v[190:191], v[18:19], 0, s[0:1]
	s_mov_b32 m0, s14
	v_readfirstlane_b32 s7, v39
	global_load_lds_dwordx4 v[190:191], off
	v_lshl_add_u64 v[190:191], v[20:21], 0, s[0:1]
	s_mov_b32 m0, s7
	s_nop 0
	global_load_lds_dwordx4 v[190:191], off
	ds_read_b128 v[190:193], v1
	ds_read_b128 v[194:197], v1 offset:1024
	ds_read_b128 v[198:201], v1 offset:2048
	ds_read_b128 v[202:205], v1 offset:3072
	ds_read_b128 v[206:209], v1 offset:4096
	ds_read_b128 v[210:213], v1 offset:5120
	ds_read_b128 v[214:217], v1 offset:6144
	ds_read_b128 v[218:221], v1 offset:7168
	s_waitcnt lgkmcnt(8)
	s_barrier
	s_waitcnt lgkmcnt(0)
	s_setprio 1
	s_waitcnt lgkmcnt(0)
	v_mfma_f32_16x16x32_f16 v[86:89], v[154:157], v[190:193], v[86:89]
	v_mfma_f32_16x16x32_f16 v[90:93], v[162:165], v[190:193], v[90:93]
	v_mfma_f32_16x16x32_f16 v[94:97], v[154:157], v[198:201], v[94:97]
	v_mfma_f32_16x16x32_f16 v[98:101], v[162:165], v[198:201], v[98:101]
	v_mfma_f32_16x16x32_f16 v[102:105], v[154:157], v[206:209], v[102:105]
	v_mfma_f32_16x16x32_f16 v[106:109], v[162:165], v[206:209], v[106:109]
	v_mfma_f32_16x16x32_f16 v[110:113], v[154:157], v[214:217], v[110:113]
	v_mfma_f32_16x16x32_f16 v[114:117], v[162:165], v[214:217], v[114:117]
	v_mfma_f32_16x16x32_f16 v[86:89], v[158:161], v[194:197], v[86:89]
	v_mfma_f32_16x16x32_f16 v[90:93], v[166:169], v[194:197], v[90:93]
	v_mfma_f32_16x16x32_f16 v[94:97], v[158:161], v[202:205], v[94:97]
	v_mfma_f32_16x16x32_f16 v[98:101], v[166:169], v[202:205], v[98:101]
	v_mfma_f32_16x16x32_f16 v[102:105], v[158:161], v[210:213], v[102:105]
	v_mfma_f32_16x16x32_f16 v[106:109], v[166:169], v[210:213], v[106:109]
	v_mfma_f32_16x16x32_f16 v[110:113], v[158:161], v[218:221], v[110:113]
	v_mfma_f32_16x16x32_f16 v[114:117], v[166:169], v[218:221], v[114:117]
	s_setprio 0
	s_barrier
	s_mov_b64 s[0:1], 0x300
	v_readfirstlane_b32 s15, v36
	v_lshl_add_u64 v[38:39], v[30:31], 0, s[0:1]
	s_mov_b32 m0, s15
	v_readfirstlane_b32 s15, v41
	ds_read_b128 v[222:225], v6
	ds_read_b128 v[226:229], v7
	ds_read_b128 v[230:233], v8
	ds_read_b128 v[234:237], v9
	global_load_lds_dwordx4 v[38:39], off
	v_lshl_add_u64 v[36:37], v[32:33], 0, s[0:1]
	s_mov_b32 m0, s15
	s_nop 0
	global_load_lds_dwordx4 v[36:37], off
	s_barrier
	s_waitcnt lgkmcnt(0)
	s_setprio 1
	s_waitcnt lgkmcnt(0)
	v_mfma_f32_16x16x32_f16 v[36:39], v[222:225], v[190:193], v[134:137]
	v_mfma_f32_16x16x32_f16 v[134:137], v[222:225], v[198:201], v[138:141]
	v_mfma_f32_16x16x32_f16 v[66:69], v[222:225], v[206:209], v[66:69]
	v_mfma_f32_16x16x32_f16 v[70:73], v[230:233], v[206:209], v[70:73]
	v_mfma_f32_16x16x32_f16 v[74:77], v[222:225], v[214:217], v[74:77]
	v_mfma_f32_16x16x32_f16 v[78:81], v[230:233], v[214:217], v[78:81]
	v_mfma_f32_16x16x32_f16 v[58:61], v[230:233], v[190:193], v[58:61]
	v_mfma_f32_16x16x32_f16 v[134:137], v[226:229], v[202:205], v[134:137]
	v_mfma_f32_16x16x32_f16 v[62:65], v[230:233], v[198:201], v[62:65]
	v_mfma_f32_16x16x32_f16 v[66:69], v[226:229], v[210:213], v[66:69]
	v_mfma_f32_16x16x32_f16 v[70:73], v[234:237], v[210:213], v[70:73]
	v_mfma_f32_16x16x32_f16 v[74:77], v[226:229], v[218:221], v[74:77]
	v_mfma_f32_16x16x32_f16 v[78:81], v[234:237], v[218:221], v[78:81]
	v_mfma_f32_16x16x32_f16 v[36:39], v[226:229], v[194:197], v[36:39]
	v_mfma_f32_16x16x32_f16 v[58:61], v[234:237], v[194:197], v[58:61]
	v_mfma_f32_16x16x32_f16 v[62:65], v[234:237], v[202:205], v[62:65]
	s_setprio 0
	v_readfirstlane_b32 s15, v35
	v_lshl_add_u64 v[40:41], v[26:27], 0, s[0:1]
	s_mov_b32 m0, s15
	v_readfirstlane_b32 s15, v42
	s_barrier
	ds_read_b128 v[138:141], v1 offset:16384
	ds_read_b128 v[190:193], v1 offset:17408
	ds_read_b128 v[194:197], v1 offset:18432
	ds_read_b128 v[198:201], v1 offset:19456
	ds_read_b128 v[202:205], v1 offset:20480
	ds_read_b128 v[206:209], v1 offset:21504
	ds_read_b128 v[210:213], v1 offset:22528
	ds_read_b128 v[214:217], v1 offset:23552
	global_load_lds_dwordx4 v[40:41], off
	v_lshl_add_u64 v[40:41], v[28:29], 0, s[0:1]
	s_mov_b32 m0, s15
	s_nop 0
	global_load_lds_dwordx4 v[40:41], off
	s_barrier
	s_waitcnt lgkmcnt(0)
	s_setprio 1
	s_waitcnt lgkmcnt(0)
	v_mfma_f32_16x16x32_f16 v[126:129], v[154:157], v[210:213], v[126:129]
	v_mfma_f32_16x16x32_f16 v[46:49], v[154:157], v[138:141], v[46:49]
	v_mfma_f32_16x16x32_f16 v[170:173], v[162:165], v[138:141], v[170:173]
	v_mfma_f32_16x16x32_f16 v[174:177], v[154:157], v[194:197], v[174:177]
	v_mfma_f32_16x16x32_f16 v[178:181], v[162:165], v[194:197], v[178:181]
	v_mfma_f32_16x16x32_f16 v[182:185], v[154:157], v[202:205], v[182:185]
	v_mfma_f32_16x16x32_f16 v[186:189], v[162:165], v[202:205], v[186:189]
	v_mfma_f32_16x16x32_f16 v[126:129], v[158:161], v[214:217], v[126:129]
	v_mfma_f32_16x16x32_f16 v[50:53], v[162:165], v[210:213], v[50:53]
	v_mfma_f32_16x16x32_f16 v[46:49], v[158:161], v[190:193], v[46:49]
	v_mfma_f32_16x16x32_f16 v[170:173], v[166:169], v[190:193], v[170:173]
	v_mfma_f32_16x16x32_f16 v[174:177], v[158:161], v[198:201], v[174:177]
	v_mfma_f32_16x16x32_f16 v[178:181], v[166:169], v[198:201], v[178:181]
	v_mfma_f32_16x16x32_f16 v[182:185], v[158:161], v[206:209], v[182:185]
	v_mfma_f32_16x16x32_f16 v[186:189], v[166:169], v[206:209], v[186:189]
	v_mfma_f32_16x16x32_f16 v[50:53], v[166:169], v[214:217], v[50:53]
	s_setprio 0
	s_barrier
	v_readfirstlane_b32 s15, v34
	v_lshl_add_u64 v[40:41], v[22:23], 0, s[0:1]
	s_mov_b32 m0, s15
	v_readfirstlane_b32 s15, v43
	global_load_lds_dwordx4 v[40:41], off
	v_lshl_add_u64 v[34:35], v[24:25], 0, s[0:1]
	s_mov_b32 m0, s15
	s_nop 0
	global_load_lds_dwordx4 v[34:35], off
	s_waitcnt vmcnt(6)
	s_barrier
	s_setprio 1
	v_mfma_f32_16x16x32_f16 v[40:43], v[222:225], v[138:141], v[54:57]
	v_mfma_f32_16x16x32_f16 v[54:57], v[230:233], v[138:141], v[82:85]
	v_mfma_f32_16x16x32_f16 v[82:85], v[222:225], v[194:197], v[130:133]
	v_mfma_f32_16x16x32_f16 v[130:133], v[230:233], v[194:197], v[142:145]
	v_mfma_f32_16x16x32_f16 v[138:141], v[222:225], v[202:205], v[146:149]
	v_mfma_f32_16x16x32_f16 v[142:145], v[230:233], v[202:205], v[150:153]
	v_mfma_f32_16x16x32_f16 v[118:121], v[222:225], v[210:213], v[118:121]
	v_mfma_f32_16x16x32_f16 v[122:125], v[230:233], v[210:213], v[122:125]
	v_mfma_f32_16x16x32_f16 v[82:85], v[226:229], v[198:201], v[82:85]
	v_mfma_f32_16x16x32_f16 v[130:133], v[234:237], v[198:201], v[130:133]
	v_mfma_f32_16x16x32_f16 v[138:141], v[226:229], v[206:209], v[138:141]
	v_mfma_f32_16x16x32_f16 v[142:145], v[234:237], v[206:209], v[142:145]
	v_mfma_f32_16x16x32_f16 v[118:121], v[226:229], v[214:217], v[118:121]
	v_mfma_f32_16x16x32_f16 v[122:125], v[234:237], v[214:217], v[122:125]
	v_mfma_f32_16x16x32_f16 v[40:43], v[226:229], v[190:193], v[40:43]
	v_mfma_f32_16x16x32_f16 v[54:57], v[234:237], v[190:193], v[54:57]
	s_setprio 0
	s_barrier
	ds_read_b128 v[146:149], v10
	ds_read_b128 v[150:153], v11
	ds_read_b128 v[154:157], v12
	ds_read_b128 v[158:161], v13
	v_readfirstlane_b32 s15, v44
	v_lshl_add_u64 v[34:35], v[18:19], 0, s[0:1]
	s_mov_b32 m0, s15
	ds_read_b128 v[162:165], v1 offset:32768
	ds_read_b128 v[166:169], v1 offset:33792
	ds_read_b128 v[190:193], v1 offset:34816
	ds_read_b128 v[194:197], v1 offset:35840
	ds_read_b128 v[198:201], v1 offset:36864
	ds_read_b128 v[202:205], v1 offset:37888
	ds_read_b128 v[206:209], v1 offset:38912
	ds_read_b128 v[210:213], v1 offset:39936
	global_load_lds_dwordx4 v[34:35], off
	v_lshl_add_u64 v[34:35], v[20:21], 0, s[0:1]
	v_readfirstlane_b32 s0, v45
	s_mov_b32 m0, s0
	s_nop 0
	global_load_lds_dwordx4 v[34:35], off
	s_waitcnt lgkmcnt(8)
	s_barrier
	s_waitcnt lgkmcnt(0)
	s_setprio 1
	s_waitcnt lgkmcnt(0)
	v_mfma_f32_16x16x32_f16 v[86:89], v[146:149], v[162:165], v[86:89]
	v_mfma_f32_16x16x32_f16 v[90:93], v[154:157], v[162:165], v[90:93]
	v_mfma_f32_16x16x32_f16 v[94:97], v[146:149], v[190:193], v[94:97]
	v_mfma_f32_16x16x32_f16 v[98:101], v[154:157], v[190:193], v[98:101]
	v_mfma_f32_16x16x32_f16 v[102:105], v[146:149], v[198:201], v[102:105]
	v_mfma_f32_16x16x32_f16 v[106:109], v[154:157], v[198:201], v[106:109]
	v_mfma_f32_16x16x32_f16 v[110:113], v[146:149], v[206:209], v[110:113]
	v_mfma_f32_16x16x32_f16 v[114:117], v[154:157], v[206:209], v[114:117]
	v_mfma_f32_16x16x32_f16 v[86:89], v[150:153], v[166:169], v[86:89]
	v_mfma_f32_16x16x32_f16 v[90:93], v[158:161], v[166:169], v[90:93]
	v_mfma_f32_16x16x32_f16 v[94:97], v[150:153], v[194:197], v[94:97]
	v_mfma_f32_16x16x32_f16 v[98:101], v[158:161], v[194:197], v[98:101]
	v_mfma_f32_16x16x32_f16 v[102:105], v[150:153], v[202:205], v[102:105]
	v_mfma_f32_16x16x32_f16 v[106:109], v[158:161], v[202:205], v[106:109]
	v_mfma_f32_16x16x32_f16 v[110:113], v[150:153], v[210:213], v[110:113]
	v_mfma_f32_16x16x32_f16 v[114:117], v[158:161], v[210:213], v[114:117]
	s_setprio 0
	s_barrier
	s_mov_b64 s[0:1], 0x380
	s_mov_b32 m0, s10
	v_lshl_add_u64 v[30:31], v[30:31], 0, s[0:1]
	ds_read_b128 v[214:217], v14
	ds_read_b128 v[218:221], v15
	ds_read_b128 v[222:225], v16
	ds_read_b128 v[226:229], v17
	global_load_lds_dwordx4 v[30:31], off
	v_lshl_add_u64 v[30:31], v[32:33], 0, s[0:1]
	s_mov_b32 m0, s2
	s_nop 0
	global_load_lds_dwordx4 v[30:31], off
	s_barrier
	s_waitcnt lgkmcnt(0)
	s_setprio 1
	s_waitcnt lgkmcnt(0)
	v_mfma_f32_16x16x32_f16 v[30:33], v[214:217], v[162:165], v[36:39]
	v_mfma_f32_16x16x32_f16 v[66:69], v[214:217], v[198:201], v[66:69]
	v_mfma_f32_16x16x32_f16 v[70:73], v[222:225], v[198:201], v[70:73]
	v_mfma_f32_16x16x32_f16 v[74:77], v[214:217], v[206:209], v[74:77]
	v_mfma_f32_16x16x32_f16 v[78:81], v[222:225], v[206:209], v[78:81]
	v_mfma_f32_16x16x32_f16 v[30:33], v[218:221], v[166:169], v[30:33]
	v_mfma_f32_16x16x32_f16 v[34:37], v[222:225], v[162:165], v[58:61]
	v_mfma_f32_16x16x32_f16 v[58:61], v[214:217], v[190:193], v[134:137]
	v_mfma_f32_16x16x32_f16 v[62:65], v[222:225], v[190:193], v[62:65]
	v_mfma_f32_16x16x32_f16 v[66:69], v[218:221], v[202:205], v[66:69]
	v_mfma_f32_16x16x32_f16 v[70:73], v[226:229], v[202:205], v[70:73]
	v_mfma_f32_16x16x32_f16 v[74:77], v[218:221], v[210:213], v[74:77]
	v_mfma_f32_16x16x32_f16 v[78:81], v[226:229], v[210:213], v[78:81]
	v_mfma_f32_16x16x32_f16 v[34:37], v[226:229], v[166:169], v[34:37]
	v_mfma_f32_16x16x32_f16 v[58:61], v[218:221], v[194:197], v[58:61]
	v_mfma_f32_16x16x32_f16 v[62:65], v[226:229], v[194:197], v[62:65]
	s_setprio 0
	s_mov_b32 m0, s11
	v_lshl_add_u64 v[26:27], v[26:27], 0, s[0:1]
	s_barrier
	ds_read_b128 v[134:137], v1 offset:49152
	ds_read_b128 v[162:165], v1 offset:50176
	ds_read_b128 v[166:169], v1 offset:51200
	ds_read_b128 v[190:193], v1 offset:52224
	ds_read_b128 v[194:197], v1 offset:53248
	ds_read_b128 v[198:201], v1 offset:54272
	ds_read_b128 v[202:205], v1 offset:55296
	ds_read_b128 v[206:209], v1 offset:56320
	global_load_lds_dwordx4 v[26:27], off
	v_lshl_add_u64 v[26:27], v[28:29], 0, s[0:1]
	s_mov_b32 m0, s3
	s_nop 0
	global_load_lds_dwordx4 v[26:27], off
	s_barrier
	s_waitcnt lgkmcnt(0)
	s_setprio 1
	s_waitcnt lgkmcnt(0)
	v_mfma_f32_16x16x32_f16 v[26:29], v[146:149], v[134:137], v[46:49]
	v_mfma_f32_16x16x32_f16 v[126:129], v[146:149], v[202:205], v[126:129]
	v_mfma_f32_16x16x32_f16 v[26:29], v[150:153], v[162:165], v[26:29]
	v_mfma_f32_16x16x32_f16 v[44:47], v[154:157], v[134:137], v[170:173]
	v_mfma_f32_16x16x32_f16 v[170:173], v[146:149], v[166:169], v[174:177]
	v_mfma_f32_16x16x32_f16 v[174:177], v[154:157], v[166:169], v[178:181]
	v_mfma_f32_16x16x32_f16 v[178:181], v[146:149], v[194:197], v[182:185]
	v_mfma_f32_16x16x32_f16 v[182:185], v[154:157], v[194:197], v[186:189]
	v_mfma_f32_16x16x32_f16 v[126:129], v[150:153], v[206:209], v[126:129]
	v_mfma_f32_16x16x32_f16 v[48:51], v[154:157], v[202:205], v[50:53]
	v_mfma_f32_16x16x32_f16 v[44:47], v[158:161], v[162:165], v[44:47]
	v_mfma_f32_16x16x32_f16 v[170:173], v[150:153], v[190:193], v[170:173]
	v_mfma_f32_16x16x32_f16 v[174:177], v[158:161], v[190:193], v[174:177]
	v_mfma_f32_16x16x32_f16 v[178:181], v[150:153], v[198:201], v[178:181]
	v_mfma_f32_16x16x32_f16 v[182:185], v[158:161], v[198:201], v[182:185]
	v_mfma_f32_16x16x32_f16 v[48:51], v[158:161], v[206:209], v[48:51]
	s_setprio 0
	s_barrier
	s_mov_b32 m0, s5
	v_lshl_add_u64 v[22:23], v[22:23], 0, s[0:1]
	global_load_lds_dwordx4 v[22:23], off
	v_lshl_add_u64 v[22:23], v[24:25], 0, s[0:1]
	s_mov_b32 m0, s4
	s_nop 0
	global_load_lds_dwordx4 v[22:23], off
	s_waitcnt vmcnt(6)
	s_barrier
	s_setprio 1
	v_mfma_f32_16x16x32_f16 v[22:25], v[214:217], v[134:137], v[40:43]
	v_mfma_f32_16x16x32_f16 v[38:41], v[222:225], v[134:137], v[54:57]
	v_mfma_f32_16x16x32_f16 v[52:55], v[214:217], v[166:169], v[82:85]
	v_mfma_f32_16x16x32_f16 v[82:85], v[222:225], v[166:169], v[130:133]
	v_mfma_f32_16x16x32_f16 v[130:133], v[214:217], v[194:197], v[138:141]
	v_mfma_f32_16x16x32_f16 v[134:137], v[222:225], v[194:197], v[142:145]
	v_mfma_f32_16x16x32_f16 v[118:121], v[214:217], v[202:205], v[118:121]
	v_mfma_f32_16x16x32_f16 v[122:125], v[222:225], v[202:205], v[122:125]
	v_mfma_f32_16x16x32_f16 v[22:25], v[218:221], v[162:165], v[22:25]
	v_mfma_f32_16x16x32_f16 v[82:85], v[226:229], v[190:193], v[82:85]
	v_mfma_f32_16x16x32_f16 v[130:133], v[218:221], v[198:201], v[130:133]
	v_mfma_f32_16x16x32_f16 v[134:137], v[226:229], v[198:201], v[134:137]
	v_mfma_f32_16x16x32_f16 v[118:121], v[218:221], v[206:209], v[118:121]
	v_mfma_f32_16x16x32_f16 v[122:125], v[226:229], v[206:209], v[122:125]
	v_mfma_f32_16x16x32_f16 v[38:41], v[226:229], v[162:165], v[38:41]
	v_mfma_f32_16x16x32_f16 v[52:55], v[218:221], v[190:193], v[52:55]
	s_setprio 0
	s_mov_b32 m0, s14
	v_lshl_add_u64 v[18:19], v[18:19], 0, s[0:1]
	s_barrier
	ds_read_b128 v[138:141], v2
	ds_read_b128 v[142:145], v3
	ds_read_b128 v[146:149], v4
	ds_read_b128 v[2:5], v5
	global_load_lds_dwordx4 v[18:19], off
	v_lshl_add_u64 v[18:19], v[20:21], 0, s[0:1]
	s_mov_b32 m0, s7
	s_nop 0
	global_load_lds_dwordx4 v[18:19], off
	ds_read_b128 v[18:21], v1
	ds_read_b128 v[150:153], v1 offset:1024
	ds_read_b128 v[154:157], v1 offset:2048
	ds_read_b128 v[158:161], v1 offset:3072
	ds_read_b128 v[162:165], v1 offset:4096
	ds_read_b128 v[166:169], v1 offset:5120
	ds_read_b128 v[186:189], v1 offset:6144
	ds_read_b128 v[190:193], v1 offset:7168
	s_barrier
	s_waitcnt lgkmcnt(0)
	s_setprio 1
	s_waitcnt lgkmcnt(0)
	v_mfma_f32_16x16x32_f16 v[86:89], v[138:141], v[18:21], v[86:89]
	v_mfma_f32_16x16x32_f16 v[90:93], v[146:149], v[18:21], v[90:93]
	v_mfma_f32_16x16x32_f16 v[94:97], v[138:141], v[154:157], v[94:97]
	v_mfma_f32_16x16x32_f16 v[98:101], v[146:149], v[154:157], v[98:101]
	v_mfma_f32_16x16x32_f16 v[102:105], v[138:141], v[162:165], v[102:105]
	v_mfma_f32_16x16x32_f16 v[106:109], v[146:149], v[162:165], v[106:109]
	v_mfma_f32_16x16x32_f16 v[110:113], v[138:141], v[186:189], v[110:113]
	v_mfma_f32_16x16x32_f16 v[86:89], v[142:145], v[150:153], v[86:89]
	v_mfma_f32_16x16x32_f16 v[90:93], v[2:5], v[150:153], v[90:93]
	v_mfma_f32_16x16x32_f16 v[94:97], v[142:145], v[158:161], v[94:97]
	v_mfma_f32_16x16x32_f16 v[98:101], v[2:5], v[158:161], v[98:101]
	v_mfma_f32_16x16x32_f16 v[102:105], v[142:145], v[166:169], v[102:105]
	v_mfma_f32_16x16x32_f16 v[106:109], v[2:5], v[166:169], v[106:109]
	v_mfma_f32_16x16x32_f16 v[110:113], v[142:145], v[190:193], v[110:113]
	v_mfma_f32_16x16x32_f16 v[114:117], v[146:149], v[186:189], v[114:117]
	v_mfma_f32_16x16x32_f16 v[194:197], v[2:5], v[190:193], v[114:117]
	s_setprio 0
	s_barrier
	s_nop 4
	ds_read_b128 v[114:117], v6
	ds_read_b128 v[198:201], v7
	ds_read_b128 v[202:205], v8
	ds_read_b128 v[6:9], v9
	s_barrier
	s_waitcnt lgkmcnt(0)
	s_setprio 1
	s_waitcnt lgkmcnt(0)
	v_mfma_f32_16x16x32_f16 v[30:33], v[114:117], v[18:21], v[30:33]
	v_mfma_f32_16x16x32_f16 v[18:21], v[202:205], v[18:21], v[34:37]
	v_mfma_f32_16x16x32_f16 v[34:37], v[114:117], v[154:157], v[58:61]
	v_mfma_f32_16x16x32_f16 v[56:59], v[202:205], v[154:157], v[62:65]
	v_mfma_f32_16x16x32_f16 v[60:63], v[114:117], v[162:165], v[66:69]
	v_mfma_f32_16x16x32_f16 v[64:67], v[202:205], v[162:165], v[70:73]
	v_mfma_f32_16x16x32_f16 v[68:71], v[114:117], v[186:189], v[74:77]
	v_mfma_f32_16x16x32_f16 v[72:75], v[202:205], v[186:189], v[78:81]
	v_mfma_f32_16x16x32_f16 v[30:33], v[198:201], v[150:153], v[30:33]
	v_mfma_f32_16x16x32_f16 v[18:21], v[6:9], v[150:153], v[18:21]
	v_mfma_f32_16x16x32_f16 v[64:67], v[6:9], v[166:169], v[64:67]
	v_mfma_f32_16x16x32_f16 v[68:71], v[198:201], v[190:193], v[68:71]
	v_mfma_f32_16x16x32_f16 v[72:75], v[6:9], v[190:193], v[72:75]
	v_mfma_f32_16x16x32_f16 v[34:37], v[198:201], v[158:161], v[34:37]
	v_mfma_f32_16x16x32_f16 v[56:59], v[6:9], v[158:161], v[56:59]
	v_mfma_f32_16x16x32_f16 v[60:63], v[198:201], v[166:169], v[60:63]
	s_setprio 0
	s_barrier
	ds_read_b128 v[76:79], v1 offset:16384
	ds_read_b128 v[150:153], v1 offset:17408
	ds_read_b128 v[154:157], v1 offset:18432
	ds_read_b128 v[158:161], v1 offset:19456
	ds_read_b128 v[162:165], v1 offset:20480
	ds_read_b128 v[166:169], v1 offset:21504
	ds_read_b128 v[186:189], v1 offset:22528
	ds_read_b128 v[190:193], v1 offset:23552
	s_waitcnt vmcnt(4)
	s_barrier
	s_waitcnt lgkmcnt(0)
	s_setprio 1
	s_waitcnt lgkmcnt(0)
	v_mfma_f32_16x16x32_f16 v[26:29], v[138:141], v[76:79], v[26:29]
	v_mfma_f32_16x16x32_f16 v[42:45], v[146:149], v[76:79], v[44:47]
	v_mfma_f32_16x16x32_f16 v[174:177], v[146:149], v[154:157], v[174:177]
	v_mfma_f32_16x16x32_f16 v[182:185], v[146:149], v[162:165], v[182:185]
	v_mfma_f32_16x16x32_f16 v[46:49], v[146:149], v[186:189], v[48:51]
	v_mfma_f32_16x16x32_f16 v[26:29], v[142:145], v[150:153], v[26:29]
	v_mfma_f32_16x16x32_f16 v[42:45], v[2:5], v[150:153], v[42:45]
	v_mfma_f32_16x16x32_f16 v[170:173], v[138:141], v[154:157], v[170:173]
	v_mfma_f32_16x16x32_f16 v[174:177], v[2:5], v[158:161], v[174:177]
	v_mfma_f32_16x16x32_f16 v[178:181], v[138:141], v[162:165], v[178:181]
	v_mfma_f32_16x16x32_f16 v[182:185], v[2:5], v[166:169], v[182:185]
	v_mfma_f32_16x16x32_f16 v[126:129], v[138:141], v[186:189], v[126:129]
	v_mfma_f32_16x16x32_f16 v[2:5], v[2:5], v[190:193], v[46:49]
	v_mfma_f32_16x16x32_f16 v[170:173], v[142:145], v[158:161], v[170:173]
	v_mfma_f32_16x16x32_f16 v[178:181], v[142:145], v[166:169], v[178:181]
	v_mfma_f32_16x16x32_f16 v[206:209], v[142:145], v[190:193], v[126:129]
	s_setprio 0
	s_setprio 1
	v_mfma_f32_16x16x32_f16 v[22:25], v[114:117], v[76:79], v[22:25]
	v_mfma_f32_16x16x32_f16 v[46:49], v[198:201], v[150:153], v[22:25]
	v_mfma_f32_16x16x32_f16 v[22:25], v[202:205], v[76:79], v[38:41]
	v_mfma_f32_16x16x32_f16 v[38:41], v[6:9], v[150:153], v[22:25]
	v_mfma_f32_16x16x32_f16 v[22:25], v[114:117], v[154:157], v[52:55]
	v_mfma_f32_16x16x32_f16 v[50:53], v[198:201], v[158:161], v[22:25]
	v_mfma_f32_16x16x32_f16 v[22:25], v[202:205], v[154:157], v[82:85]
	v_mfma_f32_16x16x32_f16 v[146:149], v[6:9], v[158:161], v[22:25]
	v_mfma_f32_16x16x32_f16 v[22:25], v[114:117], v[162:165], v[130:133]
	v_mfma_f32_16x16x32_f16 v[210:213], v[198:201], v[166:169], v[22:25]
	v_mfma_f32_16x16x32_f16 v[22:25], v[202:205], v[162:165], v[134:137]
	v_mfma_f32_16x16x32_f16 v[166:169], v[6:9], v[166:169], v[22:25]
	v_mfma_f32_16x16x32_f16 v[22:25], v[114:117], v[186:189], v[118:121]
	v_mfma_f32_16x16x32_f16 v[198:201], v[198:201], v[190:193], v[22:25]
	v_mfma_f32_16x16x32_f16 v[22:25], v[202:205], v[186:189], v[122:125]
	v_mfma_f32_16x16x32_f16 v[186:189], v[6:9], v[190:193], v[22:25]
	s_setprio 0
	s_barrier
	ds_read_b128 v[6:9], v10
	ds_read_b128 v[76:79], v11
	ds_read_b128 v[190:193], v12
	ds_read_b128 v[10:13], v13
	s_nop 0
	ds_read_b128 v[22:25], v1 offset:32768
	ds_read_b128 v[122:125], v1 offset:33792
	ds_read_b128 v[126:129], v1 offset:34816
	ds_read_b128 v[138:141], v1 offset:35840
	ds_read_b128 v[202:205], v1 offset:36864
	ds_read_b128 v[214:217], v1 offset:37888
	ds_read_b128 v[218:221], v1 offset:38912
	ds_read_b128 v[222:225], v1 offset:39936
	s_waitcnt vmcnt(2)
	s_barrier
	s_waitcnt lgkmcnt(0)
	s_setprio 1
	s_waitcnt lgkmcnt(0)
	v_mfma_f32_16x16x32_f16 v[80:83], v[6:9], v[22:25], v[86:89]
	v_mfma_f32_16x16x32_f16 v[162:165], v[76:79], v[122:125], v[80:83]
	v_mfma_f32_16x16x32_f16 v[80:83], v[190:193], v[22:25], v[90:93]
	v_mfma_f32_16x16x32_f16 v[154:157], v[10:13], v[122:125], v[80:83]
	v_mfma_f32_16x16x32_f16 v[80:83], v[6:9], v[126:129], v[94:97]
	v_mfma_f32_16x16x32_f16 v[134:137], v[76:79], v[138:141], v[80:83]
	v_mfma_f32_16x16x32_f16 v[80:83], v[190:193], v[126:129], v[98:101]
	v_mfma_f32_16x16x32_f16 v[130:133], v[10:13], v[138:141], v[80:83]
	v_mfma_f32_16x16x32_f16 v[80:83], v[6:9], v[202:205], v[102:105]
	v_mfma_f32_16x16x32_f16 v[118:121], v[76:79], v[214:217], v[80:83]
	v_mfma_f32_16x16x32_f16 v[80:83], v[190:193], v[202:205], v[106:109]
	v_mfma_f32_16x16x32_f16 v[114:117], v[10:13], v[214:217], v[80:83]
	v_mfma_f32_16x16x32_f16 v[80:83], v[6:9], v[218:221], v[110:113]
	v_mfma_f32_16x16x32_f16 v[86:89], v[76:79], v[222:225], v[80:83]
	v_mfma_f32_16x16x32_f16 v[80:83], v[190:193], v[218:221], v[194:197]
	v_mfma_f32_16x16x32_f16 v[82:85], v[10:13], v[222:225], v[80:83]
	s_setprio 0
	s_barrier
	ds_read_b128 v[194:197], v14
	ds_read_b128 v[226:229], v15
	ds_read_b128 v[230:233], v16
	ds_read_b128 v[234:237], v17
	s_waitcnt vmcnt(0)
	s_barrier
	s_waitcnt lgkmcnt(0)
	s_setprio 1
	s_waitcnt lgkmcnt(0)
	v_mfma_f32_16x16x32_f16 v[14:17], v[194:197], v[22:25], v[30:33]
	v_mfma_f32_16x16x32_f16 v[158:161], v[226:229], v[122:125], v[14:17]
	v_mfma_f32_16x16x32_f16 v[14:17], v[230:233], v[22:25], v[18:21]
	v_mfma_f32_16x16x32_f16 v[150:153], v[234:237], v[122:125], v[14:17]
	v_mfma_f32_16x16x32_f16 v[14:17], v[194:197], v[126:129], v[34:37]
	v_mfma_f32_16x16x32_f16 v[142:145], v[226:229], v[138:141], v[14:17]
	v_mfma_f32_16x16x32_f16 v[14:17], v[230:233], v[126:129], v[56:59]
	v_mfma_f32_16x16x32_f16 v[138:141], v[234:237], v[138:141], v[14:17]
	v_mfma_f32_16x16x32_f16 v[14:17], v[194:197], v[202:205], v[60:63]
	v_mfma_f32_16x16x32_f16 v[126:129], v[226:229], v[214:217], v[14:17]
	v_mfma_f32_16x16x32_f16 v[14:17], v[230:233], v[202:205], v[64:67]
	v_mfma_f32_16x16x32_f16 v[122:125], v[234:237], v[214:217], v[14:17]
	v_mfma_f32_16x16x32_f16 v[14:17], v[194:197], v[218:221], v[68:71]
	v_mfma_f32_16x16x32_f16 v[98:101], v[226:229], v[222:225], v[14:17]
	v_mfma_f32_16x16x32_f16 v[14:17], v[230:233], v[218:221], v[72:75]
	v_mfma_f32_16x16x32_f16 v[90:93], v[234:237], v[222:225], v[14:17]
	s_setprio 0
	s_barrier
	ds_read_b128 v[30:33], v1 offset:49152
	ds_read_b128 v[34:37], v1 offset:50176
	ds_read_b128 v[54:57], v1 offset:51200
	ds_read_b128 v[58:61], v1 offset:52224
	ds_read_b128 v[62:65], v1 offset:53248
	ds_read_b128 v[202:205], v1 offset:54272
	ds_read_b128 v[214:217], v1 offset:55296
	ds_read_b128 v[218:221], v1 offset:56320
	s_barrier
	s_waitcnt lgkmcnt(0)
	s_setprio 1
	s_waitcnt lgkmcnt(0)
	v_mfma_f32_16x16x32_f16 v[14:17], v[6:9], v[30:33], v[26:29]
	v_mfma_f32_16x16x32_f16 v[102:105], v[76:79], v[34:37], v[14:17]
	v_mfma_f32_16x16x32_f16 v[14:17], v[190:193], v[30:33], v[42:45]
	v_mfma_f32_16x16x32_f16 v[94:97], v[10:13], v[34:37], v[14:17]
	v_mfma_f32_16x16x32_f16 v[14:17], v[6:9], v[54:57], v[170:173]
	v_mfma_f32_16x16x32_f16 v[70:73], v[76:79], v[58:61], v[14:17]
	v_mfma_f32_16x16x32_f16 v[14:17], v[190:193], v[54:57], v[174:177]
	v_mfma_f32_16x16x32_f16 v[66:69], v[10:13], v[58:61], v[14:17]
	v_mfma_f32_16x16x32_f16 v[14:17], v[6:9], v[62:65], v[178:181]
	v_mfma_f32_16x16x32_f16 v[22:25], v[76:79], v[202:205], v[14:17]
	v_mfma_f32_16x16x32_f16 v[14:17], v[190:193], v[62:65], v[182:185]
	v_mfma_f32_16x16x32_f16 v[6:9], v[6:9], v[214:217], v[206:209]
	v_mfma_f32_16x16x32_f16 v[2:5], v[190:193], v[214:217], v[2:5]
	v_mfma_f32_16x16x32_f16 v[18:21], v[10:13], v[202:205], v[14:17]
	v_mfma_f32_16x16x32_f16 v[14:17], v[76:79], v[218:221], v[6:9]
	v_mfma_f32_16x16x32_f16 v[6:9], v[10:13], v[218:221], v[2:5]
	s_setprio 0
	s_setprio 1
	v_mfma_f32_16x16x32_f16 v[2:5], v[194:197], v[30:33], v[46:49]
	v_mfma_f32_16x16x32_f16 v[110:113], v[226:229], v[34:37], v[2:5]
	v_mfma_f32_16x16x32_f16 v[2:5], v[230:233], v[30:33], v[38:41]
	v_mfma_f32_16x16x32_f16 v[106:109], v[234:237], v[34:37], v[2:5]
	v_mfma_f32_16x16x32_f16 v[2:5], v[194:197], v[54:57], v[50:53]
	v_mfma_f32_16x16x32_f16 v[78:81], v[226:229], v[58:61], v[2:5]
	v_mfma_f32_16x16x32_f16 v[2:5], v[230:233], v[54:57], v[146:149]
	v_mfma_f32_16x16x32_f16 v[74:77], v[234:237], v[58:61], v[2:5]
	v_mfma_f32_16x16x32_f16 v[2:5], v[194:197], v[62:65], v[210:213]
	v_mfma_f32_16x16x32_f16 v[30:33], v[226:229], v[202:205], v[2:5]
	v_mfma_f32_16x16x32_f16 v[2:5], v[230:233], v[62:65], v[166:169]
	v_mfma_f32_16x16x32_f16 v[26:29], v[234:237], v[202:205], v[2:5]
	v_mfma_f32_16x16x32_f16 v[2:5], v[194:197], v[214:217], v[198:201]
	v_mfma_f32_16x16x32_f16 v[10:13], v[226:229], v[218:221], v[2:5]
	v_mfma_f32_16x16x32_f16 v[2:5], v[230:233], v[214:217], v[186:189]
	v_mfma_f32_16x16x32_f16 v[2:5], v[234:237], v[218:221], v[2:5]
	s_setprio 0
	s_barrier
	s_add_i32 s0, 0, 0x20800
	v_bfe_u32 v166, v0, 4, 2
	v_bfe_u32 v1, v0, 6, 2
	v_lshlrev_b32_e32 v34, 5, v166
	v_lshl_or_b32 v34, v1, 7, v34
	v_add_u32_e32 v35, s0, v34
	s_add_i32 s1, 0, 0x20c00
	v_add_u32_e32 v36, s1, v34
	ds_read_b128 v[58:61], v35
	ds_read_b128 v[62:65], v36
	v_or_b32_e32 v35, 16, v34
	v_add_u32_e32 v36, s0, v35
	v_add_u32_e32 v35, s1, v35
	ds_read_b128 v[50:53], v36
	ds_read_b128 v[54:57], v35
	v_or_b32_e32 v35, 0x200, v34
	v_add_u32_e32 v36, s0, v35
	v_add_u32_e32 v35, s1, v35
	v_or_b32_e32 v34, 0x210, v34
	ds_read_b128 v[42:45], v36
	ds_read_b128 v[46:49], v35
	v_add_u32_e32 v35, s0, v34
	v_and_b32_e32 v146, 15, v0
	v_ashrrev_i32_e32 v0, 2, v0
	s_movk_i32 s0, 0xffc0
	v_and_or_b32 v168, v0, s0, v146
	s_add_i32 s0, 0, 0x20000
	v_add_u32_e32 v38, s1, v34
	v_lshl_add_u32 v169, v168, 3, s0
	ds_read_b128 v[34:37], v35
	ds_read_b128 v[38:41], v38
	s_waitcnt vmcnt(0)
	ds_read2st64_b64 v[146:149], v169 offset1:2
	v_lshlrev_b32_e32 v0, 5, v1
	v_lshlrev_b32_e32 v1, 3, v166
	v_or3_b32 v166, v0, v1, s13
	v_add_u32_e32 v167, s12, v168
	s_waitcnt lgkmcnt(0)
	v_pk_fma_f32 v[0:1], v[146:147], v[58:59], v[162:163] op_sel_hi:[0,1,1] neg_lo:[1,0,0] neg_hi:[1,0,0]
	v_pk_fma_f32 v[0:1], v[146:147], v[0:1], v[62:63] op_sel:[1,0,0]
	v_mul_lo_u32 v170, v167, s6
	v_cvt_pk_f16_f32 v162, v0, v1
	v_pk_fma_f32 v[0:1], v[146:147], v[60:61], v[164:165] op_sel_hi:[0,1,1] neg_lo:[1,0,0] neg_hi:[1,0,0]
	v_pk_fma_f32 v[0:1], v[146:147], v[0:1], v[64:65] op_sel:[1,0,0]
	s_and_b32 s9, s9, 0xffff
	v_cvt_pk_f16_f32 v163, v0, v1
	v_pk_fma_f32 v[0:1], v[146:147], v[50:51], v[154:155] op_sel_hi:[0,1,1] neg_lo:[1,0,0] neg_hi:[1,0,0]
	v_pk_fma_f32 v[0:1], v[146:147], v[0:1], v[54:55] op_sel:[1,0,0]
	s_mov_b32 s11, 0x20000
	v_cvt_pk_f16_f32 v164, v0, v1
	v_pk_fma_f32 v[0:1], v[146:147], v[52:53], v[156:157] op_sel_hi:[0,1,1] neg_lo:[1,0,0] neg_hi:[1,0,0]
	v_pk_fma_f32 v[0:1], v[146:147], v[0:1], v[56:57] op_sel:[1,0,0]
	s_mov_b32 s10, 0x7ffffff0
	v_cvt_pk_f16_f32 v165, v0, v1
	v_pk_fma_f32 v[0:1], v[146:147], v[42:43], v[158:159] op_sel_hi:[0,1,1] neg_lo:[1,0,0] neg_hi:[1,0,0]
	v_pk_fma_f32 v[0:1], v[146:147], v[0:1], v[46:47] op_sel:[1,0,0]
	v_add_lshl_u32 v170, v166, v170, 1
	v_cvt_pk_f16_f32 v154, v0, v1
	v_pk_fma_f32 v[0:1], v[146:147], v[44:45], v[160:161] op_sel_hi:[0,1,1] neg_lo:[1,0,0] neg_hi:[1,0,0]
	v_pk_fma_f32 v[0:1], v[146:147], v[0:1], v[48:49] op_sel:[1,0,0]
	buffer_store_dwordx4 v[162:165], v170, s[8:11], 0 offen sc1
	v_cvt_pk_f16_f32 v155, v0, v1
	v_pk_fma_f32 v[0:1], v[146:147], v[34:35], v[150:151] op_sel_hi:[0,1,1] neg_lo:[1,0,0] neg_hi:[1,0,0]
	v_pk_fma_f32 v[0:1], v[146:147], v[0:1], v[38:39] op_sel:[1,0,0]
	s_nop 0
	v_cvt_pk_f16_f32 v156, v0, v1
	v_pk_fma_f32 v[0:1], v[146:147], v[36:37], v[152:153] op_sel_hi:[0,1,1] neg_lo:[1,0,0] neg_hi:[1,0,0]
	v_pk_fma_f32 v[0:1], v[146:147], v[0:1], v[40:41] op_sel:[1,0,0]
	s_nop 0
	v_cvt_pk_f16_f32 v157, v0, v1
	v_or_b32_e32 v0, 16, v168
	v_add_u32_e32 v146, s12, v0
	v_lshl_add_u32 v0, v0, 3, s0
	ds_read_b64 v[0:1], v0
	buffer_store_dwordx4 v[154:157], v170, s[8:11], 0 offen offset:256 sc1
	s_waitcnt lgkmcnt(0)
	v_pk_fma_f32 v[134:135], v[0:1], v[58:59], v[134:135] op_sel_hi:[0,1,1] neg_lo:[1,0,0] neg_hi:[1,0,0]
	v_pk_fma_f32 v[136:137], v[0:1], v[60:61], v[136:137] op_sel_hi:[0,1,1] neg_lo:[1,0,0] neg_hi:[1,0,0]
	v_pk_fma_f32 v[130:131], v[0:1], v[50:51], v[130:131] op_sel_hi:[0,1,1] neg_lo:[1,0,0] neg_hi:[1,0,0]
	v_pk_fma_f32 v[134:135], v[0:1], v[134:135], v[62:63] op_sel:[1,0,0]
	v_pk_fma_f32 v[136:137], v[0:1], v[136:137], v[64:65] op_sel:[1,0,0]
	v_pk_fma_f32 v[130:131], v[0:1], v[130:131], v[54:55] op_sel:[1,0,0]
	v_cvt_pk_f16_f32 v134, v134, v135
	v_cvt_pk_f16_f32 v135, v136, v137
	v_cvt_pk_f16_f32 v136, v130, v131
	v_pk_fma_f32 v[130:131], v[0:1], v[52:53], v[132:133] op_sel_hi:[0,1,1] neg_lo:[1,0,0] neg_hi:[1,0,0]
	v_pk_fma_f32 v[130:131], v[0:1], v[130:131], v[56:57] op_sel:[1,0,0]
	v_mul_lo_u32 v154, v146, s6
	v_or_b32_e32 v155, 32, v168
	v_or_b32_e32 v156, 48, v168
	v_cvt_pk_f16_f32 v137, v130, v131
	v_pk_fma_f32 v[130:131], v[0:1], v[42:43], v[142:143] op_sel_hi:[0,1,1] neg_lo:[1,0,0] neg_hi:[1,0,0]
	v_pk_fma_f32 v[132:133], v[0:1], v[44:45], v[144:145] op_sel_hi:[0,1,1] neg_lo:[1,0,0] neg_hi:[1,0,0]
	v_lshl_add_u32 v146, v155, 3, s0
	v_lshl_add_u32 v147, v156, 3, s0
	v_add_lshl_u32 v154, v166, v154, 1
	v_pk_fma_f32 v[130:131], v[0:1], v[130:131], v[46:47] op_sel:[1,0,0]
	v_pk_fma_f32 v[132:133], v[0:1], v[132:133], v[48:49] op_sel:[1,0,0]
	ds_read_b64 v[150:151], v146
	ds_read_b64 v[146:147], v147
	ds_read_b64 v[152:153], v169 offset:1408
	buffer_store_dwordx4 v[134:137], v154, s[8:11], 0 offen sc1
	v_cvt_pk_f16_f32 v130, v130, v131
	v_cvt_pk_f16_f32 v131, v132, v133
	v_pk_fma_f32 v[132:133], v[0:1], v[34:35], v[138:139] op_sel_hi:[0,1,1] neg_lo:[1,0,0] neg_hi:[1,0,0]
	v_pk_fma_f32 v[134:135], v[0:1], v[36:37], v[140:141] op_sel_hi:[0,1,1] neg_lo:[1,0,0] neg_hi:[1,0,0]
	v_pk_fma_f32 v[132:133], v[0:1], v[132:133], v[38:39] op_sel:[1,0,0]
	v_pk_fma_f32 v[0:1], v[0:1], v[134:135], v[40:41] op_sel:[1,0,0]
	v_cvt_pk_f16_f32 v132, v132, v133
	v_cvt_pk_f16_f32 v133, v0, v1
	v_add_u32_e32 v0, s12, v155
	buffer_store_dwordx4 v[130:133], v154, s[8:11], 0 offen offset:256 sc1
	s_and_saveexec_b64 s[44:45], vcc
	s_cbranch_execz .LBB6_34
	s_barrier
.LBB6_34:
	s_or_b64 exec, exec, s[44:45]
	s_waitcnt lgkmcnt(0)
	v_pk_fma_f32 v[2:3], v[152:153], v[34:35], v[2:3] op_sel_hi:[0,1,1] neg_lo:[1,0,0] neg_hi:[1,0,0]
	v_pk_fma_f32 v[4:5], v[152:153], v[36:37], v[4:5] op_sel_hi:[0,1,1] neg_lo:[1,0,0] neg_hi:[1,0,0]
	v_mul_lo_u32 v130, v0, s6
	v_pk_fma_f32 v[0:1], v[150:151], v[58:59], v[118:119] op_sel_hi:[0,1,1] neg_lo:[1,0,0] neg_hi:[1,0,0]
	v_pk_fma_f32 v[0:1], v[150:151], v[0:1], v[62:63] op_sel:[1,0,0]
	v_add_lshl_u32 v130, v166, v130, 1
	v_cvt_pk_f16_f32 v118, v0, v1
	v_pk_fma_f32 v[0:1], v[150:151], v[60:61], v[120:121] op_sel_hi:[0,1,1] neg_lo:[1,0,0] neg_hi:[1,0,0]
	v_pk_fma_f32 v[0:1], v[150:151], v[0:1], v[64:65] op_sel:[1,0,0]
	v_pk_fma_f32 v[2:3], v[152:153], v[2:3], v[38:39] op_sel:[1,0,0]
	v_cvt_pk_f16_f32 v119, v0, v1
	v_pk_fma_f32 v[0:1], v[150:151], v[50:51], v[114:115] op_sel_hi:[0,1,1] neg_lo:[1,0,0] neg_hi:[1,0,0]
	v_pk_fma_f32 v[0:1], v[150:151], v[0:1], v[54:55] op_sel:[1,0,0]
	v_pk_fma_f32 v[4:5], v[152:153], v[4:5], v[40:41] op_sel:[1,0,0]
	v_cvt_pk_f16_f32 v120, v0, v1
	v_pk_fma_f32 v[0:1], v[150:151], v[52:53], v[116:117] op_sel_hi:[0,1,1] neg_lo:[1,0,0] neg_hi:[1,0,0]
	v_pk_fma_f32 v[0:1], v[150:151], v[0:1], v[56:57] op_sel:[1,0,0]
	v_cvt_pk_f16_f32 v2, v2, v3
	v_cvt_pk_f16_f32 v121, v0, v1
	v_pk_fma_f32 v[0:1], v[150:151], v[42:43], v[126:127] op_sel_hi:[0,1,1] neg_lo:[1,0,0] neg_hi:[1,0,0]
	v_pk_fma_f32 v[0:1], v[150:151], v[0:1], v[46:47] op_sel:[1,0,0]
	buffer_store_dwordx4 v[118:121], v130, s[8:11], 0 offen sc1
	v_cvt_pk_f16_f32 v114, v0, v1
	v_pk_fma_f32 v[0:1], v[150:151], v[44:45], v[128:129] op_sel_hi:[0,1,1] neg_lo:[1,0,0] neg_hi:[1,0,0]
	v_pk_fma_f32 v[0:1], v[150:151], v[0:1], v[48:49] op_sel:[1,0,0]
	v_cvt_pk_f16_f32 v3, v4, v5
	v_cvt_pk_f16_f32 v115, v0, v1
	v_pk_fma_f32 v[0:1], v[150:151], v[34:35], v[122:123] op_sel_hi:[0,1,1] neg_lo:[1,0,0] neg_hi:[1,0,0]
	v_pk_fma_f32 v[0:1], v[150:151], v[0:1], v[38:39] op_sel:[1,0,0]
	s_nop 0
	v_cvt_pk_f16_f32 v116, v0, v1
	v_pk_fma_f32 v[0:1], v[150:151], v[36:37], v[124:125] op_sel_hi:[0,1,1] neg_lo:[1,0,0] neg_hi:[1,0,0]
	v_pk_fma_f32 v[0:1], v[150:151], v[0:1], v[40:41] op_sel:[1,0,0]
	s_nop 0
	v_cvt_pk_f16_f32 v117, v0, v1
	v_add_u32_e32 v0, s12, v156
	buffer_store_dwordx4 v[114:117], v130, s[8:11], 0 offen offset:256 sc1
	s_nop 1
	v_mul_lo_u32 v114, v0, s6
	v_pk_fma_f32 v[0:1], v[146:147], v[58:59], v[86:87] op_sel_hi:[0,1,1] neg_lo:[1,0,0] neg_hi:[1,0,0]
	v_pk_fma_f32 v[0:1], v[146:147], v[0:1], v[62:63] op_sel:[1,0,0]
	v_add_lshl_u32 v114, v166, v114, 1
	v_cvt_pk_f16_f32 v86, v0, v1
	v_pk_fma_f32 v[0:1], v[146:147], v[60:61], v[88:89] op_sel_hi:[0,1,1] neg_lo:[1,0,0] neg_hi:[1,0,0]
	v_pk_fma_f32 v[0:1], v[146:147], v[0:1], v[64:65] op_sel:[1,0,0]
	s_nop 0
	v_cvt_pk_f16_f32 v87, v0, v1
	v_pk_fma_f32 v[0:1], v[146:147], v[50:51], v[82:83] op_sel_hi:[0,1,1] neg_lo:[1,0,0] neg_hi:[1,0,0]
	v_pk_fma_f32 v[0:1], v[146:147], v[0:1], v[54:55] op_sel:[1,0,0]
	s_nop 0
	v_cvt_pk_f16_f32 v88, v0, v1
	v_pk_fma_f32 v[0:1], v[146:147], v[52:53], v[84:85] op_sel_hi:[0,1,1] neg_lo:[1,0,0] neg_hi:[1,0,0]
	v_pk_fma_f32 v[0:1], v[146:147], v[0:1], v[56:57] op_sel:[1,0,0]
	s_nop 0
	v_cvt_pk_f16_f32 v89, v0, v1
	v_pk_fma_f32 v[0:1], v[146:147], v[42:43], v[98:99] op_sel_hi:[0,1,1] neg_lo:[1,0,0] neg_hi:[1,0,0]
	v_pk_fma_f32 v[0:1], v[146:147], v[0:1], v[46:47] op_sel:[1,0,0]
	buffer_store_dwordx4 v[86:89], v114, s[8:11], 0 offen sc1
	v_cvt_pk_f16_f32 v82, v0, v1
	v_pk_fma_f32 v[0:1], v[146:147], v[44:45], v[100:101] op_sel_hi:[0,1,1] neg_lo:[1,0,0] neg_hi:[1,0,0]
	v_pk_fma_f32 v[0:1], v[146:147], v[0:1], v[48:49] op_sel:[1,0,0]
	s_nop 0
	v_cvt_pk_f16_f32 v83, v0, v1
	v_pk_fma_f32 v[0:1], v[146:147], v[34:35], v[90:91] op_sel_hi:[0,1,1] neg_lo:[1,0,0] neg_hi:[1,0,0]
	v_pk_fma_f32 v[0:1], v[146:147], v[0:1], v[38:39] op_sel:[1,0,0]
	s_nop 0
	v_cvt_pk_f16_f32 v84, v0, v1
	v_pk_fma_f32 v[0:1], v[146:147], v[36:37], v[92:93] op_sel_hi:[0,1,1] neg_lo:[1,0,0] neg_hi:[1,0,0]
	v_pk_fma_f32 v[0:1], v[146:147], v[0:1], v[40:41] op_sel:[1,0,0]
	s_nop 0
	v_cvt_pk_f16_f32 v85, v0, v1
	v_add_u32_e32 v0, 0x80, v167
	v_mul_lo_u32 v86, v0, s6
	v_pk_fma_f32 v[0:1], v[148:149], v[58:59], v[102:103] op_sel_hi:[0,1,1] neg_lo:[1,0,0] neg_hi:[1,0,0]
	v_pk_fma_f32 v[0:1], v[148:149], v[0:1], v[62:63] op_sel:[1,0,0]
	buffer_store_dwordx4 v[82:85], v114, s[8:11], 0 offen offset:256 sc1
	v_add_lshl_u32 v90, v166, v86, 1
	ds_read2_b64 v[86:89], v169 offset0:144 offset1:160
	v_cvt_pk_f16_f32 v82, v0, v1
	v_pk_fma_f32 v[0:1], v[148:149], v[60:61], v[104:105] op_sel_hi:[0,1,1] neg_lo:[1,0,0] neg_hi:[1,0,0]
	v_pk_fma_f32 v[0:1], v[148:149], v[0:1], v[64:65] op_sel:[1,0,0]
	s_nop 0
	v_cvt_pk_f16_f32 v83, v0, v1
	v_pk_fma_f32 v[0:1], v[148:149], v[50:51], v[94:95] op_sel_hi:[0,1,1] neg_lo:[1,0,0] neg_hi:[1,0,0]
	v_pk_fma_f32 v[0:1], v[148:149], v[0:1], v[54:55] op_sel:[1,0,0]
	s_nop 0
	v_cvt_pk_f16_f32 v84, v0, v1
	v_pk_fma_f32 v[0:1], v[148:149], v[52:53], v[96:97] op_sel_hi:[0,1,1] neg_lo:[1,0,0] neg_hi:[1,0,0]
	v_pk_fma_f32 v[0:1], v[148:149], v[0:1], v[56:57] op_sel:[1,0,0]
	s_nop 0
	v_cvt_pk_f16_f32 v85, v0, v1
	v_pk_fma_f32 v[0:1], v[148:149], v[42:43], v[110:111] op_sel_hi:[0,1,1] neg_lo:[1,0,0] neg_hi:[1,0,0]
	v_pk_fma_f32 v[0:1], v[148:149], v[0:1], v[46:47] op_sel:[1,0,0]
	buffer_store_dwordx4 v[82:85], v90, s[8:11], 0 offen sc1
	s_nop 1
	v_cvt_pk_f16_f32 v82, v0, v1
	v_pk_fma_f32 v[0:1], v[148:149], v[44:45], v[112:113] op_sel_hi:[0,1,1] neg_lo:[1,0,0] neg_hi:[1,0,0]
	v_pk_fma_f32 v[0:1], v[148:149], v[0:1], v[48:49] op_sel:[1,0,0]
	s_nop 0
	v_cvt_pk_f16_f32 v83, v0, v1
	v_pk_fma_f32 v[0:1], v[148:149], v[34:35], v[106:107] op_sel_hi:[0,1,1] neg_lo:[1,0,0] neg_hi:[1,0,0]
	v_pk_fma_f32 v[0:1], v[148:149], v[0:1], v[38:39] op_sel:[1,0,0]
	s_nop 0
	v_cvt_pk_f16_f32 v84, v0, v1
	v_pk_fma_f32 v[0:1], v[148:149], v[36:37], v[108:109] op_sel_hi:[0,1,1] neg_lo:[1,0,0] neg_hi:[1,0,0]
	v_pk_fma_f32 v[0:1], v[148:149], v[0:1], v[40:41] op_sel:[1,0,0]
	s_nop 0
	v_cvt_pk_f16_f32 v85, v0, v1
	v_add_u32_e32 v0, 0x90, v167
	buffer_store_dwordx4 v[82:85], v90, s[8:11], 0 offen offset:256 sc1
	s_nop 1
	v_mul_lo_u32 v82, v0, s6
	s_waitcnt lgkmcnt(0)
	v_pk_fma_f32 v[0:1], v[86:87], v[58:59], v[70:71] op_sel_hi:[0,1,1] neg_lo:[1,0,0] neg_hi:[1,0,0]
	v_pk_fma_f32 v[0:1], v[86:87], v[0:1], v[62:63] op_sel:[1,0,0]
	v_add_lshl_u32 v82, v166, v82, 1
	v_cvt_pk_f16_f32 v70, v0, v1
	v_pk_fma_f32 v[0:1], v[86:87], v[60:61], v[72:73] op_sel_hi:[0,1,1] neg_lo:[1,0,0] neg_hi:[1,0,0]
	v_pk_fma_f32 v[0:1], v[86:87], v[0:1], v[64:65] op_sel:[1,0,0]
	s_nop 0
	v_cvt_pk_f16_f32 v71, v0, v1
	v_pk_fma_f32 v[0:1], v[86:87], v[50:51], v[66:67] op_sel_hi:[0,1,1] neg_lo:[1,0,0] neg_hi:[1,0,0]
	v_pk_fma_f32 v[0:1], v[86:87], v[0:1], v[54:55] op_sel:[1,0,0]
	s_nop 0
	v_cvt_pk_f16_f32 v72, v0, v1
	v_pk_fma_f32 v[0:1], v[86:87], v[52:53], v[68:69] op_sel_hi:[0,1,1] neg_lo:[1,0,0] neg_hi:[1,0,0]
	v_pk_fma_f32 v[0:1], v[86:87], v[0:1], v[56:57] op_sel:[1,0,0]
	s_nop 0
	v_cvt_pk_f16_f32 v73, v0, v1
	v_pk_fma_f32 v[0:1], v[86:87], v[42:43], v[78:79] op_sel_hi:[0,1,1] neg_lo:[1,0,0] neg_hi:[1,0,0]
	v_pk_fma_f32 v[0:1], v[86:87], v[0:1], v[46:47] op_sel:[1,0,0]
	buffer_store_dwordx4 v[70:73], v82, s[8:11], 0 offen sc1
	v_cvt_pk_f16_f32 v66, v0, v1
	v_pk_fma_f32 v[0:1], v[86:87], v[44:45], v[80:81] op_sel_hi:[0,1,1] neg_lo:[1,0,0] neg_hi:[1,0,0]
	v_pk_fma_f32 v[0:1], v[86:87], v[0:1], v[48:49] op_sel:[1,0,0]
	s_nop 0
	v_cvt_pk_f16_f32 v67, v0, v1
	v_pk_fma_f32 v[0:1], v[86:87], v[34:35], v[74:75] op_sel_hi:[0,1,1] neg_lo:[1,0,0] neg_hi:[1,0,0]
	v_pk_fma_f32 v[0:1], v[86:87], v[0:1], v[38:39] op_sel:[1,0,0]
	s_nop 0
	v_cvt_pk_f16_f32 v68, v0, v1
	v_pk_fma_f32 v[0:1], v[86:87], v[36:37], v[76:77] op_sel_hi:[0,1,1] neg_lo:[1,0,0] neg_hi:[1,0,0]
	v_pk_fma_f32 v[0:1], v[86:87], v[0:1], v[40:41] op_sel:[1,0,0]
	s_nop 0
	v_cvt_pk_f16_f32 v69, v0, v1
	v_add_u32_e32 v0, 0xa0, v167
	buffer_store_dwordx4 v[66:69], v82, s[8:11], 0 offen offset:256 sc1
	s_nop 1
	v_mul_lo_u32 v66, v0, s6
	v_pk_fma_f32 v[0:1], v[88:89], v[58:59], v[22:23] op_sel_hi:[0,1,1] neg_lo:[1,0,0] neg_hi:[1,0,0]
	v_pk_fma_f32 v[0:1], v[88:89], v[0:1], v[62:63] op_sel:[1,0,0]
	v_add_lshl_u32 v66, v166, v66, 1
	v_cvt_pk_f16_f32 v22, v0, v1
	v_pk_fma_f32 v[0:1], v[88:89], v[60:61], v[24:25] op_sel_hi:[0,1,1] neg_lo:[1,0,0] neg_hi:[1,0,0]
	v_pk_fma_f32 v[0:1], v[88:89], v[0:1], v[64:65] op_sel:[1,0,0]
	s_nop 0
	v_cvt_pk_f16_f32 v23, v0, v1
	v_pk_fma_f32 v[0:1], v[88:89], v[50:51], v[18:19] op_sel_hi:[0,1,1] neg_lo:[1,0,0] neg_hi:[1,0,0]
	v_pk_fma_f32 v[0:1], v[88:89], v[0:1], v[54:55] op_sel:[1,0,0]
	s_nop 0
	v_cvt_pk_f16_f32 v24, v0, v1
	v_pk_fma_f32 v[0:1], v[88:89], v[52:53], v[20:21] op_sel_hi:[0,1,1] neg_lo:[1,0,0] neg_hi:[1,0,0]
	v_pk_fma_f32 v[0:1], v[88:89], v[0:1], v[56:57] op_sel:[1,0,0]
	s_nop 0
	v_cvt_pk_f16_f32 v25, v0, v1
	v_pk_fma_f32 v[0:1], v[88:89], v[42:43], v[30:31] op_sel_hi:[0,1,1] neg_lo:[1,0,0] neg_hi:[1,0,0]
	v_pk_fma_f32 v[0:1], v[88:89], v[0:1], v[46:47] op_sel:[1,0,0]
	buffer_store_dwordx4 v[22:25], v66, s[8:11], 0 offen sc1
	v_cvt_pk_f16_f32 v18, v0, v1
	v_pk_fma_f32 v[0:1], v[88:89], v[44:45], v[32:33] op_sel_hi:[0,1,1] neg_lo:[1,0,0] neg_hi:[1,0,0]
	v_pk_fma_f32 v[0:1], v[88:89], v[0:1], v[48:49] op_sel:[1,0,0]
	s_nop 0
	v_cvt_pk_f16_f32 v19, v0, v1
	v_pk_fma_f32 v[0:1], v[88:89], v[34:35], v[26:27] op_sel_hi:[0,1,1] neg_lo:[1,0,0] neg_hi:[1,0,0]
	v_pk_fma_f32 v[0:1], v[88:89], v[0:1], v[38:39] op_sel:[1,0,0]
	s_nop 0
	v_cvt_pk_f16_f32 v20, v0, v1
	v_pk_fma_f32 v[0:1], v[88:89], v[36:37], v[28:29] op_sel_hi:[0,1,1] neg_lo:[1,0,0] neg_hi:[1,0,0]
	v_pk_fma_f32 v[0:1], v[88:89], v[0:1], v[40:41] op_sel:[1,0,0]
	s_nop 0
	v_cvt_pk_f16_f32 v21, v0, v1
	v_add_u32_e32 v0, 0xb0, v167
	buffer_store_dwordx4 v[18:21], v66, s[8:11], 0 offen offset:256 sc1
	s_nop 1
	v_mul_lo_u32 v18, v0, s6
	v_pk_fma_f32 v[0:1], v[152:153], v[58:59], v[14:15] op_sel_hi:[0,1,1] neg_lo:[1,0,0] neg_hi:[1,0,0]
	v_pk_fma_f32 v[0:1], v[152:153], v[0:1], v[62:63] op_sel:[1,0,0]
	s_nop 0
	v_cvt_pk_f16_f32 v14, v0, v1
	v_pk_fma_f32 v[0:1], v[152:153], v[60:61], v[16:17] op_sel_hi:[0,1,1] neg_lo:[1,0,0] neg_hi:[1,0,0]
	v_pk_fma_f32 v[0:1], v[152:153], v[0:1], v[64:65] op_sel:[1,0,0]
	s_nop 0
	v_cvt_pk_f16_f32 v15, v0, v1
	v_pk_fma_f32 v[0:1], v[152:153], v[50:51], v[6:7] op_sel_hi:[0,1,1] neg_lo:[1,0,0] neg_hi:[1,0,0]
	v_pk_fma_f32 v[0:1], v[152:153], v[0:1], v[54:55] op_sel:[1,0,0]
	v_pk_fma_f32 v[6:7], v[152:153], v[44:45], v[12:13] op_sel_hi:[0,1,1] neg_lo:[1,0,0] neg_hi:[1,0,0]
	v_cvt_pk_f16_f32 v16, v0, v1
	v_pk_fma_f32 v[0:1], v[152:153], v[52:53], v[8:9] op_sel_hi:[0,1,1] neg_lo:[1,0,0] neg_hi:[1,0,0]
	v_pk_fma_f32 v[0:1], v[152:153], v[0:1], v[56:57] op_sel:[1,0,0]
	v_pk_fma_f32 v[6:7], v[152:153], v[6:7], v[48:49] op_sel:[1,0,0]
	v_cvt_pk_f16_f32 v17, v0, v1
	v_pk_fma_f32 v[0:1], v[152:153], v[42:43], v[10:11] op_sel_hi:[0,1,1] neg_lo:[1,0,0] neg_hi:[1,0,0]
	v_pk_fma_f32 v[0:1], v[152:153], v[0:1], v[46:47] op_sel:[1,0,0]
	v_add_lshl_u32 v8, v166, v18, 1
	v_cvt_pk_f16_f32 v0, v0, v1
	v_cvt_pk_f16_f32 v1, v6, v7
	buffer_store_dwordx4 v[14:17], v8, s[8:11], 0 offen sc1
	buffer_store_dwordx4 v[0:3], v8, s[8:11], 0 offen offset:256 sc1
	s_endpgm

.LBB8_6:
	s_or_b64 exec, exec, s[2:3]
	s_add_i32 s0, 0, 0x18000
	v_add_u32_e32 v48, s0, v38
	s_mov_b64 s[0:1], 0x80
	v_readfirstlane_b32 s22, v48
	v_add_u32_e32 v49, 0x2000, v48
	v_lshl_add_u64 v[2:3], v[30:31], 0, s[0:1]
	s_mov_b32 m0, s22
	v_readfirstlane_b32 s21, v49
	v_add_u32_e32 v46, 0x8000, v35
	s_waitcnt vmcnt(4)
	s_barrier
	global_load_lds_dwordx4 v[2:3], off
	v_lshl_add_u64 v[2:3], v[32:33], 0, s[0:1]
	s_mov_b32 m0, s21
	v_readfirstlane_b32 s19, v46
	v_add_u32_e32 v47, 0xa000, v35
	s_add_i32 s2, 0, 0x1c000
	global_load_lds_dwordx4 v[2:3], off
	v_lshl_add_u64 v[2:3], v[26:27], 0, s[0:1]
	s_mov_b32 m0, s19
	v_readfirstlane_b32 s16, v47
	v_add_u32_e32 v37, s2, v38
	global_load_lds_dwordx4 v[2:3], off
	v_lshl_add_u64 v[2:3], v[28:29], 0, s[0:1]
	s_mov_b32 m0, s16
	v_readfirstlane_b32 s3, v37
	v_add_u32_e32 v39, 0x2000, v37
	global_load_lds_dwordx4 v[2:3], off
	v_lshl_add_u64 v[2:3], v[22:23], 0, s[0:1]
	s_mov_b32 m0, s3
	v_readfirstlane_b32 s2, v39
	global_load_lds_dwordx4 v[2:3], off
	v_lshl_add_u64 v[2:3], v[24:25], 0, s[0:1]
	s_mov_b32 m0, s2
	v_lshlrev_b32_e32 v1, 6, v0
	global_load_lds_dwordx4 v[2:3], off
	v_lshlrev_b32_e32 v4, 2, v0
	v_and_b32_e32 v2, 0x3c0, v1
	v_and_b32_e32 v3, 48, v0
	v_and_b32_e32 v4, 32, v4
	v_bitop3_b32 v6, v2, v4, v3 bitop3:0x36
	v_and_b32_e32 v1, 0x3000, v1
	v_add3_u32 v234, 0, v1, v6
	v_add_u32_e32 v2, 0x10000, v234
	v_add_u32_e32 v4, 0x10800, v234
	s_waitcnt vmcnt(6)
	s_barrier
	v_add_u32_e32 v3, 0x10400, v234
	ds_read_b128 v[10:13], v2
	ds_read_b128 v[14:17], v3
	v_add_u32_e32 v5, 0x10c00, v234
	ds_read_b128 v[50:53], v4
	ds_read_b128 v[54:57], v5
	v_lshlrev_b32_e32 v1, 5, v0
	v_and_b32_e32 v1, 0x2000, v1
	v_add3_u32 v1, 0, v1, v6
	v_add_u32_e32 v38, 0xc000, v35
	v_add_u32_e32 v40, 0xe000, v35
	v_readfirstlane_b32 s7, v38
	v_lshl_add_u64 v[6:7], v[18:19], 0, s[0:1]
	s_mov_b32 m0, s7
	v_readfirstlane_b32 s4, v40
	global_load_lds_dwordx4 v[6:7], off
	v_lshl_add_u64 v[6:7], v[20:21], 0, s[0:1]
	s_mov_b32 m0, s4
	s_nop 0
	global_load_lds_dwordx4 v[6:7], off
	ds_read_b128 v[42:45], v1
	ds_read_b128 v[58:61], v1 offset:1024
	ds_read_b128 v[62:65], v1 offset:2048
	ds_read_b128 v[66:69], v1 offset:3072
	ds_read_b128 v[70:73], v1 offset:4096
	ds_read_b128 v[74:77], v1 offset:5120
	ds_read_b128 v[78:81], v1 offset:6144
	ds_read_b128 v[82:85], v1 offset:7168
	s_waitcnt lgkmcnt(8)
	s_barrier
	s_waitcnt lgkmcnt(0)
	s_setprio 1
	s_waitcnt lgkmcnt(0)
	v_mfma_f32_16x16x32_f16 v[6:9], v[10:13], v[42:45], 0
	v_mfma_f32_16x16x32_f16 v[86:89], v[14:17], v[58:61], v[6:9]
	v_mfma_f32_16x16x32_f16 v[6:9], v[50:53], v[42:45], 0
	v_mfma_f32_16x16x32_f16 v[90:93], v[54:57], v[58:61], v[6:9]
	v_mfma_f32_16x16x32_f16 v[6:9], v[10:13], v[62:65], 0
	v_mfma_f32_16x16x32_f16 v[94:97], v[14:17], v[66:69], v[6:9]
	v_mfma_f32_16x16x32_f16 v[6:9], v[50:53], v[62:65], 0
	v_mfma_f32_16x16x32_f16 v[98:101], v[54:57], v[66:69], v[6:9]
	v_mfma_f32_16x16x32_f16 v[6:9], v[10:13], v[70:73], 0
	v_mfma_f32_16x16x32_f16 v[102:105], v[14:17], v[74:77], v[6:9]
	v_mfma_f32_16x16x32_f16 v[6:9], v[50:53], v[70:73], 0
	v_mfma_f32_16x16x32_f16 v[106:109], v[54:57], v[74:77], v[6:9]
	v_mfma_f32_16x16x32_f16 v[6:9], v[10:13], v[78:81], 0
	v_mfma_f32_16x16x32_f16 v[110:113], v[14:17], v[82:85], v[6:9]
	v_mfma_f32_16x16x32_f16 v[6:9], v[50:53], v[78:81], 0
	v_mfma_f32_16x16x32_f16 v[114:117], v[54:57], v[82:85], v[6:9]
	s_setprio 0
	s_barrier
	s_mov_b64 s[0:1], 0x100
	v_readfirstlane_b32 s15, v36
	v_add_u32_e32 v41, 0x2000, v36
	s_nop 1
	v_add_u32_e32 v6, 0x14000, v234
	v_add_u32_e32 v8, 0x14800, v234
	v_lshl_add_u64 v[134:135], v[30:31], 0, s[0:1]
	s_mov_b32 m0, s15
	v_readfirstlane_b32 s5, v41
	v_add_u32_e32 v7, 0x14400, v234
	ds_read_b128 v[118:121], v6
	ds_read_b128 v[122:125], v7
	v_add_u32_e32 v9, 0x14c00, v234
	ds_read_b128 v[126:129], v8
	ds_read_b128 v[130:133], v9
	global_load_lds_dwordx4 v[134:135], off
	v_lshl_add_u64 v[134:135], v[32:33], 0, s[0:1]
	s_mov_b32 m0, s5
	s_nop 0
	global_load_lds_dwordx4 v[134:135], off
	s_barrier
	s_waitcnt lgkmcnt(0)
	s_setprio 1
	s_waitcnt lgkmcnt(0)
	v_mfma_f32_16x16x32_f16 v[134:137], v[118:121], v[42:45], 0
	v_mfma_f32_16x16x32_f16 v[42:45], v[126:129], v[42:45], 0
	v_mfma_f32_16x16x32_f16 v[134:137], v[122:125], v[58:61], v[134:137]
	v_mfma_f32_16x16x32_f16 v[58:61], v[130:133], v[58:61], v[42:45]
	v_mfma_f32_16x16x32_f16 v[42:45], v[118:121], v[62:65], 0
	v_mfma_f32_16x16x32_f16 v[138:141], v[122:125], v[66:69], v[42:45]
	v_mfma_f32_16x16x32_f16 v[42:45], v[126:129], v[62:65], 0
	v_mfma_f32_16x16x32_f16 v[62:65], v[130:133], v[66:69], v[42:45]
	v_mfma_f32_16x16x32_f16 v[42:45], v[118:121], v[70:73], 0
	v_mfma_f32_16x16x32_f16 v[66:69], v[122:125], v[74:77], v[42:45]
	v_mfma_f32_16x16x32_f16 v[42:45], v[126:129], v[70:73], 0
	v_mfma_f32_16x16x32_f16 v[70:73], v[130:133], v[74:77], v[42:45]
	v_mfma_f32_16x16x32_f16 v[42:45], v[118:121], v[78:81], 0
	v_mfma_f32_16x16x32_f16 v[74:77], v[122:125], v[82:85], v[42:45]
	v_mfma_f32_16x16x32_f16 v[42:45], v[126:129], v[78:81], 0
	v_mfma_f32_16x16x32_f16 v[78:81], v[130:133], v[82:85], v[42:45]
	s_setprio 0
	v_readfirstlane_b32 s17, v35
	s_nop 4
	v_lshl_add_u64 v[42:43], v[26:27], 0, s[0:1]
	s_mov_b32 m0, s17
	s_barrier
	ds_read_b128 v[82:85], v1 offset:16384
	ds_read_b128 v[142:145], v1 offset:17408
	ds_read_b128 v[146:149], v1 offset:18432
	ds_read_b128 v[150:153], v1 offset:19456
	ds_read_b128 v[154:157], v1 offset:20480
	ds_read_b128 v[158:161], v1 offset:21504
	ds_read_b128 v[162:165], v1 offset:22528
	ds_read_b128 v[166:169], v1 offset:23552
	global_load_lds_dwordx4 v[42:43], off
	v_add_u32_e32 v42, 0x2000, v35
	v_lshl_add_u64 v[44:45], v[28:29], 0, s[0:1]
	v_readfirstlane_b32 s10, v42
	s_mov_b32 m0, s10
	s_nop 0
	global_load_lds_dwordx4 v[44:45], off
	s_barrier
	s_waitcnt lgkmcnt(0)
	s_setprio 1
	s_waitcnt lgkmcnt(0)
	v_mfma_f32_16x16x32_f16 v[170:173], v[10:13], v[82:85], 0
	v_mfma_f32_16x16x32_f16 v[178:181], v[10:13], v[146:149], 0
	v_mfma_f32_16x16x32_f16 v[186:189], v[10:13], v[154:157], 0
	v_mfma_f32_16x16x32_f16 v[10:13], v[10:13], v[162:165], 0
	v_mfma_f32_16x16x32_f16 v[194:197], v[14:17], v[166:169], v[10:13]
	v_mfma_f32_16x16x32_f16 v[10:13], v[50:53], v[162:165], 0
	v_mfma_f32_16x16x32_f16 v[174:177], v[50:53], v[82:85], 0
	v_mfma_f32_16x16x32_f16 v[182:185], v[50:53], v[146:149], 0
	v_mfma_f32_16x16x32_f16 v[190:193], v[50:53], v[154:157], 0
	v_mfma_f32_16x16x32_f16 v[50:53], v[54:57], v[166:169], v[10:13]
	v_mfma_f32_16x16x32_f16 v[170:173], v[14:17], v[142:145], v[170:173]
	v_mfma_f32_16x16x32_f16 v[174:177], v[54:57], v[142:145], v[174:177]
	v_mfma_f32_16x16x32_f16 v[178:181], v[14:17], v[150:153], v[178:181]
	v_mfma_f32_16x16x32_f16 v[182:185], v[54:57], v[150:153], v[182:185]
	v_mfma_f32_16x16x32_f16 v[186:189], v[14:17], v[158:161], v[186:189]
	v_mfma_f32_16x16x32_f16 v[190:193], v[54:57], v[158:161], v[190:193]
	s_setprio 0
	s_barrier
	v_readfirstlane_b32 s14, v34
	v_add_u32_e32 v43, 0x2000, v34
	v_lshl_add_u64 v[10:11], v[22:23], 0, s[0:1]
	s_mov_b32 m0, s14
	v_readfirstlane_b32 s11, v43
	global_load_lds_dwordx4 v[10:11], off
	v_lshl_add_u64 v[10:11], v[24:25], 0, s[0:1]
	s_mov_b32 m0, s11
	s_nop 0
	global_load_lds_dwordx4 v[10:11], off
	s_waitcnt vmcnt(6)
	s_barrier
	s_setprio 1
	v_mfma_f32_16x16x32_f16 v[10:13], v[118:121], v[82:85], 0
	v_mfma_f32_16x16x32_f16 v[54:57], v[122:125], v[142:145], v[10:13]
	v_mfma_f32_16x16x32_f16 v[10:13], v[126:129], v[82:85], 0
	v_mfma_f32_16x16x32_f16 v[82:85], v[130:133], v[142:145], v[10:13]
	v_mfma_f32_16x16x32_f16 v[10:13], v[118:121], v[146:149], 0
	v_mfma_f32_16x16x32_f16 v[142:145], v[122:125], v[150:153], v[10:13]
	v_mfma_f32_16x16x32_f16 v[10:13], v[126:129], v[146:149], 0
	v_mfma_f32_16x16x32_f16 v[146:149], v[130:133], v[150:153], v[10:13]
	v_mfma_f32_16x16x32_f16 v[10:13], v[118:121], v[154:157], 0
	v_mfma_f32_16x16x32_f16 v[150:153], v[122:125], v[158:161], v[10:13]
	v_mfma_f32_16x16x32_f16 v[10:13], v[126:129], v[154:157], 0
	v_mfma_f32_16x16x32_f16 v[154:157], v[130:133], v[158:161], v[10:13]
	v_mfma_f32_16x16x32_f16 v[10:13], v[118:121], v[162:165], 0
	v_mfma_f32_16x16x32_f16 v[118:121], v[122:125], v[166:169], v[10:13]
	v_mfma_f32_16x16x32_f16 v[10:13], v[126:129], v[162:165], 0
	v_mfma_f32_16x16x32_f16 v[122:125], v[130:133], v[166:169], v[10:13]
	s_setprio 0
	s_nop 5
	v_add_u32_e32 v10, 0x18000, v234
	v_add_u32_e32 v12, 0x18800, v234
	s_barrier
	v_add_u32_e32 v11, 0x18400, v234
	ds_read_b128 v[126:129], v10
	ds_read_b128 v[130:133], v11
	v_add_u32_e32 v13, 0x18c00, v234
	ds_read_b128 v[158:161], v12
	ds_read_b128 v[162:165], v13
	v_add_u32_e32 v44, 0x4000, v35
	v_add_u32_e32 v45, 0x6000, v35
	v_readfirstlane_b32 s20, v44
	v_lshl_add_u64 v[14:15], v[18:19], 0, s[0:1]
	s_mov_b32 m0, s20
	v_readfirstlane_b32 s18, v45
	ds_read_b128 v[166:169], v1 offset:32768
	ds_read_b128 v[198:201], v1 offset:33792
	ds_read_b128 v[202:205], v1 offset:34816
	ds_read_b128 v[206:209], v1 offset:35840
	ds_read_b128 v[210:213], v1 offset:36864
	ds_read_b128 v[214:217], v1 offset:37888
	ds_read_b128 v[218:221], v1 offset:38912
	ds_read_b128 v[222:225], v1 offset:39936
	global_load_lds_dwordx4 v[14:15], off
	v_lshl_add_u64 v[14:15], v[20:21], 0, s[0:1]
	s_mov_b32 m0, s18
	s_nop 0
	global_load_lds_dwordx4 v[14:15], off
	s_waitcnt lgkmcnt(8)
	s_barrier
	s_waitcnt lgkmcnt(0)
	s_setprio 1
	s_waitcnt lgkmcnt(0)
	v_mfma_f32_16x16x32_f16 v[14:17], v[126:129], v[166:169], v[86:89]
	v_mfma_f32_16x16x32_f16 v[86:89], v[130:133], v[198:201], v[14:17]
	v_mfma_f32_16x16x32_f16 v[14:17], v[158:161], v[166:169], v[90:93]
	v_mfma_f32_16x16x32_f16 v[90:93], v[162:165], v[198:201], v[14:17]
	v_mfma_f32_16x16x32_f16 v[14:17], v[126:129], v[202:205], v[94:97]
	v_mfma_f32_16x16x32_f16 v[94:97], v[130:133], v[206:209], v[14:17]
	v_mfma_f32_16x16x32_f16 v[14:17], v[158:161], v[202:205], v[98:101]
	v_mfma_f32_16x16x32_f16 v[98:101], v[162:165], v[206:209], v[14:17]
	v_mfma_f32_16x16x32_f16 v[14:17], v[126:129], v[210:213], v[102:105]
	v_mfma_f32_16x16x32_f16 v[102:105], v[130:133], v[214:217], v[14:17]
	v_mfma_f32_16x16x32_f16 v[14:17], v[158:161], v[210:213], v[106:109]
	v_mfma_f32_16x16x32_f16 v[106:109], v[162:165], v[214:217], v[14:17]
	v_mfma_f32_16x16x32_f16 v[14:17], v[126:129], v[218:221], v[110:113]
	v_mfma_f32_16x16x32_f16 v[110:113], v[130:133], v[222:225], v[14:17]
	v_mfma_f32_16x16x32_f16 v[14:17], v[158:161], v[218:221], v[114:117]
	v_mfma_f32_16x16x32_f16 v[114:117], v[162:165], v[222:225], v[14:17]
	s_setprio 0
	s_barrier
	s_mov_b64 s[0:1], 0x180
	s_mov_b32 m0, s22
	s_nop 2
	v_add_u32_e32 v14, 0x1c000, v234
	v_add_u32_e32 v16, 0x1c800, v234
	v_lshl_add_u64 v[242:243], v[30:31], 0, s[0:1]
	v_add_u32_e32 v15, 0x1c400, v234
	ds_read_b128 v[226:229], v14
	ds_read_b128 v[230:233], v15
	v_add_u32_e32 v17, 0x1cc00, v234
	ds_read_b128 v[234:237], v16
	ds_read_b128 v[238:241], v17
	global_load_lds_dwordx4 v[242:243], off
	v_lshl_add_u64 v[242:243], v[32:33], 0, s[0:1]
	s_mov_b32 m0, s21
	s_nop 0
	global_load_lds_dwordx4 v[242:243], off
	s_barrier
	s_waitcnt lgkmcnt(0)
	s_setprio 1
	s_waitcnt lgkmcnt(0)
	v_mfma_f32_16x16x32_f16 v[134:137], v[226:229], v[166:169], v[134:137]
	v_mfma_f32_16x16x32_f16 v[58:61], v[234:237], v[166:169], v[58:61]
	v_mfma_f32_16x16x32_f16 v[138:141], v[226:229], v[202:205], v[138:141]
	v_mfma_f32_16x16x32_f16 v[62:65], v[234:237], v[202:205], v[62:65]
	v_mfma_f32_16x16x32_f16 v[66:69], v[226:229], v[210:213], v[66:69]
	v_mfma_f32_16x16x32_f16 v[70:73], v[234:237], v[210:213], v[70:73]
	v_mfma_f32_16x16x32_f16 v[74:77], v[226:229], v[218:221], v[74:77]
	v_mfma_f32_16x16x32_f16 v[78:81], v[234:237], v[218:221], v[78:81]
	v_mfma_f32_16x16x32_f16 v[134:137], v[230:233], v[198:201], v[134:137]
	v_mfma_f32_16x16x32_f16 v[58:61], v[238:241], v[198:201], v[58:61]
	v_mfma_f32_16x16x32_f16 v[138:141], v[230:233], v[206:209], v[138:141]
	v_mfma_f32_16x16x32_f16 v[62:65], v[238:241], v[206:209], v[62:65]
	v_mfma_f32_16x16x32_f16 v[66:69], v[230:233], v[214:217], v[66:69]
	v_mfma_f32_16x16x32_f16 v[70:73], v[238:241], v[214:217], v[70:73]
	v_mfma_f32_16x16x32_f16 v[74:77], v[230:233], v[222:225], v[74:77]
	v_mfma_f32_16x16x32_f16 v[78:81], v[238:241], v[222:225], v[78:81]
	s_setprio 0
	s_mov_b32 m0, s19
	v_lshl_add_u64 v[242:243], v[26:27], 0, s[0:1]
	s_barrier
	ds_read_b128 v[166:169], v1 offset:49152
	ds_read_b128 v[198:201], v1 offset:50176
	ds_read_b128 v[202:205], v1 offset:51200
	ds_read_b128 v[206:209], v1 offset:52224
	ds_read_b128 v[210:213], v1 offset:53248
	ds_read_b128 v[214:217], v1 offset:54272
	ds_read_b128 v[218:221], v1 offset:55296
	ds_read_b128 v[222:225], v1 offset:56320
	global_load_lds_dwordx4 v[242:243], off
	v_lshl_add_u64 v[242:243], v[28:29], 0, s[0:1]
	s_mov_b32 m0, s16
	s_nop 0
	global_load_lds_dwordx4 v[242:243], off
	s_barrier
	s_waitcnt lgkmcnt(0)
	s_setprio 1
	s_waitcnt lgkmcnt(0)
	v_mfma_f32_16x16x32_f16 v[170:173], v[126:129], v[166:169], v[170:173]
	v_mfma_f32_16x16x32_f16 v[178:181], v[126:129], v[202:205], v[178:181]
	v_mfma_f32_16x16x32_f16 v[186:189], v[126:129], v[210:213], v[186:189]
	v_mfma_f32_16x16x32_f16 v[126:129], v[126:129], v[218:221], v[194:197]
	v_mfma_f32_16x16x32_f16 v[50:53], v[158:161], v[218:221], v[50:53]
	v_mfma_f32_16x16x32_f16 v[174:177], v[158:161], v[166:169], v[174:177]
	v_mfma_f32_16x16x32_f16 v[182:185], v[158:161], v[202:205], v[182:185]
	v_mfma_f32_16x16x32_f16 v[190:193], v[158:161], v[210:213], v[190:193]
	v_mfma_f32_16x16x32_f16 v[126:129], v[130:133], v[222:225], v[126:129]
	v_mfma_f32_16x16x32_f16 v[50:53], v[162:165], v[222:225], v[50:53]
	v_mfma_f32_16x16x32_f16 v[170:173], v[130:133], v[198:201], v[170:173]
	v_mfma_f32_16x16x32_f16 v[174:177], v[162:165], v[198:201], v[174:177]
	v_mfma_f32_16x16x32_f16 v[178:181], v[130:133], v[206:209], v[178:181]
	v_mfma_f32_16x16x32_f16 v[182:185], v[162:165], v[206:209], v[182:185]
	v_mfma_f32_16x16x32_f16 v[186:189], v[130:133], v[214:217], v[186:189]
	v_mfma_f32_16x16x32_f16 v[190:193], v[162:165], v[214:217], v[190:193]
	s_setprio 0
	s_barrier
	s_mov_b32 m0, s3
	v_lshl_add_u64 v[130:131], v[22:23], 0, s[0:1]
	global_load_lds_dwordx4 v[130:131], off
	v_lshl_add_u64 v[130:131], v[24:25], 0, s[0:1]
	s_mov_b32 m0, s2
	s_nop 0
	global_load_lds_dwordx4 v[130:131], off
	s_waitcnt vmcnt(6)
	s_barrier
	s_setprio 1
	v_mfma_f32_16x16x32_f16 v[82:85], v[234:237], v[166:169], v[82:85]
	v_mfma_f32_16x16x32_f16 v[130:133], v[226:229], v[202:205], v[142:145]
	v_mfma_f32_16x16x32_f16 v[142:145], v[234:237], v[202:205], v[146:149]
	v_mfma_f32_16x16x32_f16 v[146:149], v[226:229], v[210:213], v[150:153]
	v_mfma_f32_16x16x32_f16 v[150:153], v[234:237], v[210:213], v[154:157]
	v_mfma_f32_16x16x32_f16 v[118:121], v[226:229], v[218:221], v[118:121]
	v_mfma_f32_16x16x32_f16 v[122:125], v[234:237], v[218:221], v[122:125]
	v_mfma_f32_16x16x32_f16 v[54:57], v[226:229], v[166:169], v[54:57]
	v_mfma_f32_16x16x32_f16 v[82:85], v[238:241], v[198:201], v[82:85]
	v_mfma_f32_16x16x32_f16 v[130:133], v[230:233], v[206:209], v[130:133]
	v_mfma_f32_16x16x32_f16 v[142:145], v[238:241], v[206:209], v[142:145]
	v_mfma_f32_16x16x32_f16 v[146:149], v[230:233], v[214:217], v[146:149]
	v_mfma_f32_16x16x32_f16 v[150:153], v[238:241], v[214:217], v[150:153]
	v_mfma_f32_16x16x32_f16 v[118:121], v[230:233], v[222:225], v[118:121]
	v_mfma_f32_16x16x32_f16 v[122:125], v[238:241], v[222:225], v[122:125]
	v_mfma_f32_16x16x32_f16 v[54:57], v[230:233], v[198:201], v[54:57]
	s_setprio 0
	s_barrier
	ds_read_b128 v[154:157], v2
	ds_read_b128 v[158:161], v3
	ds_read_b128 v[162:165], v4
	ds_read_b128 v[166:169], v5
	s_mov_b32 m0, s7
	v_lshl_add_u64 v[194:195], v[18:19], 0, s[0:1]
	global_load_lds_dwordx4 v[194:195], off
	v_lshl_add_u64 v[194:195], v[20:21], 0, s[0:1]
	s_mov_b32 m0, s4
	s_nop 0
	global_load_lds_dwordx4 v[194:195], off
	ds_read_b128 v[194:197], v1
	ds_read_b128 v[198:201], v1 offset:1024
	ds_read_b128 v[202:205], v1 offset:2048
	ds_read_b128 v[206:209], v1 offset:3072
	ds_read_b128 v[210:213], v1 offset:4096
	ds_read_b128 v[214:217], v1 offset:5120
	ds_read_b128 v[218:221], v1 offset:6144
	ds_read_b128 v[222:225], v1 offset:7168
	s_waitcnt lgkmcnt(8)
	s_barrier
	s_waitcnt lgkmcnt(0)
	s_setprio 1
	s_waitcnt lgkmcnt(0)
	v_mfma_f32_16x16x32_f16 v[86:89], v[154:157], v[194:197], v[86:89]
	v_mfma_f32_16x16x32_f16 v[90:93], v[162:165], v[194:197], v[90:93]
	v_mfma_f32_16x16x32_f16 v[94:97], v[154:157], v[202:205], v[94:97]
	v_mfma_f32_16x16x32_f16 v[98:101], v[162:165], v[202:205], v[98:101]
	v_mfma_f32_16x16x32_f16 v[102:105], v[154:157], v[210:213], v[102:105]
	v_mfma_f32_16x16x32_f16 v[106:109], v[162:165], v[210:213], v[106:109]
	v_mfma_f32_16x16x32_f16 v[110:113], v[154:157], v[218:221], v[110:113]
	v_mfma_f32_16x16x32_f16 v[86:89], v[158:161], v[198:201], v[86:89]
	v_mfma_f32_16x16x32_f16 v[90:93], v[166:169], v[198:201], v[90:93]
	v_mfma_f32_16x16x32_f16 v[94:97], v[158:161], v[206:209], v[94:97]
	v_mfma_f32_16x16x32_f16 v[98:101], v[166:169], v[206:209], v[98:101]
	v_mfma_f32_16x16x32_f16 v[102:105], v[158:161], v[214:217], v[102:105]
	v_mfma_f32_16x16x32_f16 v[106:109], v[166:169], v[214:217], v[106:109]
	v_mfma_f32_16x16x32_f16 v[110:113], v[158:161], v[222:225], v[110:113]
	v_mfma_f32_16x16x32_f16 v[114:117], v[162:165], v[218:221], v[114:117]
	v_mfma_f32_16x16x32_f16 v[114:117], v[166:169], v[222:225], v[114:117]
	s_setprio 0
	s_barrier
	s_mov_b64 s[0:1], 0x200
	s_mov_b32 m0, s15
	v_lshl_add_u64 v[242:243], v[30:31], 0, s[0:1]
	ds_read_b128 v[226:229], v6
	ds_read_b128 v[230:233], v7
	ds_read_b128 v[234:237], v8
	ds_read_b128 v[238:241], v9
	global_load_lds_dwordx4 v[242:243], off
	v_lshl_add_u64 v[242:243], v[32:33], 0, s[0:1]
	s_mov_b32 m0, s5
	s_nop 0
	global_load_lds_dwordx4 v[242:243], off
	s_barrier
	s_waitcnt lgkmcnt(0)
	s_setprio 1
	s_waitcnt lgkmcnt(0)
	v_mfma_f32_16x16x32_f16 v[134:137], v[226:229], v[194:197], v[134:137]
	v_mfma_f32_16x16x32_f16 v[58:61], v[234:237], v[194:197], v[58:61]
	v_mfma_f32_16x16x32_f16 v[138:141], v[226:229], v[202:205], v[138:141]
	v_mfma_f32_16x16x32_f16 v[62:65], v[234:237], v[202:205], v[62:65]
	v_mfma_f32_16x16x32_f16 v[66:69], v[226:229], v[210:213], v[66:69]
	v_mfma_f32_16x16x32_f16 v[70:73], v[234:237], v[210:213], v[70:73]
	v_mfma_f32_16x16x32_f16 v[74:77], v[226:229], v[218:221], v[74:77]
	v_mfma_f32_16x16x32_f16 v[78:81], v[234:237], v[218:221], v[78:81]
	v_mfma_f32_16x16x32_f16 v[134:137], v[230:233], v[198:201], v[134:137]
	v_mfma_f32_16x16x32_f16 v[58:61], v[238:241], v[198:201], v[58:61]
	v_mfma_f32_16x16x32_f16 v[138:141], v[230:233], v[206:209], v[138:141]
	v_mfma_f32_16x16x32_f16 v[62:65], v[238:241], v[206:209], v[62:65]
	v_mfma_f32_16x16x32_f16 v[66:69], v[230:233], v[214:217], v[66:69]
	v_mfma_f32_16x16x32_f16 v[70:73], v[238:241], v[214:217], v[70:73]
	v_mfma_f32_16x16x32_f16 v[74:77], v[230:233], v[222:225], v[74:77]
	v_mfma_f32_16x16x32_f16 v[78:81], v[238:241], v[222:225], v[78:81]
	s_setprio 0
	s_mov_b32 m0, s17
	v_lshl_add_u64 v[242:243], v[26:27], 0, s[0:1]
	s_barrier
	ds_read_b128 v[194:197], v1 offset:16384
	ds_read_b128 v[198:201], v1 offset:17408
	ds_read_b128 v[202:205], v1 offset:18432
	ds_read_b128 v[206:209], v1 offset:19456
	ds_read_b128 v[210:213], v1 offset:20480
	ds_read_b128 v[214:217], v1 offset:21504
	ds_read_b128 v[218:221], v1 offset:22528
	ds_read_b128 v[222:225], v1 offset:23552
	global_load_lds_dwordx4 v[242:243], off
	v_lshl_add_u64 v[242:243], v[28:29], 0, s[0:1]
	s_mov_b32 m0, s10
	s_nop 0
	global_load_lds_dwordx4 v[242:243], off
	s_barrier
	s_waitcnt lgkmcnt(0)
	s_setprio 1
	s_waitcnt lgkmcnt(0)
	v_mfma_f32_16x16x32_f16 v[126:129], v[154:157], v[218:221], v[126:129]
	v_mfma_f32_16x16x32_f16 v[50:53], v[162:165], v[218:221], v[50:53]
	v_mfma_f32_16x16x32_f16 v[170:173], v[154:157], v[194:197], v[170:173]
	v_mfma_f32_16x16x32_f16 v[174:177], v[162:165], v[194:197], v[174:177]
	v_mfma_f32_16x16x32_f16 v[178:181], v[154:157], v[202:205], v[178:181]
	v_mfma_f32_16x16x32_f16 v[182:185], v[162:165], v[202:205], v[182:185]
	v_mfma_f32_16x16x32_f16 v[186:189], v[154:157], v[210:213], v[186:189]
	v_mfma_f32_16x16x32_f16 v[190:193], v[162:165], v[210:213], v[190:193]
	v_mfma_f32_16x16x32_f16 v[126:129], v[158:161], v[222:225], v[126:129]
	v_mfma_f32_16x16x32_f16 v[50:53], v[166:169], v[222:225], v[50:53]
	v_mfma_f32_16x16x32_f16 v[170:173], v[158:161], v[198:201], v[170:173]
	v_mfma_f32_16x16x32_f16 v[174:177], v[166:169], v[198:201], v[174:177]
	v_mfma_f32_16x16x32_f16 v[178:181], v[158:161], v[206:209], v[178:181]
	v_mfma_f32_16x16x32_f16 v[182:185], v[166:169], v[206:209], v[182:185]
	v_mfma_f32_16x16x32_f16 v[186:189], v[158:161], v[214:217], v[186:189]
	v_mfma_f32_16x16x32_f16 v[190:193], v[166:169], v[214:217], v[190:193]
	s_setprio 0
	s_barrier
	s_mov_b32 m0, s14
	v_lshl_add_u64 v[154:155], v[22:23], 0, s[0:1]
	global_load_lds_dwordx4 v[154:155], off
	v_lshl_add_u64 v[154:155], v[24:25], 0, s[0:1]
	s_mov_b32 m0, s11
	s_nop 0
	global_load_lds_dwordx4 v[154:155], off
	s_waitcnt vmcnt(6)
	s_barrier
	s_setprio 1
	v_mfma_f32_16x16x32_f16 v[82:85], v[234:237], v[194:197], v[82:85]
	v_mfma_f32_16x16x32_f16 v[130:133], v[226:229], v[202:205], v[130:133]
	v_mfma_f32_16x16x32_f16 v[142:145], v[234:237], v[202:205], v[142:145]
	v_mfma_f32_16x16x32_f16 v[146:149], v[226:229], v[210:213], v[146:149]
	v_mfma_f32_16x16x32_f16 v[150:153], v[234:237], v[210:213], v[150:153]
	v_mfma_f32_16x16x32_f16 v[118:121], v[226:229], v[218:221], v[118:121]
	v_mfma_f32_16x16x32_f16 v[122:125], v[234:237], v[218:221], v[122:125]
	v_mfma_f32_16x16x32_f16 v[54:57], v[226:229], v[194:197], v[54:57]
	v_mfma_f32_16x16x32_f16 v[82:85], v[238:241], v[198:201], v[82:85]
	v_mfma_f32_16x16x32_f16 v[130:133], v[230:233], v[206:209], v[130:133]
	v_mfma_f32_16x16x32_f16 v[142:145], v[238:241], v[206:209], v[142:145]
	v_mfma_f32_16x16x32_f16 v[146:149], v[230:233], v[214:217], v[146:149]
	v_mfma_f32_16x16x32_f16 v[150:153], v[238:241], v[214:217], v[150:153]
	v_mfma_f32_16x16x32_f16 v[118:121], v[230:233], v[222:225], v[118:121]
	v_mfma_f32_16x16x32_f16 v[122:125], v[238:241], v[222:225], v[122:125]
	v_mfma_f32_16x16x32_f16 v[54:57], v[230:233], v[198:201], v[54:57]
	s_setprio 0
	s_barrier
	ds_read_b128 v[154:157], v10
	ds_read_b128 v[158:161], v11
	ds_read_b128 v[162:165], v12
	ds_read_b128 v[166:169], v13
	s_mov_b32 m0, s20
	v_lshl_add_u64 v[226:227], v[18:19], 0, s[0:1]
	ds_read_b128 v[194:197], v1 offset:32768
	ds_read_b128 v[198:201], v1 offset:33792
	ds_read_b128 v[202:205], v1 offset:34816
	ds_read_b128 v[206:209], v1 offset:35840
	ds_read_b128 v[210:213], v1 offset:36864
	ds_read_b128 v[214:217], v1 offset:37888
	ds_read_b128 v[218:221], v1 offset:38912
	ds_read_b128 v[222:225], v1 offset:39936
	global_load_lds_dwordx4 v[226:227], off
	v_lshl_add_u64 v[226:227], v[20:21], 0, s[0:1]
	s_mov_b32 m0, s18
	s_nop 0
	global_load_lds_dwordx4 v[226:227], off
	s_waitcnt lgkmcnt(8)
	s_barrier
	s_waitcnt lgkmcnt(0)
	s_setprio 1
	s_waitcnt lgkmcnt(0)
	v_mfma_f32_16x16x32_f16 v[86:89], v[154:157], v[194:197], v[86:89]
	v_mfma_f32_16x16x32_f16 v[90:93], v[162:165], v[194:197], v[90:93]
	v_mfma_f32_16x16x32_f16 v[94:97], v[154:157], v[202:205], v[94:97]
	v_mfma_f32_16x16x32_f16 v[98:101], v[162:165], v[202:205], v[98:101]
	v_mfma_f32_16x16x32_f16 v[102:105], v[154:157], v[210:213], v[102:105]
	v_mfma_f32_16x16x32_f16 v[106:109], v[162:165], v[210:213], v[106:109]
	v_mfma_f32_16x16x32_f16 v[110:113], v[154:157], v[218:221], v[110:113]
	v_mfma_f32_16x16x32_f16 v[86:89], v[158:161], v[198:201], v[86:89]
	v_mfma_f32_16x16x32_f16 v[90:93], v[166:169], v[198:201], v[90:93]
	v_mfma_f32_16x16x32_f16 v[94:97], v[158:161], v[206:209], v[94:97]
	v_mfma_f32_16x16x32_f16 v[98:101], v[166:169], v[206:209], v[98:101]
	v_mfma_f32_16x16x32_f16 v[102:105], v[158:161], v[214:217], v[102:105]
	v_mfma_f32_16x16x32_f16 v[106:109], v[166:169], v[214:217], v[106:109]
	v_mfma_f32_16x16x32_f16 v[110:113], v[158:161], v[222:225], v[110:113]
	v_mfma_f32_16x16x32_f16 v[114:117], v[162:165], v[218:221], v[114:117]
	v_mfma_f32_16x16x32_f16 v[114:117], v[166:169], v[222:225], v[114:117]
	s_setprio 0
	s_barrier
	s_mov_b64 s[0:1], 0x280
	v_readfirstlane_b32 s10, v48
	v_lshl_add_u64 v[242:243], v[30:31], 0, s[0:1]
	s_mov_b32 m0, s10
	v_readfirstlane_b32 s2, v49
	ds_read_b128 v[226:229], v14
	ds_read_b128 v[230:233], v15
	ds_read_b128 v[234:237], v16
	ds_read_b128 v[238:241], v17
	global_load_lds_dwordx4 v[242:243], off
	v_lshl_add_u64 v[242:243], v[32:33], 0, s[0:1]
	s_mov_b32 m0, s2
	s_nop 0
	global_load_lds_dwordx4 v[242:243], off
	s_barrier
	s_waitcnt lgkmcnt(0)
	s_setprio 1
	s_waitcnt lgkmcnt(0)
	v_mfma_f32_16x16x32_f16 v[134:137], v[226:229], v[194:197], v[134:137]
	v_mfma_f32_16x16x32_f16 v[58:61], v[234:237], v[194:197], v[58:61]
	v_mfma_f32_16x16x32_f16 v[138:141], v[226:229], v[202:205], v[138:141]
	v_mfma_f32_16x16x32_f16 v[62:65], v[234:237], v[202:205], v[62:65]
	v_mfma_f32_16x16x32_f16 v[66:69], v[226:229], v[210:213], v[66:69]
	v_mfma_f32_16x16x32_f16 v[70:73], v[234:237], v[210:213], v[70:73]
	v_mfma_f32_16x16x32_f16 v[74:77], v[226:229], v[218:221], v[74:77]
	v_mfma_f32_16x16x32_f16 v[78:81], v[234:237], v[218:221], v[78:81]
	v_mfma_f32_16x16x32_f16 v[134:137], v[230:233], v[198:201], v[134:137]
	v_mfma_f32_16x16x32_f16 v[58:61], v[238:241], v[198:201], v[58:61]
	v_mfma_f32_16x16x32_f16 v[138:141], v[230:233], v[206:209], v[138:141]
	v_mfma_f32_16x16x32_f16 v[62:65], v[238:241], v[206:209], v[62:65]
	v_mfma_f32_16x16x32_f16 v[66:69], v[230:233], v[214:217], v[66:69]
	v_mfma_f32_16x16x32_f16 v[70:73], v[238:241], v[214:217], v[70:73]
	v_mfma_f32_16x16x32_f16 v[74:77], v[230:233], v[222:225], v[74:77]
	v_mfma_f32_16x16x32_f16 v[78:81], v[238:241], v[222:225], v[78:81]
	s_setprio 0
	v_readfirstlane_b32 s11, v46
	v_lshl_add_u64 v[48:49], v[26:27], 0, s[0:1]
	s_mov_b32 m0, s11
	v_readfirstlane_b32 s3, v47
	s_barrier
	ds_read_b128 v[194:197], v1 offset:49152
	ds_read_b128 v[198:201], v1 offset:50176
	ds_read_b128 v[202:205], v1 offset:51200
	ds_read_b128 v[206:209], v1 offset:52224
	ds_read_b128 v[210:213], v1 offset:53248
	ds_read_b128 v[214:217], v1 offset:54272
	ds_read_b128 v[218:221], v1 offset:55296
	ds_read_b128 v[222:225], v1 offset:56320
	global_load_lds_dwordx4 v[48:49], off
	v_lshl_add_u64 v[48:49], v[28:29], 0, s[0:1]
	s_mov_b32 m0, s3
	s_nop 0
	global_load_lds_dwordx4 v[48:49], off
	s_barrier
	s_waitcnt lgkmcnt(0)
	s_setprio 1
	s_waitcnt lgkmcnt(0)
	v_mfma_f32_16x16x32_f16 v[126:129], v[154:157], v[218:221], v[126:129]
	v_mfma_f32_16x16x32_f16 v[50:53], v[162:165], v[218:221], v[50:53]
	v_mfma_f32_16x16x32_f16 v[46:49], v[154:157], v[194:197], v[170:173]
	v_mfma_f32_16x16x32_f16 v[170:173], v[162:165], v[194:197], v[174:177]
	v_mfma_f32_16x16x32_f16 v[174:177], v[154:157], v[202:205], v[178:181]
	v_mfma_f32_16x16x32_f16 v[178:181], v[162:165], v[202:205], v[182:185]
	v_mfma_f32_16x16x32_f16 v[182:185], v[154:157], v[210:213], v[186:189]
	v_mfma_f32_16x16x32_f16 v[186:189], v[162:165], v[210:213], v[190:193]
	v_mfma_f32_16x16x32_f16 v[126:129], v[158:161], v[222:225], v[126:129]
	v_mfma_f32_16x16x32_f16 v[50:53], v[166:169], v[222:225], v[50:53]
	v_mfma_f32_16x16x32_f16 v[46:49], v[158:161], v[198:201], v[46:49]
	v_mfma_f32_16x16x32_f16 v[170:173], v[166:169], v[198:201], v[170:173]
	v_mfma_f32_16x16x32_f16 v[174:177], v[158:161], v[206:209], v[174:177]
	v_mfma_f32_16x16x32_f16 v[178:181], v[166:169], v[206:209], v[178:181]
	v_mfma_f32_16x16x32_f16 v[182:185], v[158:161], v[214:217], v[182:185]
	v_mfma_f32_16x16x32_f16 v[186:189], v[166:169], v[214:217], v[186:189]
	s_setprio 0
	s_barrier
	v_readfirstlane_b32 s5, v37
	v_lshl_add_u64 v[154:155], v[22:23], 0, s[0:1]
	s_mov_b32 m0, s5
	v_readfirstlane_b32 s4, v39
	global_load_lds_dwordx4 v[154:155], off
	v_lshl_add_u64 v[154:155], v[24:25], 0, s[0:1]
	s_mov_b32 m0, s4
	s_nop 0
	global_load_lds_dwordx4 v[154:155], off
	s_waitcnt vmcnt(6)
	s_barrier
	s_setprio 1
	v_mfma_f32_16x16x32_f16 v[82:85], v[234:237], v[194:197], v[82:85]
	v_mfma_f32_16x16x32_f16 v[130:133], v[226:229], v[202:205], v[130:133]
	v_mfma_f32_16x16x32_f16 v[142:145], v[234:237], v[202:205], v[142:145]
	v_mfma_f32_16x16x32_f16 v[146:149], v[226:229], v[210:213], v[146:149]
	v_mfma_f32_16x16x32_f16 v[150:153], v[234:237], v[210:213], v[150:153]
	v_mfma_f32_16x16x32_f16 v[118:121], v[226:229], v[218:221], v[118:121]
	v_mfma_f32_16x16x32_f16 v[122:125], v[234:237], v[218:221], v[122:125]
	v_mfma_f32_16x16x32_f16 v[54:57], v[226:229], v[194:197], v[54:57]
	v_mfma_f32_16x16x32_f16 v[82:85], v[238:241], v[198:201], v[82:85]
	v_mfma_f32_16x16x32_f16 v[130:133], v[230:233], v[206:209], v[130:133]
	v_mfma_f32_16x16x32_f16 v[142:145], v[238:241], v[206:209], v[142:145]
	v_mfma_f32_16x16x32_f16 v[146:149], v[230:233], v[214:217], v[146:149]
	v_mfma_f32_16x16x32_f16 v[150:153], v[238:241], v[214:217], v[150:153]
	v_mfma_f32_16x16x32_f16 v[118:121], v[230:233], v[222:225], v[118:121]
	v_mfma_f32_16x16x32_f16 v[122:125], v[238:241], v[222:225], v[122:125]
	v_mfma_f32_16x16x32_f16 v[54:57], v[230:233], v[198:201], v[54:57]
	s_setprio 0
	s_barrier
	ds_read_b128 v[154:157], v2
	ds_read_b128 v[158:161], v3
	ds_read_b128 v[162:165], v4
	ds_read_b128 v[166:169], v5
	v_readfirstlane_b32 s14, v38
	v_lshl_add_u64 v[190:191], v[18:19], 0, s[0:1]
	s_mov_b32 m0, s14
	v_readfirstlane_b32 s7, v40
	global_load_lds_dwordx4 v[190:191], off
	v_lshl_add_u64 v[38:39], v[20:21], 0, s[0:1]
	s_mov_b32 m0, s7
	s_nop 0
	global_load_lds_dwordx4 v[38:39], off
	ds_read_b128 v[190:193], v1
	ds_read_b128 v[194:197], v1 offset:1024
	ds_read_b128 v[198:201], v1 offset:2048
	ds_read_b128 v[202:205], v1 offset:3072
	ds_read_b128 v[206:209], v1 offset:4096
	ds_read_b128 v[210:213], v1 offset:5120
	ds_read_b128 v[214:217], v1 offset:6144
	ds_read_b128 v[218:221], v1 offset:7168
	s_waitcnt lgkmcnt(8)
	s_barrier
	s_waitcnt lgkmcnt(0)
	s_setprio 1
	s_waitcnt lgkmcnt(0)
	v_mfma_f32_16x16x32_f16 v[86:89], v[154:157], v[190:193], v[86:89]
	v_mfma_f32_16x16x32_f16 v[90:93], v[162:165], v[190:193], v[90:93]
	v_mfma_f32_16x16x32_f16 v[94:97], v[154:157], v[198:201], v[94:97]
	v_mfma_f32_16x16x32_f16 v[98:101], v[162:165], v[198:201], v[98:101]
	v_mfma_f32_16x16x32_f16 v[102:105], v[154:157], v[206:209], v[102:105]
	v_mfma_f32_16x16x32_f16 v[106:109], v[162:165], v[206:209], v[106:109]
	v_mfma_f32_16x16x32_f16 v[110:113], v[154:157], v[214:217], v[110:113]
	v_mfma_f32_16x16x32_f16 v[86:89], v[158:161], v[194:197], v[86:89]
	v_mfma_f32_16x16x32_f16 v[90:93], v[166:169], v[194:197], v[90:93]
	v_mfma_f32_16x16x32_f16 v[94:97], v[158:161], v[202:205], v[94:97]
	v_mfma_f32_16x16x32_f16 v[98:101], v[166:169], v[202:205], v[98:101]
	v_mfma_f32_16x16x32_f16 v[102:105], v[158:161], v[210:213], v[102:105]
	v_mfma_f32_16x16x32_f16 v[106:109], v[166:169], v[210:213], v[106:109]
	v_mfma_f32_16x16x32_f16 v[110:113], v[158:161], v[218:221], v[110:113]
	v_mfma_f32_16x16x32_f16 v[114:117], v[162:165], v[214:217], v[114:117]
	v_mfma_f32_16x16x32_f16 v[114:117], v[166:169], v[218:221], v[114:117]
	s_setprio 0
	s_barrier
	s_mov_b64 s[0:1], 0x300
	v_readfirstlane_b32 s15, v36
	v_lshl_add_u64 v[38:39], v[30:31], 0, s[0:1]
	s_mov_b32 m0, s15
	v_readfirstlane_b32 s15, v41
	ds_read_b128 v[222:225], v6
	ds_read_b128 v[226:229], v7
	ds_read_b128 v[230:233], v8
	ds_read_b128 v[234:237], v9
	global_load_lds_dwordx4 v[38:39], off
	v_lshl_add_u64 v[36:37], v[32:33], 0, s[0:1]
	s_mov_b32 m0, s15
	s_nop 0
	global_load_lds_dwordx4 v[36:37], off
	s_barrier
	s_waitcnt lgkmcnt(0)
	s_setprio 1
	s_waitcnt lgkmcnt(0)
	v_mfma_f32_16x16x32_f16 v[36:39], v[222:225], v[190:193], v[134:137]
	v_mfma_f32_16x16x32_f16 v[58:61], v[230:233], v[190:193], v[58:61]
	v_mfma_f32_16x16x32_f16 v[134:137], v[222:225], v[198:201], v[138:141]
	v_mfma_f32_16x16x32_f16 v[62:65], v[230:233], v[198:201], v[62:65]
	v_mfma_f32_16x16x32_f16 v[66:69], v[222:225], v[206:209], v[66:69]
	v_mfma_f32_16x16x32_f16 v[70:73], v[230:233], v[206:209], v[70:73]
	v_mfma_f32_16x16x32_f16 v[74:77], v[222:225], v[214:217], v[74:77]
	v_mfma_f32_16x16x32_f16 v[78:81], v[230:233], v[214:217], v[78:81]
	v_mfma_f32_16x16x32_f16 v[36:39], v[226:229], v[194:197], v[36:39]
	v_mfma_f32_16x16x32_f16 v[58:61], v[234:237], v[194:197], v[58:61]
	v_mfma_f32_16x16x32_f16 v[134:137], v[226:229], v[202:205], v[134:137]
	v_mfma_f32_16x16x32_f16 v[62:65], v[234:237], v[202:205], v[62:65]
	v_mfma_f32_16x16x32_f16 v[66:69], v[226:229], v[210:213], v[66:69]
	v_mfma_f32_16x16x32_f16 v[70:73], v[234:237], v[210:213], v[70:73]
	v_mfma_f32_16x16x32_f16 v[74:77], v[226:229], v[218:221], v[74:77]
	v_mfma_f32_16x16x32_f16 v[78:81], v[234:237], v[218:221], v[78:81]
	s_setprio 0
	v_readfirstlane_b32 s15, v35
	v_lshl_add_u64 v[40:41], v[26:27], 0, s[0:1]
	s_mov_b32 m0, s15
	v_readfirstlane_b32 s15, v42
	s_barrier
	ds_read_b128 v[138:141], v1 offset:16384
	ds_read_b128 v[190:193], v1 offset:17408
	ds_read_b128 v[194:197], v1 offset:18432
	ds_read_b128 v[198:201], v1 offset:19456
	ds_read_b128 v[202:205], v1 offset:20480
	ds_read_b128 v[206:209], v1 offset:21504
	ds_read_b128 v[210:213], v1 offset:22528
	ds_read_b128 v[214:217], v1 offset:23552
	global_load_lds_dwordx4 v[40:41], off
	v_lshl_add_u64 v[40:41], v[28:29], 0, s[0:1]
	s_mov_b32 m0, s15
	s_nop 0
	global_load_lds_dwordx4 v[40:41], off
	s_barrier
	s_waitcnt lgkmcnt(0)
	s_setprio 1
	s_waitcnt lgkmcnt(0)
	v_mfma_f32_16x16x32_f16 v[126:129], v[154:157], v[210:213], v[126:129]
	v_mfma_f32_16x16x32_f16 v[50:53], v[162:165], v[210:213], v[50:53]
	v_mfma_f32_16x16x32_f16 v[46:49], v[154:157], v[138:141], v[46:49]
	v_mfma_f32_16x16x32_f16 v[170:173], v[162:165], v[138:141], v[170:173]
	v_mfma_f32_16x16x32_f16 v[174:177], v[154:157], v[194:197], v[174:177]
	v_mfma_f32_16x16x32_f16 v[178:181], v[162:165], v[194:197], v[178:181]
	v_mfma_f32_16x16x32_f16 v[182:185], v[154:157], v[202:205], v[182:185]
	v_mfma_f32_16x16x32_f16 v[186:189], v[162:165], v[202:205], v[186:189]
	v_mfma_f32_16x16x32_f16 v[126:129], v[158:161], v[214:217], v[126:129]
	v_mfma_f32_16x16x32_f16 v[50:53], v[166:169], v[214:217], v[50:53]
	v_mfma_f32_16x16x32_f16 v[46:49], v[158:161], v[190:193], v[46:49]
	v_mfma_f32_16x16x32_f16 v[170:173], v[166:169], v[190:193], v[170:173]
	v_mfma_f32_16x16x32_f16 v[174:177], v[158:161], v[198:201], v[174:177]
	v_mfma_f32_16x16x32_f16 v[178:181], v[166:169], v[198:201], v[178:181]
	v_mfma_f32_16x16x32_f16 v[182:185], v[158:161], v[206:209], v[182:185]
	v_mfma_f32_16x16x32_f16 v[186:189], v[166:169], v[206:209], v[186:189]
	s_setprio 0
	s_barrier
	v_readfirstlane_b32 s15, v34
	v_lshl_add_u64 v[40:41], v[22:23], 0, s[0:1]
	s_mov_b32 m0, s15
	v_readfirstlane_b32 s15, v43
	global_load_lds_dwordx4 v[40:41], off
	v_lshl_add_u64 v[34:35], v[24:25], 0, s[0:1]
	s_mov_b32 m0, s15
	s_nop 0
	global_load_lds_dwordx4 v[34:35], off
	s_waitcnt vmcnt(6)
	s_barrier
	s_setprio 1
	v_mfma_f32_16x16x32_f16 v[40:43], v[222:225], v[138:141], v[54:57]
	v_mfma_f32_16x16x32_f16 v[54:57], v[230:233], v[138:141], v[82:85]
	v_mfma_f32_16x16x32_f16 v[82:85], v[222:225], v[194:197], v[130:133]
	v_mfma_f32_16x16x32_f16 v[130:133], v[230:233], v[194:197], v[142:145]
	v_mfma_f32_16x16x32_f16 v[138:141], v[222:225], v[202:205], v[146:149]
	v_mfma_f32_16x16x32_f16 v[142:145], v[230:233], v[202:205], v[150:153]
	v_mfma_f32_16x16x32_f16 v[118:121], v[222:225], v[210:213], v[118:121]
	v_mfma_f32_16x16x32_f16 v[122:125], v[230:233], v[210:213], v[122:125]
	v_mfma_f32_16x16x32_f16 v[82:85], v[226:229], v[198:201], v[82:85]
	v_mfma_f32_16x16x32_f16 v[130:133], v[234:237], v[198:201], v[130:133]
	v_mfma_f32_16x16x32_f16 v[138:141], v[226:229], v[206:209], v[138:141]
	v_mfma_f32_16x16x32_f16 v[142:145], v[234:237], v[206:209], v[142:145]
	v_mfma_f32_16x16x32_f16 v[118:121], v[226:229], v[214:217], v[118:121]
	v_mfma_f32_16x16x32_f16 v[122:125], v[234:237], v[214:217], v[122:125]
	v_mfma_f32_16x16x32_f16 v[40:43], v[226:229], v[190:193], v[40:43]
	v_mfma_f32_16x16x32_f16 v[54:57], v[234:237], v[190:193], v[54:57]
	s_setprio 0
	s_barrier
	ds_read_b128 v[146:149], v10
	ds_read_b128 v[150:153], v11
	ds_read_b128 v[154:157], v12
	ds_read_b128 v[158:161], v13
	v_readfirstlane_b32 s15, v44
	v_lshl_add_u64 v[34:35], v[18:19], 0, s[0:1]
	s_mov_b32 m0, s15
	ds_read_b128 v[162:165], v1 offset:32768
	ds_read_b128 v[166:169], v1 offset:33792
	ds_read_b128 v[190:193], v1 offset:34816
	ds_read_b128 v[194:197], v1 offset:35840
	ds_read_b128 v[198:201], v1 offset:36864
	ds_read_b128 v[202:205], v1 offset:37888
	ds_read_b128 v[206:209], v1 offset:38912
	ds_read_b128 v[210:213], v1 offset:39936
	global_load_lds_dwordx4 v[34:35], off
	v_lshl_add_u64 v[34:35], v[20:21], 0, s[0:1]
	v_readfirstlane_b32 s0, v45
	s_mov_b32 m0, s0
	s_nop 0
	global_load_lds_dwordx4 v[34:35], off
	s_waitcnt lgkmcnt(8)
	s_barrier
	s_waitcnt lgkmcnt(0)
	s_setprio 1
	s_waitcnt lgkmcnt(0)
	v_mfma_f32_16x16x32_f16 v[86:89], v[146:149], v[162:165], v[86:89]
	v_mfma_f32_16x16x32_f16 v[90:93], v[154:157], v[162:165], v[90:93]
	v_mfma_f32_16x16x32_f16 v[94:97], v[146:149], v[190:193], v[94:97]
	v_mfma_f32_16x16x32_f16 v[98:101], v[154:157], v[190:193], v[98:101]
	v_mfma_f32_16x16x32_f16 v[102:105], v[146:149], v[198:201], v[102:105]
	v_mfma_f32_16x16x32_f16 v[106:109], v[154:157], v[198:201], v[106:109]
	v_mfma_f32_16x16x32_f16 v[110:113], v[146:149], v[206:209], v[110:113]
	v_mfma_f32_16x16x32_f16 v[86:89], v[150:153], v[166:169], v[86:89]
	v_mfma_f32_16x16x32_f16 v[90:93], v[158:161], v[166:169], v[90:93]
	v_mfma_f32_16x16x32_f16 v[94:97], v[150:153], v[194:197], v[94:97]
	v_mfma_f32_16x16x32_f16 v[98:101], v[158:161], v[194:197], v[98:101]
	v_mfma_f32_16x16x32_f16 v[102:105], v[150:153], v[202:205], v[102:105]
	v_mfma_f32_16x16x32_f16 v[106:109], v[158:161], v[202:205], v[106:109]
	v_mfma_f32_16x16x32_f16 v[110:113], v[150:153], v[210:213], v[110:113]
	v_mfma_f32_16x16x32_f16 v[114:117], v[154:157], v[206:209], v[114:117]
	v_mfma_f32_16x16x32_f16 v[114:117], v[158:161], v[210:213], v[114:117]
	s_setprio 0
	s_barrier
	s_mov_b64 s[0:1], 0x380
	s_mov_b32 m0, s10
	v_lshl_add_u64 v[30:31], v[30:31], 0, s[0:1]
	ds_read_b128 v[214:217], v14
	ds_read_b128 v[218:221], v15
	ds_read_b128 v[222:225], v16
	ds_read_b128 v[226:229], v17
	global_load_lds_dwordx4 v[30:31], off
	v_lshl_add_u64 v[30:31], v[32:33], 0, s[0:1]
	s_mov_b32 m0, s2
	s_nop 0
	global_load_lds_dwordx4 v[30:31], off
	s_barrier
	s_waitcnt lgkmcnt(0)
	s_setprio 1
	s_waitcnt lgkmcnt(0)
	v_mfma_f32_16x16x32_f16 v[30:33], v[214:217], v[162:165], v[36:39]
	v_mfma_f32_16x16x32_f16 v[34:37], v[222:225], v[162:165], v[58:61]
	v_mfma_f32_16x16x32_f16 v[58:61], v[214:217], v[190:193], v[134:137]
	v_mfma_f32_16x16x32_f16 v[62:65], v[222:225], v[190:193], v[62:65]
	v_mfma_f32_16x16x32_f16 v[66:69], v[214:217], v[198:201], v[66:69]
	v_mfma_f32_16x16x32_f16 v[70:73], v[222:225], v[198:201], v[70:73]
	v_mfma_f32_16x16x32_f16 v[74:77], v[214:217], v[206:209], v[74:77]
	v_mfma_f32_16x16x32_f16 v[78:81], v[222:225], v[206:209], v[78:81]
	v_mfma_f32_16x16x32_f16 v[34:37], v[226:229], v[166:169], v[34:37]
	v_mfma_f32_16x16x32_f16 v[58:61], v[218:221], v[194:197], v[58:61]
	v_mfma_f32_16x16x32_f16 v[62:65], v[226:229], v[194:197], v[62:65]
	v_mfma_f32_16x16x32_f16 v[66:69], v[218:221], v[202:205], v[66:69]
	v_mfma_f32_16x16x32_f16 v[70:73], v[226:229], v[202:205], v[70:73]
	v_mfma_f32_16x16x32_f16 v[74:77], v[218:221], v[210:213], v[74:77]
	v_mfma_f32_16x16x32_f16 v[78:81], v[226:229], v[210:213], v[78:81]
	v_mfma_f32_16x16x32_f16 v[30:33], v[218:221], v[166:169], v[30:33]
	s_setprio 0
	s_mov_b32 m0, s11
	v_lshl_add_u64 v[26:27], v[26:27], 0, s[0:1]
	s_barrier
	ds_read_b128 v[134:137], v1 offset:49152
	ds_read_b128 v[162:165], v1 offset:50176
	ds_read_b128 v[166:169], v1 offset:51200
	ds_read_b128 v[190:193], v1 offset:52224
	ds_read_b128 v[194:197], v1 offset:53248
	ds_read_b128 v[198:201], v1 offset:54272
	ds_read_b128 v[202:205], v1 offset:55296
	ds_read_b128 v[206:209], v1 offset:56320
	global_load_lds_dwordx4 v[26:27], off
	v_lshl_add_u64 v[26:27], v[28:29], 0, s[0:1]
	s_mov_b32 m0, s3
	s_nop 0
	global_load_lds_dwordx4 v[26:27], off
	s_barrier
	s_waitcnt lgkmcnt(0)
	s_setprio 1
	s_waitcnt lgkmcnt(0)
	v_mfma_f32_16x16x32_f16 v[26:29], v[146:149], v[134:137], v[46:49]
	v_mfma_f32_16x16x32_f16 v[126:129], v[146:149], v[202:205], v[126:129]
	v_mfma_f32_16x16x32_f16 v[48:51], v[154:157], v[202:205], v[50:53]
	v_mfma_f32_16x16x32_f16 v[44:47], v[154:157], v[134:137], v[170:173]
	v_mfma_f32_16x16x32_f16 v[170:173], v[146:149], v[166:169], v[174:177]
	v_mfma_f32_16x16x32_f16 v[174:177], v[154:157], v[166:169], v[178:181]
	v_mfma_f32_16x16x32_f16 v[178:181], v[146:149], v[194:197], v[182:185]
	v_mfma_f32_16x16x32_f16 v[182:185], v[154:157], v[194:197], v[186:189]
	v_mfma_f32_16x16x32_f16 v[126:129], v[150:153], v[206:209], v[126:129]
	v_mfma_f32_16x16x32_f16 v[48:51], v[158:161], v[206:209], v[48:51]
	v_mfma_f32_16x16x32_f16 v[26:29], v[150:153], v[162:165], v[26:29]
	v_mfma_f32_16x16x32_f16 v[44:47], v[158:161], v[162:165], v[44:47]
	v_mfma_f32_16x16x32_f16 v[170:173], v[150:153], v[190:193], v[170:173]
	v_mfma_f32_16x16x32_f16 v[174:177], v[158:161], v[190:193], v[174:177]
	v_mfma_f32_16x16x32_f16 v[178:181], v[150:153], v[198:201], v[178:181]
	v_mfma_f32_16x16x32_f16 v[182:185], v[158:161], v[198:201], v[182:185]
	s_setprio 0
	s_barrier
	s_mov_b32 m0, s5
	v_lshl_add_u64 v[22:23], v[22:23], 0, s[0:1]
	global_load_lds_dwordx4 v[22:23], off
	v_lshl_add_u64 v[22:23], v[24:25], 0, s[0:1]
	s_mov_b32 m0, s4
	s_nop 0
	global_load_lds_dwordx4 v[22:23], off
	s_waitcnt vmcnt(6)
	s_barrier
	s_setprio 1
	v_mfma_f32_16x16x32_f16 v[22:25], v[214:217], v[134:137], v[40:43]
	v_mfma_f32_16x16x32_f16 v[38:41], v[222:225], v[134:137], v[54:57]
	v_mfma_f32_16x16x32_f16 v[52:55], v[214:217], v[166:169], v[82:85]
	v_mfma_f32_16x16x32_f16 v[82:85], v[222:225], v[166:169], v[130:133]
	v_mfma_f32_16x16x32_f16 v[130:133], v[214:217], v[194:197], v[138:141]
	v_mfma_f32_16x16x32_f16 v[134:137], v[222:225], v[194:197], v[142:145]
	v_mfma_f32_16x16x32_f16 v[118:121], v[214:217], v[202:205], v[118:121]
	v_mfma_f32_16x16x32_f16 v[122:125], v[222:225], v[202:205], v[122:125]
	v_mfma_f32_16x16x32_f16 v[52:55], v[218:221], v[190:193], v[52:55]
	v_mfma_f32_16x16x32_f16 v[82:85], v[226:229], v[190:193], v[82:85]
	v_mfma_f32_16x16x32_f16 v[130:133], v[218:221], v[198:201], v[130:133]
	v_mfma_f32_16x16x32_f16 v[134:137], v[226:229], v[198:201], v[134:137]
	v_mfma_f32_16x16x32_f16 v[118:121], v[218:221], v[206:209], v[118:121]
	v_mfma_f32_16x16x32_f16 v[122:125], v[226:229], v[206:209], v[122:125]
	v_mfma_f32_16x16x32_f16 v[22:25], v[218:221], v[162:165], v[22:25]
	v_mfma_f32_16x16x32_f16 v[38:41], v[226:229], v[162:165], v[38:41]
	s_setprio 0
	s_mov_b32 m0, s14
	v_lshl_add_u64 v[18:19], v[18:19], 0, s[0:1]
	s_barrier
	ds_read_b128 v[138:141], v2
	ds_read_b128 v[142:145], v3
	ds_read_b128 v[146:149], v4
	ds_read_b128 v[2:5], v5
	global_load_lds_dwordx4 v[18:19], off
	v_lshl_add_u64 v[18:19], v[20:21], 0, s[0:1]
	s_mov_b32 m0, s7
	s_nop 0
	global_load_lds_dwordx4 v[18:19], off
	ds_read_b128 v[18:21], v1
	ds_read_b128 v[150:153], v1 offset:1024
	ds_read_b128 v[154:157], v1 offset:2048
	ds_read_b128 v[158:161], v1 offset:3072
	ds_read_b128 v[162:165], v1 offset:4096
	ds_read_b128 v[166:169], v1 offset:5120
	ds_read_b128 v[186:189], v1 offset:6144
	ds_read_b128 v[190:193], v1 offset:7168
	s_barrier
	s_waitcnt lgkmcnt(0)
	s_setprio 1
	s_waitcnt lgkmcnt(0)
	v_mfma_f32_16x16x32_f16 v[86:89], v[138:141], v[18:21], v[86:89]
	v_mfma_f32_16x16x32_f16 v[90:93], v[146:149], v[18:21], v[90:93]
	v_mfma_f32_16x16x32_f16 v[94:97], v[138:141], v[154:157], v[94:97]
	v_mfma_f32_16x16x32_f16 v[98:101], v[146:149], v[154:157], v[98:101]
	v_mfma_f32_16x16x32_f16 v[102:105], v[138:141], v[162:165], v[102:105]
	v_mfma_f32_16x16x32_f16 v[106:109], v[146:149], v[162:165], v[106:109]
	v_mfma_f32_16x16x32_f16 v[110:113], v[138:141], v[186:189], v[110:113]
	v_mfma_f32_16x16x32_f16 v[86:89], v[142:145], v[150:153], v[86:89]
	v_mfma_f32_16x16x32_f16 v[90:93], v[2:5], v[150:153], v[90:93]
	v_mfma_f32_16x16x32_f16 v[94:97], v[142:145], v[158:161], v[94:97]
	v_mfma_f32_16x16x32_f16 v[98:101], v[2:5], v[158:161], v[98:101]
	v_mfma_f32_16x16x32_f16 v[102:105], v[142:145], v[166:169], v[102:105]
	v_mfma_f32_16x16x32_f16 v[106:109], v[2:5], v[166:169], v[106:109]
	v_mfma_f32_16x16x32_f16 v[110:113], v[142:145], v[190:193], v[110:113]
	v_mfma_f32_16x16x32_f16 v[114:117], v[146:149], v[186:189], v[114:117]
	v_mfma_f32_16x16x32_f16 v[114:117], v[2:5], v[190:193], v[114:117]
	s_setprio 0
	s_barrier
	ds_read_b128 v[194:197], v6
	ds_read_b128 v[198:201], v7
	ds_read_b128 v[202:205], v8
	ds_read_b128 v[6:9], v9
	s_barrier
	s_waitcnt lgkmcnt(0)
	s_setprio 1
	s_waitcnt lgkmcnt(0)
	v_mfma_f32_16x16x32_f16 v[30:33], v[194:197], v[18:21], v[30:33]
	v_mfma_f32_16x16x32_f16 v[18:21], v[202:205], v[18:21], v[34:37]
	v_mfma_f32_16x16x32_f16 v[34:37], v[194:197], v[154:157], v[58:61]
	v_mfma_f32_16x16x32_f16 v[56:59], v[202:205], v[154:157], v[62:65]
	v_mfma_f32_16x16x32_f16 v[60:63], v[194:197], v[162:165], v[66:69]
	v_mfma_f32_16x16x32_f16 v[64:67], v[202:205], v[162:165], v[70:73]
	v_mfma_f32_16x16x32_f16 v[68:71], v[194:197], v[186:189], v[74:77]
	v_mfma_f32_16x16x32_f16 v[72:75], v[202:205], v[186:189], v[78:81]
	v_mfma_f32_16x16x32_f16 v[34:37], v[198:201], v[158:161], v[34:37]
	v_mfma_f32_16x16x32_f16 v[56:59], v[6:9], v[158:161], v[56:59]
	v_mfma_f32_16x16x32_f16 v[60:63], v[198:201], v[166:169], v[60:63]
	v_mfma_f32_16x16x32_f16 v[64:67], v[6:9], v[166:169], v[64:67]
	v_mfma_f32_16x16x32_f16 v[68:71], v[198:201], v[190:193], v[68:71]
	v_mfma_f32_16x16x32_f16 v[72:75], v[6:9], v[190:193], v[72:75]
	v_mfma_f32_16x16x32_f16 v[30:33], v[198:201], v[150:153], v[30:33]
	v_mfma_f32_16x16x32_f16 v[18:21], v[6:9], v[150:153], v[18:21]
	s_setprio 0
	s_barrier
	ds_read_b128 v[76:79], v1 offset:16384
	ds_read_b128 v[150:153], v1 offset:17408
	ds_read_b128 v[154:157], v1 offset:18432
	ds_read_b128 v[158:161], v1 offset:19456
	ds_read_b128 v[162:165], v1 offset:20480
	ds_read_b128 v[166:169], v1 offset:21504
	ds_read_b128 v[186:189], v1 offset:22528
	ds_read_b128 v[190:193], v1 offset:23552
	s_waitcnt vmcnt(4)
	s_barrier
	s_waitcnt lgkmcnt(0)
	s_setprio 1
	s_waitcnt lgkmcnt(0)
	v_mfma_f32_16x16x32_f16 v[42:45], v[146:149], v[76:79], v[44:47]
	v_mfma_f32_16x16x32_f16 v[174:177], v[146:149], v[154:157], v[174:177]
	v_mfma_f32_16x16x32_f16 v[182:185], v[146:149], v[162:165], v[182:185]
	v_mfma_f32_16x16x32_f16 v[46:49], v[146:149], v[186:189], v[48:51]
	v_mfma_f32_16x16x32_f16 v[26:29], v[138:141], v[76:79], v[26:29]
	v_mfma_f32_16x16x32_f16 v[42:45], v[2:5], v[150:153], v[42:45]
	v_mfma_f32_16x16x32_f16 v[170:173], v[138:141], v[154:157], v[170:173]
	v_mfma_f32_16x16x32_f16 v[174:177], v[2:5], v[158:161], v[174:177]
	v_mfma_f32_16x16x32_f16 v[178:181], v[138:141], v[162:165], v[178:181]
	v_mfma_f32_16x16x32_f16 v[182:185], v[2:5], v[166:169], v[182:185]
	v_mfma_f32_16x16x32_f16 v[126:129], v[138:141], v[186:189], v[126:129]
	v_mfma_f32_16x16x32_f16 v[2:5], v[2:5], v[190:193], v[46:49]
	v_mfma_f32_16x16x32_f16 v[26:29], v[142:145], v[150:153], v[26:29]
	v_mfma_f32_16x16x32_f16 v[170:173], v[142:145], v[158:161], v[170:173]
	v_mfma_f32_16x16x32_f16 v[178:181], v[142:145], v[166:169], v[178:181]
	v_mfma_f32_16x16x32_f16 v[206:209], v[142:145], v[190:193], v[126:129]
	s_setprio 0
	s_setprio 1
	v_mfma_f32_16x16x32_f16 v[46:49], v[194:197], v[154:157], v[52:55]
	v_mfma_f32_16x16x32_f16 v[50:53], v[202:205], v[154:157], v[82:85]
	v_mfma_f32_16x16x32_f16 v[210:213], v[6:9], v[158:161], v[50:53]
	v_mfma_f32_16x16x32_f16 v[50:53], v[194:197], v[162:165], v[130:133]
	v_mfma_f32_16x16x32_f16 v[214:217], v[198:201], v[166:169], v[50:53]
	v_mfma_f32_16x16x32_f16 v[50:53], v[202:205], v[162:165], v[134:137]
	v_mfma_f32_16x16x32_f16 v[166:169], v[6:9], v[166:169], v[50:53]
	v_mfma_f32_16x16x32_f16 v[50:53], v[194:197], v[186:189], v[118:121]
	v_mfma_f32_16x16x32_f16 v[22:25], v[194:197], v[76:79], v[22:25]
	v_mfma_f32_16x16x32_f16 v[38:41], v[202:205], v[76:79], v[38:41]
	v_mfma_f32_16x16x32_f16 v[194:197], v[198:201], v[190:193], v[50:53]
	v_mfma_f32_16x16x32_f16 v[50:53], v[202:205], v[186:189], v[122:125]
	v_mfma_f32_16x16x32_f16 v[22:25], v[198:201], v[150:153], v[22:25]
	v_mfma_f32_16x16x32_f16 v[38:41], v[6:9], v[150:153], v[38:41]
	v_mfma_f32_16x16x32_f16 v[46:49], v[198:201], v[158:161], v[46:49]
	v_mfma_f32_16x16x32_f16 v[186:189], v[6:9], v[190:193], v[50:53]
	s_setprio 0
	s_barrier
	ds_read_b128 v[6:9], v10
	ds_read_b128 v[82:85], v11
	ds_read_b128 v[190:193], v12
	ds_read_b128 v[10:13], v13
	ds_read_b128 v[50:53], v1 offset:32768
	ds_read_b128 v[76:79], v1 offset:33792
	ds_read_b128 v[118:121], v1 offset:34816
	ds_read_b128 v[126:129], v1 offset:35840
	ds_read_b128 v[198:201], v1 offset:36864
	ds_read_b128 v[202:205], v1 offset:37888
	ds_read_b128 v[218:221], v1 offset:38912
	ds_read_b128 v[222:225], v1 offset:39936
	s_waitcnt vmcnt(2)
	s_barrier
	s_waitcnt lgkmcnt(0)
	s_setprio 1
	s_waitcnt lgkmcnt(0)
	v_mfma_f32_16x16x32_f16 v[86:89], v[6:9], v[50:53], v[86:89]
	v_mfma_f32_16x16x32_f16 v[162:165], v[82:85], v[76:79], v[86:89]
	v_mfma_f32_16x16x32_f16 v[86:89], v[190:193], v[50:53], v[90:93]
	v_mfma_f32_16x16x32_f16 v[154:157], v[10:13], v[76:79], v[86:89]
	v_mfma_f32_16x16x32_f16 v[86:89], v[6:9], v[118:121], v[94:97]
	v_mfma_f32_16x16x32_f16 v[146:149], v[82:85], v[126:129], v[86:89]
	v_mfma_f32_16x16x32_f16 v[86:89], v[190:193], v[118:121], v[98:101]
	v_mfma_f32_16x16x32_f16 v[138:141], v[10:13], v[126:129], v[86:89]
	v_mfma_f32_16x16x32_f16 v[86:89], v[6:9], v[198:201], v[102:105]
	v_mfma_f32_16x16x32_f16 v[130:133], v[82:85], v[202:205], v[86:89]
	v_mfma_f32_16x16x32_f16 v[86:89], v[190:193], v[198:201], v[106:109]
	v_mfma_f32_16x16x32_f16 v[122:125], v[10:13], v[202:205], v[86:89]
	v_mfma_f32_16x16x32_f16 v[86:89], v[6:9], v[218:221], v[110:113]
	v_mfma_f32_16x16x32_f16 v[110:113], v[82:85], v[222:225], v[86:89]
	v_mfma_f32_16x16x32_f16 v[86:89], v[190:193], v[218:221], v[114:117]
	v_mfma_f32_16x16x32_f16 v[102:105], v[10:13], v[222:225], v[86:89]
	s_setprio 0
	s_barrier
	ds_read_b128 v[114:117], v14
	ds_read_b128 v[226:229], v15
	ds_read_b128 v[230:233], v16
	ds_read_b128 v[234:237], v17
	s_waitcnt vmcnt(0)
	s_barrier
	s_waitcnt lgkmcnt(0)
	s_setprio 1
	s_waitcnt lgkmcnt(0)
	v_mfma_f32_16x16x32_f16 v[14:17], v[114:117], v[50:53], v[30:33]
	v_mfma_f32_16x16x32_f16 v[158:161], v[226:229], v[76:79], v[14:17]
	v_mfma_f32_16x16x32_f16 v[14:17], v[230:233], v[50:53], v[18:21]
	v_mfma_f32_16x16x32_f16 v[150:153], v[234:237], v[76:79], v[14:17]
	v_mfma_f32_16x16x32_f16 v[14:17], v[114:117], v[118:121], v[34:37]
	v_mfma_f32_16x16x32_f16 v[142:145], v[226:229], v[126:129], v[14:17]
	v_mfma_f32_16x16x32_f16 v[14:17], v[230:233], v[118:121], v[56:59]
	v_mfma_f32_16x16x32_f16 v[134:137], v[234:237], v[126:129], v[14:17]
	v_mfma_f32_16x16x32_f16 v[14:17], v[114:117], v[198:201], v[60:63]
	v_mfma_f32_16x16x32_f16 v[126:129], v[226:229], v[202:205], v[14:17]
	v_mfma_f32_16x16x32_f16 v[14:17], v[230:233], v[198:201], v[64:67]
	v_mfma_f32_16x16x32_f16 v[118:121], v[234:237], v[202:205], v[14:17]
	v_mfma_f32_16x16x32_f16 v[14:17], v[114:117], v[218:221], v[68:71]
	v_mfma_f32_16x16x32_f16 v[106:109], v[226:229], v[222:225], v[14:17]
	v_mfma_f32_16x16x32_f16 v[14:17], v[230:233], v[218:221], v[72:75]
	v_mfma_f32_16x16x32_f16 v[98:101], v[234:237], v[222:225], v[14:17]
	s_setprio 0
	s_barrier
	ds_read_b128 v[18:21], v1 offset:49152
	ds_read_b128 v[30:33], v1 offset:50176
	ds_read_b128 v[34:37], v1 offset:51200
	ds_read_b128 v[54:57], v1 offset:52224
	ds_read_b128 v[58:61], v1 offset:53248
	ds_read_b128 v[198:201], v1 offset:54272
	ds_read_b128 v[202:205], v1 offset:55296
	ds_read_b128 v[218:221], v1 offset:56320
	s_barrier
	s_waitcnt lgkmcnt(0)
	s_setprio 1
	s_waitcnt lgkmcnt(0)
	v_mfma_f32_16x16x32_f16 v[14:17], v[6:9], v[18:21], v[26:29]
	v_mfma_f32_16x16x32_f16 v[94:97], v[82:85], v[30:33], v[14:17]
	v_mfma_f32_16x16x32_f16 v[14:17], v[190:193], v[18:21], v[42:45]
	v_mfma_f32_16x16x32_f16 v[86:89], v[10:13], v[30:33], v[14:17]
	v_mfma_f32_16x16x32_f16 v[14:17], v[6:9], v[34:37], v[170:173]
	v_mfma_f32_16x16x32_f16 v[78:81], v[82:85], v[54:57], v[14:17]
	v_mfma_f32_16x16x32_f16 v[14:17], v[190:193], v[34:37], v[174:177]
	v_mfma_f32_16x16x32_f16 v[70:73], v[10:13], v[54:57], v[14:17]
	v_mfma_f32_16x16x32_f16 v[14:17], v[6:9], v[58:61], v[178:181]
	v_mfma_f32_16x16x32_f16 v[62:65], v[82:85], v[198:201], v[14:17]
	v_mfma_f32_16x16x32_f16 v[14:17], v[190:193], v[58:61], v[182:185]
	v_mfma_f32_16x16x32_f16 v[6:9], v[6:9], v[202:205], v[206:209]
	v_mfma_f32_16x16x32_f16 v[2:5], v[190:193], v[202:205], v[2:5]
	v_mfma_f32_16x16x32_f16 v[50:53], v[10:13], v[198:201], v[14:17]
	v_mfma_f32_16x16x32_f16 v[14:17], v[82:85], v[218:221], v[6:9]
	v_mfma_f32_16x16x32_f16 v[10:13], v[10:13], v[218:221], v[2:5]
	s_setprio 0
	s_setprio 1
	v_mfma_f32_16x16x32_f16 v[2:5], v[114:117], v[18:21], v[22:25]
	v_mfma_f32_16x16x32_f16 v[6:9], v[230:233], v[18:21], v[38:41]
	v_mfma_f32_16x16x32_f16 v[90:93], v[226:229], v[30:33], v[2:5]
	v_mfma_f32_16x16x32_f16 v[2:5], v[114:117], v[34:37], v[46:49]
	v_mfma_f32_16x16x32_f16 v[82:85], v[234:237], v[30:33], v[6:9]
	v_mfma_f32_16x16x32_f16 v[6:9], v[230:233], v[34:37], v[210:213]
	v_mfma_f32_16x16x32_f16 v[74:77], v[226:229], v[54:57], v[2:5]
	v_mfma_f32_16x16x32_f16 v[2:5], v[114:117], v[58:61], v[214:217]
	v_mfma_f32_16x16x32_f16 v[66:69], v[234:237], v[54:57], v[6:9]
	v_mfma_f32_16x16x32_f16 v[6:9], v[230:233], v[58:61], v[166:169]
	v_mfma_f32_16x16x32_f16 v[58:61], v[226:229], v[198:201], v[2:5]
	v_mfma_f32_16x16x32_f16 v[2:5], v[114:117], v[202:205], v[194:197]
	v_mfma_f32_16x16x32_f16 v[34:37], v[234:237], v[198:201], v[6:9]
	v_mfma_f32_16x16x32_f16 v[6:9], v[226:229], v[218:221], v[2:5]
	v_mfma_f32_16x16x32_f16 v[2:5], v[230:233], v[202:205], v[186:189]
	v_mfma_f32_16x16x32_f16 v[2:5], v[234:237], v[218:221], v[2:5]
	s_setprio 0
	s_barrier
	s_add_i32 s0, 0, 0x20800
	v_bfe_u32 v166, v0, 4, 2
	v_bfe_u32 v1, v0, 6, 2
	v_lshlrev_b32_e32 v18, 5, v166
	v_lshl_or_b32 v18, v1, 7, v18
	v_add_u32_e32 v19, s0, v18
	s_add_i32 s1, 0, 0x20c00
	v_add_u32_e32 v20, s1, v18
	ds_read_b128 v[54:57], v19
	ds_read_b128 v[46:49], v20
	v_or_b32_e32 v19, 16, v18
	v_add_u32_e32 v20, s0, v19
	v_add_u32_e32 v19, s1, v19
	ds_read_b128 v[42:45], v20
	ds_read_b128 v[38:41], v19
	v_or_b32_e32 v19, 0x200, v18
	v_add_u32_e32 v20, s0, v19
	v_add_u32_e32 v19, s1, v19
	v_or_b32_e32 v18, 0x210, v18
	ds_read_b128 v[30:33], v20
	ds_read_b128 v[26:29], v19
	v_add_u32_e32 v19, s0, v18
	v_and_b32_e32 v114, 15, v0
	v_ashrrev_i32_e32 v0, 2, v0
	s_movk_i32 s0, 0xffc0
	v_and_or_b32 v169, v0, s0, v114
	s_add_i32 s0, 0, 0x20000
	v_add_u32_e32 v18, s1, v18
	v_lshl_add_u32 v168, v169, 3, s0
	ds_read_b128 v[22:25], v19
	ds_read_b128 v[18:21], v18
	s_waitcnt vmcnt(0)
	ds_read2st64_b64 v[114:117], v168 offset1:2
	v_lshlrev_b32_e32 v0, 5, v1
	v_lshlrev_b32_e32 v1, 3, v166
	v_or3_b32 v166, v0, v1, s13
	v_add_u32_e32 v167, s12, v169
	s_waitcnt lgkmcnt(0)
	v_fma_f32 v154, -v114, v42, v154
	v_fma_f32 v154, v115, v154, v38
	v_fma_f32 v1, -v114, v54, v162
	v_fma_f32 v162, -v114, v55, v163
	v_fma_f32 v163, -v114, v56, v164
	v_fma_f32 v164, -v114, v57, v165
	v_max_f32_e32 v165, 0, v154
	v_fma_f32 v154, -v114, v43, v155
	v_fma_f32 v154, v115, v154, v39
	v_max_f32_e32 v170, 0, v154
	v_fma_f32 v154, -v114, v44, v156
	v_fma_f32 v154, v115, v154, v40
	v_max_f32_e32 v156, 0, v154
	v_fma_f32 v154, -v114, v45, v157
	v_fma_f32 v1, v115, v1, v46
	v_fma_f32 v162, v115, v162, v47
	v_fma_f32 v163, v115, v163, v48
	v_fma_f32 v164, v115, v164, v49
	v_fma_f32 v154, v115, v154, v41
	v_mul_lo_u32 v0, v167, s6
	v_max_f32_e32 v1, 0, v1
	v_max_f32_e32 v162, 0, v162
	v_max_f32_e32 v163, 0, v163
	v_max_f32_e32 v164, 0, v164
	v_max_f32_e32 v157, 0, v154
	s_and_b32 s9, s9, 0xffff
	s_mov_b32 s11, 0x20000
	s_mov_b32 s10, 0x7ffffff0
	v_cvt_pk_f16_f32 v155, v163, v164
	v_cvt_pk_f16_f32 v154, v1, v162
	v_cvt_pk_f16_f32 v157, v156, v157
	v_cvt_pk_f16_f32 v156, v165, v170
	v_add_lshl_u32 v0, v166, v0, 1
	buffer_store_dwordx4 v[154:157], v0, s[8:11], 0 offen sc1
	v_fma_f32 v1, -v114, v30, v158
	v_fma_f32 v150, -v114, v22, v150
	v_fma_f32 v154, -v114, v31, v159
	v_fma_f32 v155, -v114, v32, v160
	v_fma_f32 v156, -v114, v33, v161
	v_fma_f32 v151, -v114, v23, v151
	v_fma_f32 v152, -v114, v24, v152
	v_fma_f32 v114, -v114, v25, v153
	v_fma_f32 v1, v115, v1, v26
	v_fma_f32 v154, v115, v154, v27
	v_fma_f32 v155, v115, v155, v28
	v_fma_f32 v156, v115, v156, v29
	v_fma_f32 v150, v115, v150, v18
	v_fma_f32 v151, v115, v151, v19
	v_fma_f32 v152, v115, v152, v20
	v_fma_f32 v114, v115, v114, v21
	v_max_f32_e32 v1, 0, v1
	v_max_f32_e32 v154, 0, v154
	v_max_f32_e32 v155, 0, v155
	v_max_f32_e32 v156, 0, v156
	v_max_f32_e32 v150, 0, v150
	v_max_f32_e32 v151, 0, v151
	v_max_f32_e32 v152, 0, v152
	v_max_f32_e32 v114, 0, v114
	v_cvt_pk_f16_f32 v153, v152, v114
	v_cvt_pk_f16_f32 v152, v150, v151
	v_cvt_pk_f16_f32 v151, v155, v156
	v_cvt_pk_f16_f32 v150, v1, v154
	buffer_store_dwordx4 v[150:153], v0, s[8:11], 0 offen offset:256 sc1
	v_or_b32_e32 v0, 16, v169
	v_add_u32_e32 v114, s12, v0
	v_lshl_add_u32 v0, v0, 3, s0
	ds_read_b64 v[0:1], v0
	v_or_b32_e32 v155, 32, v169
	v_or_b32_e32 v156, 48, v169
	v_mul_lo_u32 v154, v114, s6
	v_lshl_add_u32 v114, v155, 3, s0
	s_waitcnt lgkmcnt(0)
	v_fma_f32 v146, -v0, v54, v146
	v_fma_f32 v147, -v0, v55, v147
	v_fma_f32 v148, -v0, v56, v148
	v_fma_f32 v149, -v0, v57, v149
	v_fma_f32 v138, -v0, v42, v138
	v_fma_f32 v139, -v0, v43, v139
	v_fma_f32 v140, -v0, v44, v140
	v_fma_f32 v141, -v0, v45, v141
	v_fma_f32 v146, v1, v146, v46
	v_fma_f32 v147, v1, v147, v47
	v_fma_f32 v148, v1, v148, v48
	v_fma_f32 v149, v1, v149, v49
	v_fma_f32 v138, v1, v138, v38
	v_fma_f32 v139, v1, v139, v39
	v_fma_f32 v140, v1, v140, v40
	v_fma_f32 v141, v1, v141, v41
	v_lshl_add_u32 v115, v156, 3, s0
	v_max_f32_e32 v146, 0, v146
	v_max_f32_e32 v147, 0, v147
	v_max_f32_e32 v148, 0, v148
	v_max_f32_e32 v149, 0, v149
	v_max_f32_e32 v138, 0, v138
	v_max_f32_e32 v139, 0, v139
	v_max_f32_e32 v140, 0, v140
	v_max_f32_e32 v141, 0, v141
	ds_read_b64 v[152:153], v114
	ds_read_b64 v[114:115], v115
	ds_read_b64 v[150:151], v168 offset:1408
	v_cvt_pk_f16_f32 v141, v140, v141
	v_cvt_pk_f16_f32 v140, v138, v139
	v_cvt_pk_f16_f32 v139, v148, v149
	v_cvt_pk_f16_f32 v138, v146, v147
	v_add_lshl_u32 v146, v166, v154, 1
	buffer_store_dwordx4 v[138:141], v146, s[8:11], 0 offen sc1
	v_fma_f32 v134, -v0, v22, v134
	v_fma_f32 v135, -v0, v23, v135
	v_fma_f32 v138, -v0, v30, v142
	v_fma_f32 v139, -v0, v31, v143
	v_fma_f32 v140, -v0, v32, v144
	v_fma_f32 v141, -v0, v33, v145
	v_fma_f32 v136, -v0, v24, v136
	v_fma_f32 v0, -v0, v25, v137
	v_fma_f32 v136, v1, v136, v20
	v_fma_f32 v0, v1, v0, v21
	v_fma_f32 v138, v1, v138, v26
	v_fma_f32 v139, v1, v139, v27
	v_fma_f32 v140, v1, v140, v28
	v_fma_f32 v141, v1, v141, v29
	v_fma_f32 v134, v1, v134, v18
	v_fma_f32 v135, v1, v135, v19
	v_max_f32_e32 v136, 0, v136
	v_max_f32_e32 v0, 0, v0
	s_waitcnt lgkmcnt(2)
	v_fma_f32 v1, -v152, v54, v130
	v_fma_f32 v130, -v152, v55, v131
	v_fma_f32 v131, -v152, v56, v132
	v_fma_f32 v132, -v152, v57, v133
	v_fma_f32 v122, -v152, v42, v122
	v_fma_f32 v123, -v152, v43, v123
	v_fma_f32 v124, -v152, v44, v124
	v_fma_f32 v125, -v152, v45, v125
	v_cvt_pk_f16_f32 v137, v136, v0
	v_add_u32_e32 v0, s12, v155
	v_fma_f32 v1, v153, v1, v46
	v_fma_f32 v130, v153, v130, v47
	v_fma_f32 v131, v153, v131, v48
	v_fma_f32 v132, v153, v132, v49
	v_fma_f32 v122, v153, v122, v38
	v_fma_f32 v123, v153, v123, v39
	v_fma_f32 v124, v153, v124, v40
	v_fma_f32 v125, v153, v125, v41
	v_max_f32_e32 v138, 0, v138
	v_max_f32_e32 v139, 0, v139
	v_max_f32_e32 v140, 0, v140
	v_max_f32_e32 v141, 0, v141
	v_max_f32_e32 v134, 0, v134
	v_max_f32_e32 v135, 0, v135
	v_mul_lo_u32 v0, v0, s6
	v_max_f32_e32 v1, 0, v1
	v_max_f32_e32 v130, 0, v130
	v_max_f32_e32 v131, 0, v131
	v_max_f32_e32 v132, 0, v132
	v_max_f32_e32 v122, 0, v122
	v_max_f32_e32 v123, 0, v123
	v_max_f32_e32 v124, 0, v124
	v_max_f32_e32 v125, 0, v125
	v_cvt_pk_f16_f32 v136, v134, v135
	v_cvt_pk_f16_f32 v135, v140, v141
	v_cvt_pk_f16_f32 v134, v138, v139
	v_cvt_pk_f16_f32 v125, v124, v125
	v_cvt_pk_f16_f32 v124, v122, v123
	v_cvt_pk_f16_f32 v123, v131, v132
	v_cvt_pk_f16_f32 v122, v1, v130
	v_add_lshl_u32 v0, v166, v0, 1
	buffer_store_dwordx4 v[134:137], v146, s[8:11], 0 offen offset:256 sc1
	s_and_saveexec_b64 s[24:25], vcc
	s_cbranch_execz .LBB8_8
	s_barrier
.LBB8_8:
	s_or_b64 exec, exec, s[24:25]
	buffer_store_dwordx4 v[122:125], v0, s[8:11], 0 offen sc1
	v_fma_f32 v1, -v152, v30, v126
	v_fma_f32 v118, -v152, v22, v118
	v_fma_f32 v122, -v152, v31, v127
	v_fma_f32 v123, -v152, v32, v128
	v_fma_f32 v124, -v152, v33, v129
	v_fma_f32 v119, -v152, v23, v119
	v_fma_f32 v120, -v152, v24, v120
	v_fma_f32 v121, -v152, v25, v121
	v_fma_f32 v1, v153, v1, v26
	v_fma_f32 v122, v153, v122, v27
	v_fma_f32 v123, v153, v123, v28
	v_fma_f32 v124, v153, v124, v29
	v_fma_f32 v118, v153, v118, v18
	v_fma_f32 v119, v153, v119, v19
	v_fma_f32 v120, v153, v120, v20
	v_fma_f32 v121, v153, v121, v21
	v_max_f32_e32 v1, 0, v1
	v_max_f32_e32 v122, 0, v122
	v_max_f32_e32 v123, 0, v123
	v_max_f32_e32 v124, 0, v124
	v_max_f32_e32 v118, 0, v118
	v_max_f32_e32 v119, 0, v119
	v_max_f32_e32 v120, 0, v120
	v_max_f32_e32 v121, 0, v121
	v_cvt_pk_f16_f32 v121, v120, v121
	v_cvt_pk_f16_f32 v120, v118, v119
	v_cvt_pk_f16_f32 v119, v123, v124
	v_cvt_pk_f16_f32 v118, v1, v122
	s_waitcnt lgkmcnt(1)
	v_fma_f32 v1, -v114, v54, v110
	v_fma_f32 v110, -v114, v55, v111
	v_fma_f32 v111, -v114, v56, v112
	v_fma_f32 v112, -v114, v57, v113
	v_fma_f32 v102, -v114, v42, v102
	v_fma_f32 v103, -v114, v43, v103
	v_fma_f32 v104, -v114, v44, v104
	v_fma_f32 v105, -v114, v45, v105
	buffer_store_dwordx4 v[118:121], v0, s[8:11], 0 offen offset:256 sc1
	v_add_u32_e32 v0, s12, v156
	v_fma_f32 v1, v115, v1, v46
	v_fma_f32 v110, v115, v110, v47
	v_fma_f32 v111, v115, v111, v48
	v_fma_f32 v112, v115, v112, v49
	v_fma_f32 v102, v115, v102, v38
	v_fma_f32 v103, v115, v103, v39
	v_fma_f32 v104, v115, v104, v40
	v_fma_f32 v105, v115, v105, v41
	v_mul_lo_u32 v0, v0, s6
	v_max_f32_e32 v1, 0, v1
	v_max_f32_e32 v110, 0, v110
	v_max_f32_e32 v111, 0, v111
	v_max_f32_e32 v112, 0, v112
	v_max_f32_e32 v102, 0, v102
	v_max_f32_e32 v103, 0, v103
	v_max_f32_e32 v104, 0, v104
	v_max_f32_e32 v105, 0, v105
	v_cvt_pk_f16_f32 v105, v104, v105
	v_cvt_pk_f16_f32 v104, v102, v103
	v_cvt_pk_f16_f32 v103, v111, v112
	v_cvt_pk_f16_f32 v102, v1, v110
	v_add_lshl_u32 v0, v166, v0, 1
	buffer_store_dwordx4 v[102:105], v0, s[8:11], 0 offen sc1
	v_fma_f32 v1, -v114, v30, v106
	v_fma_f32 v98, -v114, v22, v98
	v_fma_f32 v102, -v114, v31, v107
	v_fma_f32 v103, -v114, v32, v108
	v_fma_f32 v104, -v114, v33, v109
	v_fma_f32 v99, -v114, v23, v99
	v_fma_f32 v100, -v114, v24, v100
	v_fma_f32 v101, -v114, v25, v101
	v_fma_f32 v1, v115, v1, v26
	v_fma_f32 v102, v115, v102, v27
	v_fma_f32 v103, v115, v103, v28
	v_fma_f32 v104, v115, v104, v29
	v_fma_f32 v98, v115, v98, v18
	v_fma_f32 v99, v115, v99, v19
	v_fma_f32 v100, v115, v100, v20
	v_fma_f32 v101, v115, v101, v21
	v_max_f32_e32 v1, 0, v1
	v_max_f32_e32 v102, 0, v102
	v_max_f32_e32 v103, 0, v103
	v_max_f32_e32 v104, 0, v104
	v_max_f32_e32 v98, 0, v98
	v_max_f32_e32 v99, 0, v99
	v_max_f32_e32 v100, 0, v100
	v_max_f32_e32 v101, 0, v101
	v_cvt_pk_f16_f32 v101, v100, v101
	v_cvt_pk_f16_f32 v100, v98, v99
	v_cvt_pk_f16_f32 v99, v103, v104
	v_cvt_pk_f16_f32 v98, v1, v102
	v_fma_f32 v1, -v116, v54, v94
	v_fma_f32 v94, -v116, v55, v95
	v_fma_f32 v95, -v116, v56, v96
	v_fma_f32 v96, -v116, v57, v97
	v_fma_f32 v86, -v116, v42, v86
	v_fma_f32 v87, -v116, v43, v87
	v_fma_f32 v88, -v116, v44, v88
	v_fma_f32 v89, -v116, v45, v89
	buffer_store_dwordx4 v[98:101], v0, s[8:11], 0 offen offset:256 sc1
	v_add_u32_e32 v0, 0x80, v167
	v_fma_f32 v1, v117, v1, v46
	v_fma_f32 v94, v117, v94, v47
	v_fma_f32 v95, v117, v95, v48
	v_fma_f32 v96, v117, v96, v49
	v_fma_f32 v86, v117, v86, v38
	v_fma_f32 v87, v117, v87, v39
	v_fma_f32 v88, v117, v88, v40
	v_fma_f32 v89, v117, v89, v41
	v_mul_lo_u32 v0, v0, s6
	v_max_f32_e32 v1, 0, v1
	v_max_f32_e32 v94, 0, v94
	v_max_f32_e32 v95, 0, v95
	v_max_f32_e32 v96, 0, v96
	v_max_f32_e32 v86, 0, v86
	v_max_f32_e32 v87, 0, v87
	v_max_f32_e32 v88, 0, v88
	v_max_f32_e32 v89, 0, v89
	v_cvt_pk_f16_f32 v89, v88, v89
	v_cvt_pk_f16_f32 v88, v86, v87
	v_cvt_pk_f16_f32 v87, v95, v96
	v_cvt_pk_f16_f32 v86, v1, v94
	v_add_lshl_u32 v0, v166, v0, 1
	buffer_store_dwordx4 v[86:89], v0, s[8:11], 0 offen sc1
	v_fma_f32 v1, -v116, v30, v90
	v_fma_f32 v82, -v116, v22, v82
	v_fma_f32 v86, -v116, v31, v91
	v_fma_f32 v86, v117, v86, v27
	v_max_f32_e32 v90, 0, v86
	v_fma_f32 v86, -v116, v32, v92
	v_fma_f32 v87, -v116, v33, v93
	v_fma_f32 v83, -v116, v23, v83
	v_fma_f32 v84, -v116, v24, v84
	v_fma_f32 v85, -v116, v25, v85
	v_fma_f32 v86, v117, v86, v28
	v_fma_f32 v87, v117, v87, v29
	v_fma_f32 v82, v117, v82, v18
	v_fma_f32 v83, v117, v83, v19
	v_fma_f32 v84, v117, v84, v20
	v_fma_f32 v85, v117, v85, v21
	v_max_f32_e32 v86, 0, v86
	v_max_f32_e32 v87, 0, v87
	v_max_f32_e32 v82, 0, v82
	v_max_f32_e32 v83, 0, v83
	v_max_f32_e32 v84, 0, v84
	v_max_f32_e32 v85, 0, v85
	v_cvt_pk_f16_f32 v85, v84, v85
	v_cvt_pk_f16_f32 v84, v82, v83
	v_cvt_pk_f16_f32 v83, v86, v87
	ds_read2_b64 v[86:89], v168 offset0:144 offset1:160
	v_fma_f32 v1, v117, v1, v26
	v_max_f32_e32 v1, 0, v1
	v_cvt_pk_f16_f32 v82, v1, v90
	buffer_store_dwordx4 v[82:85], v0, s[8:11], 0 offen offset:256 sc1
	s_waitcnt lgkmcnt(0)
	v_fma_f32 v1, -v86, v54, v78
	v_fma_f32 v78, -v86, v55, v79
	v_fma_f32 v79, -v86, v56, v80
	v_fma_f32 v80, -v86, v57, v81
	v_fma_f32 v70, -v86, v42, v70
	v_fma_f32 v71, -v86, v43, v71
	v_fma_f32 v72, -v86, v44, v72
	v_fma_f32 v73, -v86, v45, v73
	v_add_u32_e32 v0, 0x90, v167
	v_fma_f32 v1, v87, v1, v46
	v_fma_f32 v78, v87, v78, v47
	v_fma_f32 v79, v87, v79, v48
	v_fma_f32 v80, v87, v80, v49
	v_fma_f32 v70, v87, v70, v38
	v_fma_f32 v71, v87, v71, v39
	v_fma_f32 v72, v87, v72, v40
	v_fma_f32 v73, v87, v73, v41
	v_mul_lo_u32 v0, v0, s6
	v_max_f32_e32 v1, 0, v1
	v_max_f32_e32 v78, 0, v78
	v_max_f32_e32 v79, 0, v79
	v_max_f32_e32 v80, 0, v80
	v_max_f32_e32 v70, 0, v70
	v_max_f32_e32 v71, 0, v71
	v_max_f32_e32 v72, 0, v72
	v_max_f32_e32 v73, 0, v73
	v_cvt_pk_f16_f32 v73, v72, v73
	v_cvt_pk_f16_f32 v72, v70, v71
	v_cvt_pk_f16_f32 v71, v79, v80
	v_cvt_pk_f16_f32 v70, v1, v78
	v_add_lshl_u32 v0, v166, v0, 1
	buffer_store_dwordx4 v[70:73], v0, s[8:11], 0 offen sc1
	v_fma_f32 v1, -v86, v30, v74
	v_fma_f32 v66, -v86, v22, v66
	v_fma_f32 v70, -v86, v31, v75
	v_fma_f32 v71, -v86, v32, v76
	v_fma_f32 v72, -v86, v33, v77
	v_fma_f32 v67, -v86, v23, v67
	v_fma_f32 v68, -v86, v24, v68
	v_fma_f32 v69, -v86, v25, v69
	v_fma_f32 v1, v87, v1, v26
	v_fma_f32 v70, v87, v70, v27
	v_fma_f32 v71, v87, v71, v28
	v_fma_f32 v72, v87, v72, v29
	v_fma_f32 v66, v87, v66, v18
	v_fma_f32 v67, v87, v67, v19
	v_fma_f32 v68, v87, v68, v20
	v_fma_f32 v69, v87, v69, v21
	v_max_f32_e32 v1, 0, v1
	v_max_f32_e32 v70, 0, v70
	v_max_f32_e32 v71, 0, v71
	v_max_f32_e32 v72, 0, v72
	v_max_f32_e32 v66, 0, v66
	v_max_f32_e32 v67, 0, v67
	v_max_f32_e32 v68, 0, v68
	v_max_f32_e32 v69, 0, v69
	v_cvt_pk_f16_f32 v69, v68, v69
	v_cvt_pk_f16_f32 v68, v66, v67
	v_cvt_pk_f16_f32 v67, v71, v72
	v_cvt_pk_f16_f32 v66, v1, v70
	v_fma_f32 v1, -v88, v54, v62
	v_fma_f32 v62, -v88, v55, v63
	v_fma_f32 v63, -v88, v56, v64
	v_fma_f32 v64, -v88, v57, v65
	v_fma_f32 v50, -v88, v42, v50
	v_fma_f32 v51, -v88, v43, v51
	v_fma_f32 v52, -v88, v44, v52
	v_fma_f32 v53, -v88, v45, v53
	buffer_store_dwordx4 v[66:69], v0, s[8:11], 0 offen offset:256 sc1
	v_add_u32_e32 v0, 0xa0, v167
	v_fma_f32 v1, v89, v1, v46
	v_fma_f32 v62, v89, v62, v47
	v_fma_f32 v63, v89, v63, v48
	v_fma_f32 v64, v89, v64, v49
	v_fma_f32 v50, v89, v50, v38
	v_fma_f32 v51, v89, v51, v39
	v_fma_f32 v52, v89, v52, v40
	v_fma_f32 v53, v89, v53, v41
	v_mul_lo_u32 v0, v0, s6
	v_max_f32_e32 v1, 0, v1
	v_max_f32_e32 v62, 0, v62
	v_max_f32_e32 v63, 0, v63
	v_max_f32_e32 v64, 0, v64
	v_max_f32_e32 v50, 0, v50
	v_max_f32_e32 v51, 0, v51
	v_max_f32_e32 v52, 0, v52
	v_max_f32_e32 v53, 0, v53
	v_cvt_pk_f16_f32 v53, v52, v53
	v_cvt_pk_f16_f32 v52, v50, v51
	v_cvt_pk_f16_f32 v51, v63, v64
	v_cvt_pk_f16_f32 v50, v1, v62
	v_add_lshl_u32 v0, v166, v0, 1
	buffer_store_dwordx4 v[50:53], v0, s[8:11], 0 offen sc1
	v_fma_f32 v1, -v88, v30, v58
	v_fma_f32 v34, -v88, v22, v34
	v_fma_f32 v50, -v88, v31, v59
	v_fma_f32 v35, -v88, v23, v35
	v_fma_f32 v36, -v88, v24, v36
	v_fma_f32 v37, -v88, v25, v37
	v_fma_f32 v1, v89, v1, v26
	v_fma_f32 v50, v89, v50, v27
	v_fma_f32 v34, v89, v34, v18
	v_fma_f32 v35, v89, v35, v19
	v_fma_f32 v36, v89, v36, v20
	v_fma_f32 v37, v89, v37, v21
	v_max_f32_e32 v1, 0, v1
	v_max_f32_e32 v50, 0, v50
	v_fma_f32 v51, -v88, v32, v60
	v_fma_f32 v52, -v88, v33, v61
	v_max_f32_e32 v34, 0, v34
	v_max_f32_e32 v35, 0, v35
	v_max_f32_e32 v36, 0, v36
	v_max_f32_e32 v37, 0, v37
	v_fma_f32 v51, v89, v51, v28
	v_fma_f32 v52, v89, v52, v29
	v_cvt_pk_f16_f32 v37, v36, v37
	v_cvt_pk_f16_f32 v36, v34, v35
	v_cvt_pk_f16_f32 v34, v1, v50
	v_fma_f32 v1, -v150, v54, v14
	v_fma_f32 v14, -v150, v55, v15
	v_fma_f32 v10, -v150, v42, v10
	v_fma_f32 v11, -v150, v43, v11
	v_fma_f32 v12, -v150, v44, v12
	v_fma_f32 v13, -v150, v45, v13
	v_max_f32_e32 v51, 0, v51
	v_max_f32_e32 v52, 0, v52
	v_fma_f32 v1, v151, v1, v46
	v_fma_f32 v14, v151, v14, v47
	v_fma_f32 v10, v151, v10, v38
	v_fma_f32 v11, v151, v11, v39
	v_fma_f32 v12, v151, v12, v40
	v_fmac_f32_e32 v41, v151, v13
	v_cvt_pk_f16_f32 v35, v51, v52
	v_max_f32_e32 v1, 0, v1
	v_max_f32_e32 v14, 0, v14
	v_max_f32_e32 v10, 0, v10
	v_max_f32_e32 v11, 0, v11
	v_max_f32_e32 v12, 0, v12
	v_max_f32_e32 v13, 0, v41
	buffer_store_dwordx4 v[34:37], v0, s[8:11], 0 offen offset:256 sc1
	v_add_u32_e32 v0, 0xb0, v167
	v_cvt_pk_f16_f32 v13, v12, v13
	v_cvt_pk_f16_f32 v12, v10, v11
	v_cvt_pk_f16_f32 v10, v1, v14
	v_fma_f32 v1, -v150, v31, v7
	v_fma_f32 v3, -v150, v23, v3
	v_mul_lo_u32 v0, v0, s6
	v_fma_f32 v1, v151, v1, v27
	v_fma_f32 v3, v151, v3, v19
	v_fma_f32 v15, -v150, v56, v16
	v_fma_f32 v16, -v150, v57, v17
	v_add_lshl_u32 v14, v166, v0, 1
	v_fma_f32 v0, -v150, v30, v6
	v_max_f32_e32 v6, 0, v1
	v_fma_f32 v1, -v150, v32, v8
	v_fma_f32 v7, -v150, v33, v9
	v_fma_f32 v2, -v150, v22, v2
	v_max_f32_e32 v8, 0, v3
	v_fma_f32 v3, -v150, v24, v4
	v_fma_f32 v4, -v150, v25, v5
	v_fma_f32 v15, v151, v15, v48
	v_fmac_f32_e32 v49, v151, v16
	v_fma_f32 v0, v151, v0, v26
	v_fma_f32 v1, v151, v1, v28
	v_fmac_f32_e32 v29, v151, v7
	v_fma_f32 v2, v151, v2, v18
	v_fma_f32 v3, v151, v3, v20
	v_fmac_f32_e32 v21, v151, v4
	v_max_f32_e32 v15, 0, v15
	v_max_f32_e32 v16, 0, v49
	v_max_f32_e32 v0, 0, v0
	v_max_f32_e32 v1, 0, v1
	v_max_f32_e32 v7, 0, v29
	v_max_f32_e32 v2, 0, v2
	v_max_f32_e32 v3, 0, v3
	v_max_f32_e32 v4, 0, v21
	v_cvt_pk_f16_f32 v11, v15, v16
	v_cvt_pk_f16_f32 v3, v3, v4
	v_cvt_pk_f16_f32 v2, v2, v8
	v_cvt_pk_f16_f32 v1, v1, v7
	v_cvt_pk_f16_f32 v0, v0, v6
	buffer_store_dwordx4 v[10:13], v14, s[8:11], 0 offen sc1
	buffer_store_dwordx4 v[0:3], v14, s[8:11], 0 offen offset:256 sc1
	s_endpgm
